# v28: conv/SiLU phase: fold sigmoid -log2e and x4 scale into taps/biases (f32, algebraically identical), drop redundant zero-init before fp8 pack; -440 VALU per 32 rows
# speedup vs baseline: 1.0020x; 1.0020x over previous
; #define GAS __attribute__((address_space(1)))
; __device__ __forceinline__ void conv_phase(Frame& F) {
;     constexpr int C8 = DFF / 8, TB = 32, NTB = M / TB;
;     const size_t total = (size_t)C8 * NTB;
;     for (size_t idx = (size_t)F.gw * 64 + F.lane; idx < total; idx += (size_t)F.NGW * 64) {
;         const int c8 = (int)(idx % C8), tb = (int)(idx / C8), ch = 8 * c8, t0 = tb * TB;
;         const int acol = (ch >> 7) * 256 + (ch & 127);
;         f32x2 wg[3][4], wv[3][4], bg[4], bv[4];
; #pragma unroll
;         for (int j = 0; j < 3; ++j) { const f32x4 a = *(const GAS f32x4*)(F.cvw + (size_t)j * F2 + ch) * (1.f / S_A), b = *(const GAS f32x4*)(F.cvw + (size_t)j * F2 + ch + 4) * (1.f / S_A);
;             const f32x4 c = *(const GAS f32x4*)(F.cvw + (size_t)j * F2 + DFF + ch) * (1.f / S_A), d = *(const GAS f32x4*)(F.cvw + (size_t)j * F2 + DFF + ch + 4) * (1.f / S_A);
;             wg[j][0] = (f32x2){a.x, a.y}; wg[j][1] = (f32x2){a.z, a.w}; wg[j][2] = (f32x2){b.x, b.y}; wg[j][3] = (f32x2){b.z, b.w};
;             wv[j][0] = (f32x2){c.x, c.y}; wv[j][1] = (f32x2){c.z, c.w}; wv[j][2] = (f32x2){d.x, d.y}; wv[j][3] = (f32x2){d.z, d.w}; }
;         { const f32x4 a = *(const GAS f32x4*)(F.cvb + ch), b = *(const GAS f32x4*)(F.cvb + ch + 4), c = *(const GAS f32x4*)(F.cvb + DFF + ch), d = *(const GAS f32x4*)(F.cvb + DFF + ch + 4);
;           bg[0] = (f32x2){a.x, a.y}; bg[1] = (f32x2){a.z, a.w}; bg[2] = (f32x2){b.x, b.y}; bg[3] = (f32x2){b.z, b.w}; bv[0] = (f32x2){c.x, c.y}; bv[1] = (f32x2){c.z, c.w}; bv[2] = (f32x2){d.x, d.y}; bv[3] = (f32x2){d.z, d.w}; }
;         f32x2 g1[4], g2[4], v1[4], v2[4];
;         const bool first = (t0 & (SEQ - 1)) == 0;
;         const unsigned char* ap = (const unsigned char*)F.A + (size_t)t0 * F2 + acol;
;         if (first) {
; #pragma unroll
;             for (int e = 0; e < 4; ++e) { g1[e] = g2[e] = v1[e] = v2[e] = (f32x2){0.f, 0.f}; }
;         } else {
;             const v2u ga = *(const GAS v2u*)(ap - F2), gb = *(const GAS v2u*)(ap - 2 * (size_t)F2), va = *(const GAS v2u*)(ap - F2 + 128), vb = *(const GAS v2u*)(ap - 2 * (size_t)F2 + 128);
;             unpack8_fp8(ga, g1); unpack8_fp8(gb, g2); unpack8_fp8(va, v1); unpack8_fp8(vb, v2);
;         }
;         v2u GA[8], VA[8], GB[8], VB[8];
.LBB0_2565:
	v_readlane_b32 s2, v249, 13
	v_readlane_b32 s3, v249, 14
	s_cmp_lt_i32 s2, 11
	v_readlane_b32 s4, v249, 11
	s_cselect_b64 s[2:3], -1, 0
	v_readlane_b32 s5, v249, 12
	s_add_u32 s4, s4, 0x3e600000
	s_addc_u32 s5, s5, 0
	s_and_b64 s[0:1], s[2:3], s[0:1]
	s_andn2_b64 vcc, exec, s[0:1]
	s_cbranch_vccnz .LBB0_2572
	v_readlane_b32 s2, v249, 38
	v_readlane_b32 s3, v249, 39
	s_ashr_i32 s3, s2, 31
	s_lshl_b64 s[2:3], s[2:3], 6
	s_waitcnt vmcnt(0)
	v_mov_b64_e32 v[2:3], 0x55fff
	v_cmp_gt_u64_e32 vcc, s[2:3], v[2:3]
	s_cbranch_vccnz .LBB0_2572
	v_readlane_b32 s8, v249, 0
	v_readlane_b32 s10, v249, 2
	v_readlane_b32 s11, v249, 3
	v_readlane_b32 s12, v249, 4
	v_readlane_b32 s13, v249, 5
	v_readlane_b32 s14, v249, 6
	v_readlane_b32 s15, v249, 7
	v_readlane_b32 s9, v249, 1
	s_mov_b64 s[14:15], s[10:11]
	s_mov_b64 s[12:13], s[8:9]
	v_or_b32_e32 v66, s2, v180
	s_add_u32 s2, s12, 0xac00
	v_mov_b32_e32 v67, s3
	s_addc_u32 s3, s13, 0
	s_add_u32 s6, s12, 0x15800
	s_addc_u32 s7, s13, 0
	s_add_u32 s8, s12, 0x20400
	s_addc_u32 s9, s13, 0
	s_add_u32 s10, s12, 0x2b000
	s_addc_u32 s11, s13, 0
	s_add_u32 s12, s12, 0x35c00
	s_addc_u32 s13, s13, 0
	v_readlane_b32 s16, v249, 46
	s_add_u32 s14, s14, 0xac00
	v_readlane_b32 s17, v249, 47
	s_addc_u32 s15, s15, 0
	s_ashr_i32 s17, s16, 31
	s_lshl_b64 s[18:19], s[16:17], 6
	s_mov_b64 s[16:17], 0
	s_mov_b32 s21, 0x2fa0be83
	v_mov_b32_e32 v69, 0
	s_movk_i32 s24, 0x7f00
	s_mov_b32 s44, 0xbdb8aa3b
	s_mov_b32 s80, 0xbe317218
	s_mov_b32 s82, 0xbfb8aa3b
	s_mov_b32 s94, 0xc0317218
	s_mov_b32 s20, 0x3d800000
	s_movk_i32 s25, 0x5000
	s_mov_b32 s26, 0xa000
	s_mov_b32 s27, 0x10000
	s_mov_b32 s28, 0x15000
	s_mov_b32 s29, 0x1a000
	s_mov_b32 s30, 0x20000
	s_mov_b32 s31, 0x25000
	s_mov_b32 s33, 0x2b000
	s_mov_b32 s34, 0x30000
	s_mov_b32 s35, 0x35000
	s_mov_b32 s36, 0x3b000
	s_mov_b32 s37, 0x40000
	s_mov_b32 s38, 0x45000
	s_mov_b32 s39, 0x4b000
	s_mov_b32 s40, 0x50000
	s_mov_b32 s41, 0xc3e00000
	s_mov_b32 s42, 0x56000
	s_movk_i32 s43, 0x2000
	s_mov_b32 s46, 0x8000
	s_mov_b32 s47, 0xd000
	s_mov_b32 s48, 0x12000
	s_mov_b32 s49, 0x5b000
	s_mov_b32 s50, 0x60000
	s_mov_b32 s51, 0x66000
	s_mov_b32 s52, 0x6b000
	s_mov_b32 s53, 0x70000
	s_mov_b32 s54, 0x76000
	s_mov_b32 s55, 0x7b000
	s_mov_b32 s56, 0x18000
	s_mov_b32 s57, 0x1d000
	s_mov_b32 s58, 0x22000
	s_mov_b32 s59, 0x28000
	s_mov_b32 s60, 0x81000
	s_mov_b32 s61, 0x86000
	s_mov_b32 s62, 0x8b000
	s_mov_b32 s63, 0x91000
	s_mov_b32 s64, 0x96000
	s_mov_b32 s65, 0x9b000
	s_mov_b32 s66, 0xa1000
	s_mov_b32 s67, 0xa6000
	s_mov_b32 s68, 0x2d000
	s_mov_b32 s69, 0x33000
	s_mov_b32 s70, 0x38000
	s_mov_b32 s71, 0x3d000
	s_mov_b32 s72, 0x43000
	s_mov_b32 s73, 0x48000
	s_mov_b32 s74, 0x4d000
	v_mov_b32_e32 v1, 0x43e00000
	s_branch .LBB0_2569
.LBB0_2568:
	s_or_b64 exec, exec, s[22:23]
	v_add_co_u32_e32 v74, vcc, s25, v72
	s_waitcnt vmcnt(14)
	v_pk_mul_f32 v[62:63], v[62:63], s[44:45] op_sel_hi:[1,0]
	v_addc_co_u32_e32 v75, vcc, 0, v73, vcc
	global_load_dwordx2 v[160:161], v[72:73], off nt
	global_load_dwordx2 v[176:177], v[72:73], off offset:128 nt
	global_load_dwordx2 v[182:183], v[74:75], off offset:1536 nt
	global_load_dwordx2 v[170:171], v[74:75], off offset:1664 nt
	v_add_co_u32_e32 v74, vcc, s26, v72
	s_waitcnt vmcnt(14)
	v_pk_mul_f32 v[50:51], v[50:51], s[44:45] op_sel_hi:[1,0]
	v_addc_co_u32_e32 v75, vcc, 0, v73, vcc
	v_add_co_u32_e32 v76, vcc, s27, v72
	s_waitcnt vmcnt(6)
	v_pk_mul_f32 v[14:15], v[14:15], s[82:83] op_sel_hi:[1,0]
	v_pk_fma_f32 v[152:153], v[62:63], v[152:153], v[14:15]
	v_addc_co_u32_e32 v77, vcc, 0, v73, vcc
	global_load_dwordx2 v[156:157], v[74:75], off offset:3072 nt
	global_load_dwordx2 v[154:155], v[74:75], off offset:3200 nt
	global_load_dwordx2 v[140:141], v[76:77], off offset:512 nt
	global_load_dwordx2 v[138:139], v[76:77], off offset:640 nt
	v_add_co_u32_e32 v74, vcc, s28, v72
	v_pk_mul_f32 v[34:35], v[34:35], s[44:45] op_sel_hi:[1,0]
	s_nop 0
	v_addc_co_u32_e32 v75, vcc, 0, v73, vcc
	v_add_co_u32_e32 v76, vcc, s29, v72
	v_pk_fma_f32 v[152:153], v[50:51], v[132:133], v[152:153]
	s_nop 0
	v_addc_co_u32_e32 v77, vcc, 0, v73, vcc
	global_load_dwordx2 v[104:105], v[74:75], off offset:2048 nt
	global_load_dwordx2 v[100:101], v[74:75], off offset:2176 nt
	global_load_dwordx2 v[96:97], v[76:77], off offset:3584 nt
	global_load_dwordx2 v[92:93], v[76:77], off offset:3712 nt
	v_add_co_u32_e32 v74, vcc, s30, v72
	v_pk_mul_f32 v[64:65], v[64:65], s[44:45] op_sel_hi:[1,0]
	s_nop 0
	v_addc_co_u32_e32 v75, vcc, 0, v73, vcc
	v_add_co_u32_e32 v76, vcc, s31, v72
	v_pk_mul_f32 v[52:53], v[52:53], s[44:45] op_sel_hi:[1,0]
	s_nop 0
	v_addc_co_u32_e32 v77, vcc, 0, v73, vcc
	global_load_dwordx2 v[88:89], v[74:75], off offset:1024 nt
	global_load_dwordx2 v[84:85], v[74:75], off offset:1152 nt
	global_load_dwordx2 v[80:81], v[76:77], off offset:2560 nt
	s_nop 0
	global_load_dwordx2 v[76:77], v[76:77], off offset:2688 nt
	v_add_co_u32_e32 v74, vcc, s33, v72
	v_pk_mul_f32 v[16:17], v[16:17], s[82:83] op_sel_hi:[1,0]
	v_pk_fma_f32 v[148:149], v[64:65], v[148:149], v[16:17]
	s_nop 0
	v_addc_co_u32_e32 v75, vcc, 0, v73, vcc
	v_add_co_u32_e32 v78, vcc, s34, v72
	v_pk_mul_f32 v[36:37], v[36:37], s[44:45] op_sel_hi:[1,0]
	s_nop 0
	v_addc_co_u32_e32 v79, vcc, 0, v73, vcc
	global_load_dwordx2 v[134:135], v[74:75], off nt
	global_load_dwordx2 v[130:131], v[74:75], off offset:128 nt
	global_load_dwordx2 v[126:127], v[78:79], off offset:1536 nt
	global_load_dwordx2 v[122:123], v[78:79], off offset:1664 nt
	v_add_co_u32_e32 v74, vcc, s35, v72
	v_pk_fma_f32 v[148:149], v[52:53], v[124:125], v[148:149]
	s_nop 0
	v_addc_co_u32_e32 v75, vcc, 0, v73, vcc
	v_add_co_u32_e32 v78, vcc, s36, v72
	v_pk_mul_f32 v[58:59], v[58:59], s[80:81] op_sel_hi:[1,0]
	s_nop 0
	v_addc_co_u32_e32 v79, vcc, 0, v73, vcc
	global_load_dwordx2 v[118:119], v[74:75], off offset:3072 nt
	global_load_dwordx2 v[114:115], v[74:75], off offset:3200 nt
	global_load_dwordx2 v[110:111], v[78:79], off offset:512 nt
	global_load_dwordx2 v[106:107], v[78:79], off offset:640 nt
	v_add_co_u32_e32 v74, vcc, s37, v72
	v_pk_mul_f32 v[42:43], v[42:43], s[80:81] op_sel_hi:[1,0]
	s_nop 0
	v_addc_co_u32_e32 v75, vcc, 0, v73, vcc
	v_add_co_u32_e32 v78, vcc, s38, v72
	s_waitcnt vmcnt(24)
; #define GAS __attribute__((address_space(1)))
; __device__ __forceinline__ float sigmoidf_(float x) { return __builtin_amdgcn_rcpf(1.0f + __builtin_amdgcn_exp2f(-1.4426950408889634f * x)); }
; __device__ __forceinline__ void conv_phase(Frame& F) {
;     ...
;         for (int j = 0; j < 3; ++j) { const f32x4 a = *(const GAS f32x4*)(F.cvw + (size_t)j * F2 + ch) * (1.f / S_A), b = *(const GAS f32x4*)(F.cvw + (size_t)j * F2 + ch + 4) * (1.f / S_A);
;             const f32x4 c = *(const GAS f32x4*)(F.cvw + (size_t)j * F2 + DFF + ch) * (1.f / S_A), d = *(const GAS f32x4*)(F.cvw + (size_t)j * F2 + DFF + ch + 4) * (1.f / S_A);
;             wg[j][0] = (f32x2){a.x, a.y}; wg[j][1] = (f32x2){a.z, a.w}; wg[j][2] = (f32x2){b.x, b.y}; wg[j][3] = (f32x2){b.z, b.w};
;             wv[j][0] = (f32x2){c.x, c.y}; wv[j][1] = (f32x2){c.z, c.w}; wv[j][2] = (f32x2){d.x, d.y}; wv[j][3] = (f32x2){d.z, d.w}; }
;         { const f32x4 a = *(const GAS f32x4*)(F.cvb + ch), b = *(const GAS f32x4*)(F.cvb + ch + 4), c = *(const GAS f32x4*)(F.cvb + DFF + ch), d = *(const GAS f32x4*)(F.cvb + DFF + ch + 4);
;           bg[0] = (f32x2){a.x, a.y}; bg[1] = (f32x2){a.z, a.w}; bg[2] = (f32x2){b.x, b.y}; bg[3] = (f32x2){b.z, b.w}; bv[0] = (f32x2){c.x, c.y}; bv[1] = (f32x2){c.z, c.w}; bv[2] = (f32x2){d.x, d.y}; bv[3] = (f32x2){d.z, d.w}; }
;         f32x2 g1[4], g2[4], v1[4], v2[4];
;         const bool first = (t0 & (SEQ - 1)) == 0;
;         const unsigned char* ap = (const unsigned char*)F.A + (size_t)t0 * F2 + acol;
;         if (first) {
; #pragma unroll
;             for (int e = 0; e < 4; ++e) { g1[e] = g2[e] = v1[e] = v2[e] = (f32x2){0.f, 0.f}; }
;         } else {
;             const v2u ga = *(const GAS v2u*)(ap - F2), gb = *(const GAS v2u*)(ap - 2 * (size_t)F2), va = *(const GAS v2u*)(ap - F2 + 128), vb = *(const GAS v2u*)(ap - 2 * (size_t)F2 + 128);
;             unpack8_fp8(ga, g1); unpack8_fp8(gb, g2); unpack8_fp8(va, v1); unpack8_fp8(vb, v2);
;         }
;         v2u GA[8], VA[8], GB[8], VB[8];
	v_pk_mul_f32 v[10:11], v[10:11], s[94:95] op_sel_hi:[1,0]
	v_pk_fma_f32 v[158:159], v[58:59], v[158:159], v[10:11]
	v_addc_co_u32_e32 v79, vcc, 0, v73, vcc
	global_load_dwordx2 v[102:103], v[74:75], off offset:2048 nt
	global_load_dwordx2 v[98:99], v[74:75], off offset:2176 nt
	global_load_dwordx2 v[94:95], v[78:79], off offset:3584 nt
	global_load_dwordx2 v[90:91], v[78:79], off offset:3712 nt
	v_add_co_u32_e32 v74, vcc, s39, v72
	v_pk_mul_f32 v[26:27], v[26:27], s[80:81] op_sel_hi:[1,0]
	s_nop 0
	v_addc_co_u32_e32 v75, vcc, 0, v73, vcc
	v_add_co_u32_e32 v162, vcc, s40, v72
	v_pk_fma_f32 v[158:159], v[42:43], v[136:137], v[158:159]
	s_nop 0
	v_addc_co_u32_e32 v163, vcc, 0, v73, vcc
	s_waitcnt vmcnt(27)
	v_cvt_pk_f32_fp8_e32 v[178:179], v160
	v_cvt_pk_f32_fp8_sdwa v[168:169], v160 src0_sel:WORD_1
	s_waitcnt vmcnt(26)
	v_cvt_pk_f32_fp8_e32 v[172:173], v176
	v_cvt_pk_f32_fp8_sdwa v[166:167], v176 src0_sel:WORD_1
	v_pk_fma_f32 v[180:181], v[34:35], v[178:179], v[152:153]
	global_load_dwordx2 v[86:87], v[74:75], off offset:1024 nt
	global_load_dwordx2 v[82:83], v[74:75], off offset:1152 nt
	global_load_dwordx2 v[78:79], v[162:163], off offset:2560 nt
	s_nop 0
	global_load_dwordx2 v[74:75], v[162:163], off offset:2688 nt
	v_exp_f32_e32 v175, v180
	v_exp_f32_e32 v184, v181
	v_cvt_pk_f32_fp8_e32 v[162:163], v177
	v_add_f32_e32 v175, 1.0, v175
	v_rcp_f32_e32 v176, v175
	v_add_f32_e32 v175, 1.0, v184
	v_cvt_pk_f32_fp8_sdwa v[152:153], v177 src0_sel:WORD_1
	v_rcp_f32_e32 v177, v175
	v_pk_fma_f32 v[148:149], v[36:37], v[168:169], v[148:149]
	v_pk_fma_f32 v[158:159], v[26:27], v[172:173], v[158:159]
	v_pk_mul_f32 v[176:177], v[180:181], v[176:177]
	v_exp_f32_e32 v175, v148
	v_exp_f32_e32 v180, v149
	v_add_f32_e32 v175, 1.0, v175
	v_cvt_pk_f32_fp8_e32 v[164:165], v161
	v_pk_mul_f32 v[158:159], v[158:159], v[176:177]
	v_rcp_f32_e32 v176, v175
	v_add_f32_e32 v175, 1.0, v180
	v_pk_mul_f32 v[54:55], v[54:55], s[44:45] op_sel_hi:[1,0]
	v_rcp_f32_e32 v177, v175
	v_pk_mul_f32 v[38:39], v[38:39], s[44:45] op_sel_hi:[1,0]
	v_pk_mul_f32 v[6:7], v[6:7], s[82:83] op_sel_hi:[1,0]
	v_pk_fma_f32 v[144:145], v[54:55], v[144:145], v[6:7]
	v_pk_mul_f32 v[22:23], v[22:23], s[44:45] op_sel_hi:[1,0]
	v_pk_fma_f32 v[144:145], v[38:39], v[116:117], v[144:145]
	v_pk_mul_f32 v[60:61], v[60:61], s[80:81] op_sel_hi:[1,0]
	v_pk_fma_f32 v[144:145], v[22:23], v[164:165], v[144:145]
	v_pk_mul_f32 v[148:149], v[148:149], v[176:177]
	v_pk_mul_f32 v[44:45], v[44:45], s[80:81] op_sel_hi:[1,0]
	v_pk_mul_f32 v[12:13], v[12:13], s[94:95] op_sel_hi:[1,0]
	v_pk_fma_f32 v[150:151], v[60:61], v[150:151], v[12:13]
	v_exp_f32_e32 v175, v144
	v_exp_f32_e32 v176, v145
	v_pk_mul_f32 v[28:29], v[28:29], s[80:81] op_sel_hi:[1,0]
	v_pk_fma_f32 v[150:151], v[44:45], v[128:129], v[150:151]
	v_cvt_pk_f32_fp8_sdwa v[160:161], v161 src0_sel:WORD_1
	v_pk_fma_f32 v[150:151], v[28:29], v[166:167], v[150:151]
	v_pk_mul_f32 v[56:57], v[56:57], s[44:45] op_sel_hi:[1,0]
	v_pk_mul_f32 v[40:41], v[40:41], s[44:45] op_sel_hi:[1,0]
	v_pk_mul_f32 v[148:149], v[150:151], v[148:149]
	v_add_f32_e32 v150, 1.0, v175
	v_add_f32_e32 v151, 1.0, v176
	v_rcp_f32_e32 v150, v150
	v_rcp_f32_e32 v151, v151
	v_pk_mul_f32 v[8:9], v[8:9], s[82:83] op_sel_hi:[1,0]
	v_pk_fma_f32 v[70:71], v[56:57], v[70:71], v[8:9]
	v_pk_mul_f32 v[24:25], v[24:25], s[44:45] op_sel_hi:[1,0]
	v_pk_fma_f32 v[70:71], v[40:41], v[108:109], v[70:71]
	v_pk_mul_f32 v[46:47], v[46:47], s[80:81] op_sel_hi:[1,0]
	v_pk_fma_f32 v[70:71], v[24:25], v[160:161], v[70:71]
	v_pk_mul_f32 v[144:145], v[144:145], v[150:151]
	v_pk_mul_f32 v[30:31], v[30:31], s[80:81] op_sel_hi:[1,0]
	v_pk_mul_f32 v[2:3], v[2:3], s[94:95] op_sel_hi:[1,0]
	v_pk_fma_f32 v[146:147], v[46:47], v[146:147], v[2:3]
	v_exp_f32_e32 v150, v70
	v_exp_f32_e32 v151, v71
	v_pk_mul_f32 v[18:19], v[18:19], s[80:81] op_sel_hi:[1,0]
	v_pk_fma_f32 v[146:147], v[30:31], v[120:121], v[146:147]
	v_pk_mul_f32 v[48:49], v[48:49], s[80:81] op_sel_hi:[1,0]
	v_pk_fma_f32 v[146:147], v[18:19], v[162:163], v[146:147]
	v_pk_mul_f32 v[32:33], v[32:33], s[80:81] op_sel_hi:[1,0]
	v_pk_mul_f32 v[4:5], v[4:5], s[94:95] op_sel_hi:[1,0]
	v_pk_fma_f32 v[142:143], v[48:49], v[142:143], v[4:5]
	v_pk_mul_f32 v[144:145], v[146:147], v[144:145]
	v_add_f32_e32 v146, 1.0, v150
	v_add_f32_e32 v147, 1.0, v151
	v_rcp_f32_e32 v146, v146
	v_rcp_f32_e32 v147, v147
	v_pk_mul_f32 v[20:21], v[20:21], s[80:81] op_sel_hi:[1,0]
	v_pk_fma_f32 v[142:143], v[32:33], v[112:113], v[142:143]
	v_med3_f32 v144, v144, s41, v1
	v_pk_fma_f32 v[142:143], v[20:21], v[152:153], v[142:143]
	v_pk_mul_f32 v[70:71], v[70:71], v[146:147]
	v_med3_f32 v146, v159, s41, v1
	v_pk_mul_f32 v[70:71], v[142:143], v[70:71]
	v_med3_f32 v143, v158, s41, v1
	v_cvt_pk_fp8_f32 v142, v143, v146
	v_med3_f32 v145, v145, s41, v1
	v_cvt_pk_fp8_f32 v143, v144, v145
	s_waitcnt vmcnt(29)
	v_cvt_pk_f32_fp8_e32 v[180:181], v182
	v_med3_f32 v70, v70, s41, v1
	v_med3_f32 v71, v71, s41, v1
	v_pk_fma_f32 v[132:133], v[62:63], v[132:133], v[14:15]
	v_cvt_pk_fp8_f32 v143, v70, v71 op_sel:[0,0,1]
	v_mul_u32_u24_e32 v70, 0x56000, v174
	v_mov_b32_e32 v71, v69
	v_pk_fma_f32 v[132:133], v[50:51], v[178:179], v[132:133]
	v_med3_f32 v146, v148, s41, v1
	v_med3_f32 v147, v149, s41, v1
	v_lshl_add_u64 v[70:71], s[4:5], 0, v[70:71]
	v_pk_fma_f32 v[148:149], v[34:35], v[180:181], v[132:133]
	v_lshl_add_u64 v[70:71], v[70:71], 0, v[68:69]
	v_exp_f32_e32 v68, v148
	v_exp_f32_e32 v176, v149
	v_cvt_pk_f32_fp8_sdwa v[158:159], v182 src0_sel:WORD_1
	v_add_f32_e32 v68, 1.0, v68
	s_waitcnt vmcnt(28)
; __device__ __forceinline__ float sigmoidf_(float x) { return __builtin_amdgcn_rcpf(1.0f + __builtin_amdgcn_exp2f(-1.4426950408889634f * x)); }
	v_cvt_pk_f32_fp8_e32 v[174:175], v170
	v_cvt_pk_f32_fp8_sdwa v[150:151], v170 src0_sel:WORD_1
	v_rcp_f32_e32 v170, v68
	v_add_f32_e32 v68, 1.0, v176
	v_cvt_pk_f32_fp8_e32 v[144:145], v171
	v_cvt_pk_f32_fp8_sdwa v[132:133], v171 src0_sel:WORD_1
	v_rcp_f32_e32 v171, v68
	v_pk_fma_f32 v[124:125], v[64:65], v[124:125], v[16:17]
	v_pk_fma_f32 v[136:137], v[58:59], v[136:137], v[10:11]
	v_pk_fma_f32 v[124:125], v[52:53], v[168:169], v[124:125]
	v_pk_mul_f32 v[148:149], v[148:149], v[170:171]
	v_pk_fma_f32 v[124:125], v[36:37], v[158:159], v[124:125]
	v_pk_fma_f32 v[136:137], v[42:43], v[172:173], v[136:137]
	v_exp_f32_e32 v68, v124
	v_exp_f32_e32 v170, v125
	v_pk_fma_f32 v[136:137], v[26:27], v[174:175], v[136:137]
	v_cvt_pk_fp8_f32 v142, v146, v147 op_sel:[0,0,1]
	v_cvt_pk_f32_fp8_e32 v[146:147], v183
	v_add_f32_e32 v68, 1.0, v68
	v_pk_mul_f32 v[136:137], v[136:137], v[148:149]
	v_rcp_f32_e32 v148, v68
	v_add_f32_e32 v68, 1.0, v170
	v_rcp_f32_e32 v149, v68
	v_pk_fma_f32 v[116:117], v[54:55], v[116:117], v[6:7]
	v_pk_fma_f32 v[128:129], v[60:61], v[128:129], v[12:13]
	v_pk_fma_f32 v[116:117], v[38:39], v[164:165], v[116:117]
	v_pk_mul_f32 v[124:125], v[124:125], v[148:149]
	v_pk_fma_f32 v[116:117], v[22:23], v[146:147], v[116:117]
	v_pk_fma_f32 v[128:129], v[44:45], v[166:167], v[128:129]
	v_exp_f32_e32 v68, v116
	v_exp_f32_e32 v148, v117
	v_pk_fma_f32 v[128:129], v[28:29], v[150:151], v[128:129]
	global_store_dwordx2 v[70:71], v[142:143], off
	v_cvt_pk_f32_fp8_sdwa v[142:143], v183 src0_sel:WORD_1
	v_add_f32_e32 v68, 1.0, v68
	v_pk_mul_f32 v[124:125], v[128:129], v[124:125]
	v_rcp_f32_e32 v128, v68
	v_add_f32_e32 v68, 1.0, v148
	v_rcp_f32_e32 v129, v68
	v_pk_fma_f32 v[108:109], v[56:57], v[108:109], v[8:9]
	v_pk_fma_f32 v[120:121], v[46:47], v[120:121], v[2:3]
	v_pk_fma_f32 v[108:109], v[40:41], v[160:161], v[108:109]
	v_pk_mul_f32 v[116:117], v[116:117], v[128:129]
	v_pk_fma_f32 v[108:109], v[24:25], v[142:143], v[108:109]
	v_pk_fma_f32 v[120:121], v[30:31], v[162:163], v[120:121]
	v_exp_f32_e32 v68, v108
	v_exp_f32_e32 v128, v109
	v_pk_fma_f32 v[120:121], v[18:19], v[144:145], v[120:121]
	v_add_f32_e32 v68, 1.0, v68
	v_pk_fma_f32 v[112:113], v[48:49], v[112:113], v[4:5]
	v_pk_mul_f32 v[116:117], v[120:121], v[116:117]
	v_rcp_f32_e32 v120, v68
	v_add_f32_e32 v68, 1.0, v128
	v_rcp_f32_e32 v121, v68
	v_pk_fma_f32 v[112:113], v[32:33], v[152:153], v[112:113]
	v_med3_f32 v68, v136, s41, v1
	v_pk_fma_f32 v[112:113], v[20:21], v[132:133], v[112:113]
	v_pk_mul_f32 v[108:109], v[108:109], v[120:121]
	v_med3_f32 v116, v116, s41, v1
	v_pk_mul_f32 v[108:109], v[112:113], v[108:109]
	v_med3_f32 v113, v137, s41, v1
	v_cvt_pk_fp8_f32 v112, v68, v113
	v_med3_f32 v117, v117, s41, v1
	v_cvt_pk_fp8_f32 v113, v116, v117
	v_med3_f32 v68, v124, s41, v1
	v_med3_f32 v120, v125, s41, v1
	v_cvt_pk_fp8_f32 v112, v68, v120 op_sel:[0,0,1]
	v_med3_f32 v68, v108, s41, v1
	v_med3_f32 v108, v109, s41, v1
	v_cvt_pk_fp8_f32 v113, v68, v108 op_sel:[0,0,1]
	v_add_co_u32_e32 v108, vcc, s43, v70
	s_waitcnt vmcnt(28)
	v_cvt_pk_f32_fp8_e32 v[182:183], v156
	v_addc_co_u32_e32 v109, vcc, 0, v71, vcc
	global_store_dwordx2 v[108:109], v[112:113], off offset:2816
	v_pk_fma_f32 v[112:113], v[62:63], v[178:179], v[14:15]
	s_waitcnt vmcnt(28)
	v_cvt_pk_f32_fp8_e32 v[176:177], v154
	v_pk_fma_f32 v[112:113], v[50:51], v[180:181], v[112:113]
	v_pk_fma_f32 v[128:129], v[58:59], v[172:173], v[10:11]
	v_pk_fma_f32 v[112:113], v[34:35], v[182:183], v[112:113]
	v_cvt_pk_f32_fp8_sdwa v[170:171], v156 src0_sel:WORD_1
	v_exp_f32_e32 v68, v112
	v_exp_f32_e32 v121, v113
	v_pk_fma_f32 v[128:129], v[42:43], v[174:175], v[128:129]
	v_add_f32_e32 v68, 1.0, v68
	v_rcp_f32_e32 v120, v68
	v_add_f32_e32 v68, 1.0, v121
	v_rcp_f32_e32 v121, v68
	v_pk_fma_f32 v[128:129], v[26:27], v[176:177], v[128:129]
	v_cvt_pk_f32_fp8_e32 v[136:137], v157
	v_cvt_pk_f32_fp8_sdwa v[108:109], v157 src0_sel:WORD_1
	v_pk_mul_f32 v[112:113], v[112:113], v[120:121]
	v_pk_mul_f32 v[112:113], v[128:129], v[112:113]
	v_pk_fma_f32 v[128:129], v[64:65], v[168:169], v[16:17]
	v_cvt_pk_f32_fp8_sdwa v[156:157], v154 src0_sel:WORD_1
	v_pk_fma_f32 v[128:129], v[52:53], v[158:159], v[128:129]
	v_pk_fma_f32 v[128:129], v[36:37], v[170:171], v[128:129]
	v_cvt_pk_f32_fp8_e32 v[124:125], v155
	v_exp_f32_e32 v68, v128
	v_exp_f32_e32 v148, v129
	v_cvt_pk_f32_fp8_sdwa v[116:117], v155 src0_sel:WORD_1
	v_add_f32_e32 v68, 1.0, v68
	v_rcp_f32_e32 v120, v68
	v_add_f32_e32 v68, 1.0, v148
	v_rcp_f32_e32 v121, v68
	v_pk_fma_f32 v[148:149], v[60:61], v[166:167], v[12:13]
	v_pk_fma_f32 v[152:153], v[48:49], v[152:153], v[4:5]
	v_pk_fma_f32 v[148:149], v[44:45], v[150:151], v[148:149]
	v_pk_mul_f32 v[120:121], v[128:129], v[120:121]
	v_pk_fma_f32 v[148:149], v[28:29], v[156:157], v[148:149]
	v_med3_f32 v113, v113, s41, v1
	v_pk_mul_f32 v[120:121], v[148:149], v[120:121]
	v_pk_fma_f32 v[148:149], v[54:55], v[164:165], v[6:7]
	v_pk_fma_f32 v[148:149], v[38:39], v[146:147], v[148:149]
	v_pk_fma_f32 v[152:153], v[32:33], v[132:133], v[152:153]
	v_pk_fma_f32 v[148:149], v[22:23], v[136:137], v[148:149]
	v_pk_fma_f32 v[152:153], v[20:21], v[116:117], v[152:153]
	v_exp_f32_e32 v68, v148
	v_exp_f32_e32 v154, v149
	v_add_f32_e32 v68, 1.0, v68
	v_rcp_f32_e32 v128, v68
	v_add_f32_e32 v68, 1.0, v154
	v_rcp_f32_e32 v129, v68
	v_pk_fma_f32 v[154:155], v[46:47], v[162:163], v[2:3]
	s_waitcnt vmcnt(27)
	v_cvt_pk_f32_fp8_e32 v[168:169], v140
	v_pk_fma_f32 v[154:155], v[30:31], v[144:145], v[154:155]
	v_pk_mul_f32 v[128:129], v[148:149], v[128:129]
	v_pk_fma_f32 v[154:155], v[18:19], v[124:125], v[154:155]
	s_waitcnt vmcnt(26)
; __device__ __forceinline__ float sigmoidf_(float x) { return __builtin_amdgcn_rcpf(1.0f + __builtin_amdgcn_exp2f(-1.4426950408889634f * x)); }
	v_cvt_pk_f32_fp8_e32 v[162:163], v138
	v_pk_mul_f32 v[128:129], v[154:155], v[128:129]
	v_pk_fma_f32 v[154:155], v[56:57], v[160:161], v[8:9]
	v_pk_fma_f32 v[154:155], v[40:41], v[142:143], v[154:155]
	v_pk_fma_f32 v[158:159], v[64:65], v[158:159], v[16:17]
	v_pk_fma_f32 v[154:155], v[24:25], v[108:109], v[154:155]
	v_pk_fma_f32 v[158:159], v[52:53], v[170:171], v[158:159]
	v_exp_f32_e32 v68, v154
	v_exp_f32_e32 v160, v155
	v_pk_fma_f32 v[146:147], v[54:55], v[146:147], v[6:7]
	v_add_f32_e32 v68, 1.0, v68
	v_rcp_f32_e32 v148, v68
	v_add_f32_e32 v68, 1.0, v160
	v_rcp_f32_e32 v149, v68
	v_med3_f32 v68, v112, s41, v1
	v_cvt_pk_fp8_f32 v112, v68, v113
	v_med3_f32 v68, v120, s41, v1
	v_med3_f32 v120, v121, s41, v1
	v_med3_f32 v121, v128, s41, v1
	v_med3_f32 v128, v129, s41, v1
	v_cvt_pk_fp8_f32 v113, v121, v128
	v_pk_mul_f32 v[148:149], v[154:155], v[148:149]
	v_cvt_pk_fp8_f32 v112, v68, v120 op_sel:[0,0,1]
	v_pk_mul_f32 v[148:149], v[152:153], v[148:149]
	v_cvt_pk_f32_fp8_sdwa v[154:155], v140 src0_sel:WORD_1
	v_med3_f32 v68, v148, s41, v1
	v_med3_f32 v120, v149, s41, v1
	v_cvt_pk_fp8_f32 v113, v68, v120 op_sel:[0,0,1]
	v_add_co_u32_e32 v120, vcc, s25, v70
	v_cvt_pk_f32_fp8_e32 v[148:149], v141
	s_nop 0
	v_addc_co_u32_e32 v121, vcc, 0, v71, vcc
	global_store_dwordx2 v[120:121], v[112:113], off offset:1536
	v_pk_fma_f32 v[120:121], v[62:63], v[180:181], v[14:15]
	v_cvt_pk_f32_fp8_sdwa v[112:113], v141 src0_sel:WORD_1
	v_pk_fma_f32 v[120:121], v[50:51], v[182:183], v[120:121]
	v_cvt_pk_f32_fp8_sdwa v[152:153], v138 src0_sel:WORD_1
	v_pk_fma_f32 v[140:141], v[34:35], v[168:169], v[120:121]
	v_cvt_pk_f32_fp8_e32 v[128:129], v139
	v_exp_f32_e32 v68, v140
	v_exp_f32_e32 v160, v141
	v_cvt_pk_f32_fp8_sdwa v[120:121], v139 src0_sel:WORD_1
	v_add_f32_e32 v68, 1.0, v68
	v_rcp_f32_e32 v138, v68
	v_add_f32_e32 v68, 1.0, v160
	v_rcp_f32_e32 v139, v68
	v_pk_fma_f32 v[160:161], v[58:59], v[174:175], v[10:11]
	v_pk_fma_f32 v[158:159], v[36:37], v[154:155], v[158:159]
	v_pk_fma_f32 v[160:161], v[42:43], v[176:177], v[160:161]
	v_pk_fma_f32 v[160:161], v[26:27], v[162:163], v[160:161]
	v_pk_mul_f32 v[138:139], v[140:141], v[138:139]
	v_pk_mul_f32 v[138:139], v[160:161], v[138:139]
	v_exp_f32_e32 v68, v158
	v_exp_f32_e32 v160, v159
	v_add_f32_e32 v68, 1.0, v68
	v_rcp_f32_e32 v140, v68
	v_add_f32_e32 v68, 1.0, v160
	v_rcp_f32_e32 v141, v68
	v_pk_fma_f32 v[146:147], v[38:39], v[136:137], v[146:147]
	v_pk_fma_f32 v[150:151], v[60:61], v[150:151], v[12:13]
	v_pk_fma_f32 v[146:147], v[22:23], v[148:149], v[146:147]
	v_pk_mul_f32 v[140:141], v[158:159], v[140:141]
	v_exp_f32_e32 v68, v146
	v_exp_f32_e32 v158, v147
	v_pk_fma_f32 v[150:151], v[44:45], v[156:157], v[150:151]
	v_add_f32_e32 v68, 1.0, v68
	v_pk_fma_f32 v[150:151], v[28:29], v[152:153], v[150:151]
	v_pk_fma_f32 v[142:143], v[56:57], v[142:143], v[8:9]
	v_pk_fma_f32 v[142:143], v[40:41], v[108:109], v[142:143]
	v_pk_mul_f32 v[140:141], v[150:151], v[140:141]
	v_rcp_f32_e32 v150, v68
	v_add_f32_e32 v68, 1.0, v158
	v_rcp_f32_e32 v151, v68
	v_pk_fma_f32 v[142:143], v[24:25], v[112:113], v[142:143]
	v_pk_fma_f32 v[144:145], v[46:47], v[144:145], v[2:3]
	v_pk_mul_f32 v[146:147], v[146:147], v[150:151]
	v_exp_f32_e32 v68, v142
	v_exp_f32_e32 v150, v143
	v_pk_fma_f32 v[144:145], v[30:31], v[124:125], v[144:145]
	v_add_f32_e32 v68, 1.0, v68
	v_pk_fma_f32 v[144:145], v[18:19], v[128:129], v[144:145]
	v_pk_fma_f32 v[132:133], v[48:49], v[132:133], v[4:5]
	v_pk_fma_f32 v[132:133], v[32:33], v[116:117], v[132:133]
	v_pk_mul_f32 v[144:145], v[144:145], v[146:147]
	v_rcp_f32_e32 v146, v68
	v_add_f32_e32 v68, 1.0, v150
	v_rcp_f32_e32 v147, v68
	v_pk_fma_f32 v[132:133], v[20:21], v[120:121], v[132:133]
	v_med3_f32 v68, v138, s41, v1
	v_pk_mul_f32 v[142:143], v[142:143], v[146:147]
	v_med3_f32 v139, v139, s41, v1
	v_pk_mul_f32 v[132:133], v[132:133], v[142:143]
	v_cvt_pk_fp8_f32 v138, v68, v139
	v_med3_f32 v68, v140, s41, v1
	v_med3_f32 v140, v141, s41, v1
	v_med3_f32 v141, v144, s41, v1
	v_med3_f32 v142, v145, s41, v1
	v_cvt_pk_fp8_f32 v139, v141, v142
	v_cvt_pk_fp8_f32 v138, v68, v140 op_sel:[0,0,1]
	v_med3_f32 v68, v132, s41, v1
	v_med3_f32 v132, v133, s41, v1
	v_cvt_pk_fp8_f32 v139, v68, v132 op_sel:[0,0,1]
	v_add_co_u32_e32 v132, vcc, s46, v70
	s_waitcnt vmcnt(26)
	v_cvt_pk_f32_fp8_e32 v[142:143], v104
	v_addc_co_u32_e32 v133, vcc, 0, v71, vcc
	global_store_dwordx2 v[132:133], v[138:139], off offset:256
	v_pk_fma_f32 v[138:139], v[62:63], v[182:183], v[14:15]
	s_waitcnt vmcnt(26)
; __device__ __forceinline__ float sigmoidf_(float x) { return __builtin_amdgcn_rcpf(1.0f + __builtin_amdgcn_exp2f(-1.4426950408889634f * x)); }
	v_cvt_pk_f32_fp8_e32 v[164:165], v100
	v_pk_fma_f32 v[138:139], v[50:51], v[168:169], v[138:139]
	v_cvt_pk_f32_fp8_sdwa v[144:145], v100 src0_sel:WORD_1
	v_pk_fma_f32 v[138:139], v[34:35], v[142:143], v[138:139]
	v_pk_fma_f32 v[150:151], v[58:59], v[176:177], v[10:11]
	v_exp_f32_e32 v68, v138
	v_exp_f32_e32 v147, v139
	v_cvt_pk_f32_fp8_sdwa v[160:161], v104 src0_sel:WORD_1
	v_add_f32_e32 v68, 1.0, v68
	v_rcp_f32_e32 v146, v68
	v_add_f32_e32 v68, 1.0, v147
	v_rcp_f32_e32 v147, v68
	v_pk_fma_f32 v[150:151], v[42:43], v[162:163], v[150:151]
	v_cvt_pk_f32_fp8_e32 v[140:141], v105
	v_pk_fma_f32 v[150:151], v[26:27], v[164:165], v[150:151]
	v_pk_mul_f32 v[138:139], v[138:139], v[146:147]
	v_pk_mul_f32 v[138:139], v[150:151], v[138:139]
	v_pk_fma_f32 v[150:151], v[64:65], v[170:171], v[16:17]
	v_pk_fma_f32 v[150:151], v[52:53], v[154:155], v[150:151]
	v_pk_fma_f32 v[136:137], v[54:55], v[136:137], v[6:7]
	v_pk_fma_f32 v[150:151], v[36:37], v[160:161], v[150:151]
	v_pk_fma_f32 v[156:157], v[60:61], v[156:157], v[12:13]
	v_exp_f32_e32 v68, v150
	v_exp_f32_e32 v158, v151
	v_pk_fma_f32 v[136:137], v[38:39], v[148:149], v[136:137]
	v_add_f32_e32 v68, 1.0, v68
	v_rcp_f32_e32 v146, v68
	v_add_f32_e32 v68, 1.0, v158
	v_rcp_f32_e32 v147, v68
	v_pk_fma_f32 v[156:157], v[44:45], v[152:153], v[156:157]
	v_pk_fma_f32 v[136:137], v[22:23], v[140:141], v[136:137]
	v_pk_fma_f32 v[156:157], v[28:29], v[144:145], v[156:157]
	v_pk_mul_f32 v[146:147], v[150:151], v[146:147]
	v_pk_mul_f32 v[146:147], v[156:157], v[146:147]
	v_exp_f32_e32 v68, v136
	v_exp_f32_e32 v156, v137
	v_cvt_pk_f32_fp8_sdwa v[104:105], v105 src0_sel:WORD_1
	v_add_f32_e32 v68, 1.0, v68
	v_rcp_f32_e32 v150, v68
	v_add_f32_e32 v68, 1.0, v156
	v_rcp_f32_e32 v151, v68
	v_pk_fma_f32 v[108:109], v[56:57], v[108:109], v[8:9]
	v_cvt_pk_f32_fp8_e32 v[132:133], v101
	v_pk_fma_f32 v[108:109], v[40:41], v[112:113], v[108:109]
	v_pk_mul_f32 v[136:137], v[136:137], v[150:151]
	v_pk_fma_f32 v[108:109], v[24:25], v[104:105], v[108:109]
	v_pk_fma_f32 v[124:125], v[46:47], v[124:125], v[2:3]
	v_exp_f32_e32 v68, v108
	v_exp_f32_e32 v150, v109
	v_pk_fma_f32 v[124:125], v[30:31], v[128:129], v[124:125]
	v_add_f32_e32 v68, 1.0, v68
	v_pk_fma_f32 v[124:125], v[18:19], v[132:133], v[124:125]
	v_cvt_pk_f32_fp8_sdwa v[100:101], v101 src0_sel:WORD_1
	v_pk_fma_f32 v[116:117], v[48:49], v[116:117], v[4:5]
	v_pk_mul_f32 v[124:125], v[124:125], v[136:137]
	v_rcp_f32_e32 v136, v68
	v_add_f32_e32 v68, 1.0, v150
	v_rcp_f32_e32 v137, v68
	v_pk_fma_f32 v[116:117], v[32:33], v[120:121], v[116:117]
	v_med3_f32 v68, v138, s41, v1
	v_pk_fma_f32 v[116:117], v[20:21], v[100:101], v[116:117]
	v_pk_mul_f32 v[108:109], v[108:109], v[136:137]
	v_med3_f32 v124, v124, s41, v1
	v_pk_mul_f32 v[108:109], v[116:117], v[108:109]
	v_med3_f32 v117, v139, s41, v1
	v_cvt_pk_fp8_f32 v116, v68, v117
	v_med3_f32 v125, v125, s41, v1
	s_waitcnt vmcnt(25)
	v_cvt_pk_f32_fp8_e32 v[172:173], v96
	v_cvt_pk_fp8_f32 v117, v124, v125
	v_pk_fma_f32 v[138:139], v[62:63], v[168:169], v[14:15]
	v_med3_f32 v68, v146, s41, v1
	v_med3_f32 v136, v147, s41, v1
	v_pk_fma_f32 v[138:139], v[50:51], v[142:143], v[138:139]
	v_cvt_pk_fp8_f32 v116, v68, v136 op_sel:[0,0,1]
	v_med3_f32 v68, v108, s41, v1
	v_med3_f32 v108, v109, s41, v1
	v_pk_fma_f32 v[138:139], v[34:35], v[172:173], v[138:139]
	v_cvt_pk_fp8_f32 v117, v68, v108 op_sel:[0,0,1]
	s_waitcnt vmcnt(24)
	v_cvt_pk_f32_fp8_e32 v[166:167], v92
	v_cvt_pk_f32_fp8_sdwa v[124:125], v92 src0_sel:WORD_1
	v_exp_f32_e32 v68, v138
	v_exp_f32_e32 v147, v139
	v_pk_fma_f32 v[150:151], v[58:59], v[162:163], v[10:11]
	v_add_f32_e32 v68, 1.0, v68
	v_rcp_f32_e32 v146, v68
	v_add_f32_e32 v68, 1.0, v147
	v_rcp_f32_e32 v147, v68
	v_cvt_pk_f32_fp8_sdwa v[136:137], v96 src0_sel:WORD_1
	v_pk_fma_f32 v[150:151], v[42:43], v[164:165], v[150:151]
	v_add_co_u32_e32 v108, vcc, s26, v70
	v_pk_fma_f32 v[150:151], v[26:27], v[166:167], v[150:151]
	v_pk_mul_f32 v[138:139], v[138:139], v[146:147]
	v_pk_mul_f32 v[138:139], v[150:151], v[138:139]
	v_pk_fma_f32 v[150:151], v[64:65], v[154:155], v[16:17]
	v_addc_co_u32_e32 v109, vcc, 0, v71, vcc
	v_pk_fma_f32 v[150:151], v[52:53], v[160:161], v[150:151]
	global_store_dwordx2 v[108:109], v[116:117], off offset:3072
	v_pk_fma_f32 v[150:151], v[36:37], v[136:137], v[150:151]
	v_cvt_pk_f32_fp8_e32 v[116:117], v97
	v_exp_f32_e32 v68, v150
	v_exp_f32_e32 v154, v151
	v_add_f32_e32 v68, 1.0, v68
	v_rcp_f32_e32 v146, v68
	v_add_f32_e32 v68, 1.0, v154
	v_rcp_f32_e32 v147, v68
	v_pk_fma_f32 v[148:149], v[54:55], v[148:149], v[6:7]
	v_pk_fma_f32 v[152:153], v[60:61], v[152:153], v[12:13]
	v_pk_fma_f32 v[148:149], v[38:39], v[140:141], v[148:149]
	v_pk_fma_f32 v[152:153], v[44:45], v[144:145], v[152:153]
	v_pk_fma_f32 v[148:149], v[22:23], v[116:117], v[148:149]
	v_pk_fma_f32 v[152:153], v[28:29], v[124:125], v[152:153]
	v_pk_mul_f32 v[146:147], v[150:151], v[146:147]
	v_pk_mul_f32 v[146:147], v[152:153], v[146:147]
	v_exp_f32_e32 v68, v148
	v_exp_f32_e32 v152, v149
	v_cvt_pk_f32_fp8_sdwa v[96:97], v97 src0_sel:WORD_1
	v_add_f32_e32 v68, 1.0, v68
	v_rcp_f32_e32 v150, v68
	v_add_f32_e32 v68, 1.0, v152
	v_rcp_f32_e32 v151, v68
	v_pk_fma_f32 v[112:113], v[56:57], v[112:113], v[8:9]
	v_cvt_pk_f32_fp8_e32 v[108:109], v93
	v_pk_fma_f32 v[112:113], v[40:41], v[104:105], v[112:113]
	v_pk_mul_f32 v[148:149], v[148:149], v[150:151]
	v_pk_fma_f32 v[112:113], v[24:25], v[96:97], v[112:113]
	v_pk_fma_f32 v[128:129], v[46:47], v[128:129], v[2:3]
	v_exp_f32_e32 v68, v112
	v_exp_f32_e32 v150, v113
	v_pk_fma_f32 v[128:129], v[30:31], v[132:133], v[128:129]
	v_add_f32_e32 v68, 1.0, v68
	v_pk_fma_f32 v[128:129], v[18:19], v[108:109], v[128:129]
	v_cvt_pk_f32_fp8_sdwa v[92:93], v93 src0_sel:WORD_1
	v_pk_fma_f32 v[120:121], v[48:49], v[120:121], v[4:5]
	v_pk_mul_f32 v[128:129], v[128:129], v[148:149]
	v_rcp_f32_e32 v148, v68
	v_add_f32_e32 v68, 1.0, v150
	v_rcp_f32_e32 v149, v68
	v_pk_fma_f32 v[120:121], v[32:33], v[100:101], v[120:121]
	v_med3_f32 v68, v138, s41, v1
	v_pk_fma_f32 v[120:121], v[20:21], v[92:93], v[120:121]
	v_pk_mul_f32 v[112:113], v[112:113], v[148:149]
	v_med3_f32 v128, v128, s41, v1
	v_pk_mul_f32 v[112:113], v[120:121], v[112:113]
	v_med3_f32 v121, v139, s41, v1
	v_cvt_pk_fp8_f32 v120, v68, v121
	v_med3_f32 v129, v129, s41, v1
	v_cvt_pk_fp8_f32 v121, v128, v129
	s_waitcnt vmcnt(24)
; __device__ __forceinline__ float sigmoidf_(float x) { return __builtin_amdgcn_rcpf(1.0f + __builtin_amdgcn_exp2f(-1.4426950408889634f * x)); }
	v_cvt_pk_f32_fp8_e32 v[168:169], v88
	v_med3_f32 v68, v146, s41, v1
	v_med3_f32 v138, v147, s41, v1
	v_cvt_pk_fp8_f32 v120, v68, v138 op_sel:[0,0,1]
	v_med3_f32 v68, v112, s41, v1
	v_med3_f32 v112, v113, s41, v1
	v_cvt_pk_f32_fp8_sdwa v[158:159], v88 src0_sel:WORD_1
	v_cvt_pk_f32_fp8_e32 v[150:151], v89
	v_cvt_pk_f32_fp8_sdwa v[138:139], v89 src0_sel:WORD_1
	v_pk_fma_f32 v[88:89], v[62:63], v[142:143], v[14:15]
	v_cvt_pk_fp8_f32 v121, v68, v112 op_sel:[0,0,1]
	v_pk_fma_f32 v[88:89], v[50:51], v[172:173], v[88:89]
	v_add_co_u32_e32 v112, vcc, s47, v70
	v_pk_fma_f32 v[88:89], v[34:35], v[168:169], v[88:89]
	s_nop 0
	v_addc_co_u32_e32 v113, vcc, 0, v71, vcc
	s_waitcnt vmcnt(23)
	v_cvt_pk_f32_fp8_e32 v[162:163], v84
	v_cvt_pk_f32_fp8_sdwa v[154:155], v84 src0_sel:WORD_1
	v_exp_f32_e32 v68, v88
	global_store_dwordx2 v[112:113], v[120:121], off offset:1792
	v_exp_f32_e32 v112, v89
	v_add_f32_e32 v68, 1.0, v68
	v_rcp_f32_e32 v84, v68
	v_cvt_pk_f32_fp8_e32 v[146:147], v85
	v_add_f32_e32 v68, 1.0, v112
	v_cvt_pk_f32_fp8_sdwa v[142:143], v85 src0_sel:WORD_1
	v_rcp_f32_e32 v85, v68
	v_pk_fma_f32 v[112:113], v[58:59], v[164:165], v[10:11]
	v_pk_fma_f32 v[104:105], v[56:57], v[104:105], v[8:9]
	v_pk_fma_f32 v[112:113], v[42:43], v[166:167], v[112:113]
	v_pk_mul_f32 v[84:85], v[88:89], v[84:85]
	v_pk_fma_f32 v[112:113], v[26:27], v[162:163], v[112:113]
	v_pk_fma_f32 v[104:105], v[40:41], v[96:97], v[104:105]
	v_pk_mul_f32 v[84:85], v[112:113], v[84:85]
	v_pk_fma_f32 v[112:113], v[64:65], v[160:161], v[16:17]
	v_pk_fma_f32 v[112:113], v[52:53], v[136:137], v[112:113]
	v_pk_fma_f32 v[104:105], v[24:25], v[138:139], v[104:105]
	v_pk_fma_f32 v[112:113], v[36:37], v[158:159], v[112:113]
	v_pk_fma_f32 v[100:101], v[48:49], v[100:101], v[4:5]
	v_exp_f32_e32 v68, v112
	v_exp_f32_e32 v120, v113
	v_pk_fma_f32 v[100:101], v[32:33], v[92:93], v[100:101]
	v_add_f32_e32 v68, 1.0, v68
	v_rcp_f32_e32 v88, v68
	v_add_f32_e32 v68, 1.0, v120
	v_rcp_f32_e32 v89, v68
	v_pk_fma_f32 v[120:121], v[60:61], v[144:145], v[12:13]
	v_pk_fma_f32 v[100:101], v[20:21], v[142:143], v[100:101]
	v_pk_fma_f32 v[120:121], v[44:45], v[124:125], v[120:121]
	v_pk_mul_f32 v[88:89], v[112:113], v[88:89]
	v_pk_fma_f32 v[120:121], v[28:29], v[154:155], v[120:121]
	v_pk_mul_f32 v[88:89], v[120:121], v[88:89]
	v_pk_fma_f32 v[120:121], v[54:55], v[140:141], v[6:7]
	v_pk_fma_f32 v[120:121], v[38:39], v[116:117], v[120:121]
	v_med3_f32 v85, v85, s41, v1
	v_pk_fma_f32 v[120:121], v[22:23], v[150:151], v[120:121]
	s_waitcnt vmcnt(23)
	v_cvt_pk_f32_fp8_e32 v[170:171], v80
	v_exp_f32_e32 v68, v120
	v_exp_f32_e32 v128, v121
	v_cvt_pk_f32_fp8_sdwa v[160:161], v80 src0_sel:WORD_1
	v_add_f32_e32 v68, 1.0, v68
	v_rcp_f32_e32 v112, v68
	v_add_f32_e32 v68, 1.0, v128
	v_rcp_f32_e32 v113, v68
	v_pk_fma_f32 v[128:129], v[46:47], v[132:133], v[2:3]
	v_pk_fma_f32 v[128:129], v[30:31], v[108:109], v[128:129]
	v_pk_mul_f32 v[112:113], v[120:121], v[112:113]
	v_pk_fma_f32 v[128:129], v[18:19], v[146:147], v[128:129]
	v_exp_f32_e32 v68, v104
	v_pk_mul_f32 v[112:113], v[128:129], v[112:113]
	v_exp_f32_e32 v128, v105
	v_add_f32_e32 v68, 1.0, v68
	v_rcp_f32_e32 v120, v68
	v_add_f32_e32 v68, 1.0, v128
	v_rcp_f32_e32 v121, v68
	v_med3_f32 v68, v84, s41, v1
	v_cvt_pk_fp8_f32 v84, v68, v85
	v_pk_mul_f32 v[104:105], v[104:105], v[120:121]
	v_med3_f32 v68, v88, s41, v1
	v_pk_mul_f32 v[100:101], v[100:101], v[104:105]
	v_med3_f32 v88, v89, s41, v1
	v_med3_f32 v89, v112, s41, v1
	v_med3_f32 v104, v113, s41, v1
	v_cvt_pk_fp8_f32 v85, v89, v104
	v_cvt_pk_fp8_f32 v84, v68, v88 op_sel:[0,0,1]
	v_med3_f32 v68, v100, s41, v1
	v_med3_f32 v88, v101, s41, v1
	v_cvt_pk_f32_fp8_e32 v[152:153], v81
	v_cvt_pk_f32_fp8_sdwa v[140:141], v81 src0_sel:WORD_1
	v_pk_fma_f32 v[80:81], v[62:63], v[172:173], v[14:15]
	v_cvt_pk_fp8_f32 v85, v68, v88 op_sel:[0,0,1]
	v_pk_fma_f32 v[80:81], v[50:51], v[168:169], v[80:81]
	v_add_co_u32_e32 v88, vcc, s27, v70
	v_pk_fma_f32 v[80:81], v[34:35], v[170:171], v[80:81]
	s_nop 0
	v_addc_co_u32_e32 v89, vcc, 0, v71, vcc
	s_waitcnt vmcnt(22)
	v_cvt_pk_f32_fp8_e32 v[164:165], v76
	v_cvt_pk_f32_fp8_sdwa v[156:157], v76 src0_sel:WORD_1
	v_exp_f32_e32 v68, v80
	global_store_dwordx2 v[88:89], v[84:85], off offset:512
	v_exp_f32_e32 v84, v81
	v_add_f32_e32 v68, 1.0, v68
	v_rcp_f32_e32 v76, v68
	v_cvt_pk_f32_fp8_e32 v[148:149], v77
	v_add_f32_e32 v68, 1.0, v84
	v_cvt_pk_f32_fp8_sdwa v[144:145], v77 src0_sel:WORD_1
	v_rcp_f32_e32 v77, v68
	v_pk_fma_f32 v[84:85], v[58:59], v[166:167], v[10:11]
	v_pk_fma_f32 v[96:97], v[56:57], v[96:97], v[8:9]
	v_pk_fma_f32 v[84:85], v[42:43], v[162:163], v[84:85]
	v_pk_mul_f32 v[76:77], v[80:81], v[76:77]
	v_pk_fma_f32 v[84:85], v[26:27], v[164:165], v[84:85]
	v_pk_fma_f32 v[96:97], v[40:41], v[138:139], v[96:97]
	v_pk_mul_f32 v[76:77], v[84:85], v[76:77]
	v_pk_fma_f32 v[84:85], v[64:65], v[136:137], v[16:17]
	v_pk_fma_f32 v[84:85], v[52:53], v[158:159], v[84:85]
	v_pk_fma_f32 v[96:97], v[24:25], v[140:141], v[96:97]
	v_pk_fma_f32 v[84:85], v[36:37], v[160:161], v[84:85]
	v_pk_fma_f32 v[92:93], v[48:49], v[92:93], v[4:5]
	v_exp_f32_e32 v68, v84
	v_exp_f32_e32 v88, v85
	v_med3_f32 v77, v77, s41, v1
	v_add_f32_e32 v68, 1.0, v68
	v_rcp_f32_e32 v80, v68
	v_add_f32_e32 v68, 1.0, v88
	v_rcp_f32_e32 v81, v68
	v_pk_fma_f32 v[88:89], v[60:61], v[124:125], v[12:13]
	v_pk_fma_f32 v[92:93], v[32:33], v[142:143], v[92:93]
	v_pk_fma_f32 v[88:89], v[44:45], v[154:155], v[88:89]
	v_pk_mul_f32 v[80:81], v[84:85], v[80:81]
	v_pk_fma_f32 v[88:89], v[28:29], v[156:157], v[88:89]
	s_waitcnt vmcnt(22)
; #define CV_LOAD(G_, V_, r0_) do { _Pragma("unroll") for (int i_ = 0; i_ < 8; ++i_) { G_[i_] = *(const GAS v2u*)(ap + (size_t)((r0_) + i_) * F2); V_[i_] = *(const GAS v2u*)(ap + (size_t)((r0_) + i_) * F2 + 128); } } while (0)
; __device__ __forceinline__ void conv_phase(Frame& F) {
;     ...
;         CV_LOAD(GA, VA, 0); CV_LOAD(GB, VB, 8); CV_COMP(GA, VA, 0); CV_LOAD(GA, VA, 16); CV_COMP(GB, VB, 8); CV_LOAD(GB, VB, 24); CV_COMP(GA, VA, 16); CV_COMP(GB, VB, 24);
	v_cvt_pk_f32_fp8_e32 v[180:181], v134
	v_pk_mul_f32 v[80:81], v[88:89], v[80:81]
	v_pk_fma_f32 v[88:89], v[54:55], v[116:117], v[6:7]
	v_pk_fma_f32 v[88:89], v[38:39], v[150:151], v[88:89]
	v_pk_fma_f32 v[92:93], v[20:21], v[144:145], v[92:93]
	v_pk_fma_f32 v[88:89], v[22:23], v[152:153], v[88:89]
	v_exp_f32_e32 v68, v88
	v_exp_f32_e32 v100, v89
	v_pk_fma_f32 v[168:169], v[62:63], v[168:169], v[14:15]
	v_add_f32_e32 v68, 1.0, v68
	v_rcp_f32_e32 v84, v68
	v_add_f32_e32 v68, 1.0, v100
	v_rcp_f32_e32 v85, v68
	v_pk_fma_f32 v[100:101], v[46:47], v[108:109], v[2:3]
	v_pk_fma_f32 v[100:101], v[30:31], v[146:147], v[100:101]
	v_pk_mul_f32 v[84:85], v[88:89], v[84:85]
	v_pk_fma_f32 v[100:101], v[18:19], v[148:149], v[100:101]
	v_exp_f32_e32 v68, v96
	v_pk_mul_f32 v[84:85], v[100:101], v[84:85]
	v_exp_f32_e32 v100, v97
	v_add_f32_e32 v68, 1.0, v68
	v_rcp_f32_e32 v88, v68
	v_add_f32_e32 v68, 1.0, v100
	v_rcp_f32_e32 v89, v68
	v_med3_f32 v68, v76, s41, v1
	v_cvt_pk_fp8_f32 v76, v68, v77
	v_med3_f32 v68, v80, s41, v1
	v_med3_f32 v80, v81, s41, v1
	v_med3_f32 v81, v84, s41, v1
	v_med3_f32 v84, v85, s41, v1
	v_cvt_pk_fp8_f32 v77, v81, v84
	v_pk_mul_f32 v[88:89], v[96:97], v[88:89]
	v_pk_fma_f32 v[168:169], v[50:51], v[170:171], v[168:169]
	v_pk_mul_f32 v[88:89], v[92:93], v[88:89]
	v_cvt_pk_fp8_f32 v76, v68, v80 op_sel:[0,0,1]
	v_med3_f32 v68, v88, s41, v1
	v_med3_f32 v80, v89, s41, v1
	v_pk_fma_f32 v[168:169], v[34:35], v[180:181], v[168:169]
	v_cvt_pk_fp8_f32 v77, v68, v80 op_sel:[0,0,1]
	s_waitcnt vmcnt(21)
	v_cvt_pk_f32_fp8_e32 v[178:179], v130
	v_cvt_pk_f32_fp8_sdwa v[174:175], v130 src0_sel:WORD_1
	v_exp_f32_e32 v68, v168
	v_exp_f32_e32 v183, v169
	v_cvt_pk_f32_fp8_sdwa v[176:177], v134 src0_sel:WORD_1
	v_add_f32_e32 v68, 1.0, v68
	v_rcp_f32_e32 v182, v68
	v_add_f32_e32 v68, 1.0, v183
	v_rcp_f32_e32 v183, v68
	v_pk_fma_f32 v[158:159], v[64:65], v[158:159], v[16:17]
	v_add_co_u32_e32 v80, vcc, s48, v70
	v_pk_fma_f32 v[158:159], v[52:53], v[160:161], v[158:159]
	v_pk_mul_f32 v[168:169], v[168:169], v[182:183]
	v_pk_fma_f32 v[158:159], v[36:37], v[176:177], v[158:159]
	v_pk_fma_f32 v[162:163], v[58:59], v[162:163], v[10:11]
	v_exp_f32_e32 v68, v158
	v_exp_f32_e32 v182, v159
	v_addc_co_u32_e32 v81, vcc, 0, v71, vcc
	v_pk_fma_f32 v[162:163], v[42:43], v[164:165], v[162:163]
	global_store_dwordx2 v[80:81], v[76:77], off offset:3328
	v_add_co_u32_e32 v76, vcc, s42, v72
	v_pk_fma_f32 v[162:163], v[26:27], v[178:179], v[162:163]
	s_nop 0
	v_addc_co_u32_e32 v77, vcc, 0, v73, vcc
	v_cvt_pk_f32_fp8_e32 v[172:173], v135
	v_add_f32_e32 v68, 1.0, v68
	v_add_co_u32_e32 v80, vcc, s49, v72
	v_pk_mul_f32 v[162:163], v[162:163], v[168:169]
	v_rcp_f32_e32 v168, v68
	v_add_f32_e32 v68, 1.0, v182
	v_addc_co_u32_e32 v81, vcc, 0, v73, vcc
	v_rcp_f32_e32 v169, v68
	v_pk_fma_f32 v[150:151], v[54:55], v[150:151], v[6:7]
	global_load_dwordx2 v[136:137], v[76:77], off nt
	global_load_dwordx2 v[132:133], v[76:77], off offset:128 nt
	global_load_dwordx2 v[128:129], v[80:81], off offset:1536 nt
	global_load_dwordx2 v[124:125], v[80:81], off offset:1664 nt
	v_add_co_u32_e32 v76, vcc, s50, v72
	v_pk_fma_f32 v[150:151], v[38:39], v[152:153], v[150:151]
	s_nop 0
	v_addc_co_u32_e32 v77, vcc, 0, v73, vcc
	v_pk_fma_f32 v[150:151], v[22:23], v[172:173], v[150:151]
	v_add_co_u32_e32 v80, vcc, s51, v72
	s_nop 0
	s_nop 0
	v_addc_co_u32_e32 v81, vcc, 0, v73, vcc
	v_pk_mul_f32 v[158:159], v[158:159], v[168:169]
	v_exp_f32_e32 v68, v150
	global_load_dwordx2 v[120:121], v[76:77], off offset:3072 nt
	global_load_dwordx2 v[116:117], v[76:77], off offset:3200 nt
	global_load_dwordx2 v[112:113], v[80:81], off offset:512 nt
	global_load_dwordx2 v[108:109], v[80:81], off offset:640 nt
	v_add_co_u32_e32 v76, vcc, s52, v72
	v_pk_fma_f32 v[154:155], v[60:61], v[154:155], v[12:13]
	v_exp_f32_e32 v168, v151
	v_addc_co_u32_e32 v77, vcc, 0, v73, vcc
	v_pk_fma_f32 v[154:155], v[44:45], v[156:157], v[154:155]
	v_add_co_u32_e32 v80, vcc, s53, v72
	v_pk_fma_f32 v[154:155], v[28:29], v[174:175], v[154:155]
	s_nop 0
	v_addc_co_u32_e32 v81, vcc, 0, v73, vcc
	v_cvt_pk_f32_fp8_sdwa v[134:135], v135 src0_sel:WORD_1
	v_add_f32_e32 v68, 1.0, v68
	global_load_dwordx2 v[104:105], v[76:77], off offset:2048 nt
	global_load_dwordx2 v[100:101], v[76:77], off offset:2176 nt
	global_load_dwordx2 v[96:97], v[80:81], off offset:3584 nt
	global_load_dwordx2 v[92:93], v[80:81], off offset:3712 nt
	v_add_co_u32_e32 v76, vcc, s54, v72
	v_pk_mul_f32 v[154:155], v[154:155], v[158:159]
	v_rcp_f32_e32 v158, v68
	v_add_f32_e32 v68, 1.0, v168
	v_addc_co_u32_e32 v77, vcc, 0, v73, vcc
	v_rcp_f32_e32 v159, v68
	v_pk_fma_f32 v[138:139], v[56:57], v[138:139], v[8:9]
	v_add_co_u32_e32 v166, vcc, s55, v72
	v_pk_fma_f32 v[138:139], v[40:41], v[140:141], v[138:139]
	s_nop 0
	v_addc_co_u32_e32 v167, vcc, 0, v73, vcc
	v_pk_fma_f32 v[138:139], v[24:25], v[134:135], v[138:139]
	global_load_dwordx2 v[88:89], v[76:77], off offset:1024 nt
	global_load_dwordx2 v[84:85], v[76:77], off offset:1152 nt
	global_load_dwordx2 v[80:81], v[166:167], off offset:2560 nt
	s_nop 0
	global_load_dwordx2 v[76:77], v[166:167], off offset:2688 nt
	v_cvt_pk_f32_fp8_e32 v[166:167], v131
	v_pk_mul_f32 v[150:151], v[150:151], v[158:159]
	v_exp_f32_e32 v68, v138
	v_pk_fma_f32 v[146:147], v[46:47], v[146:147], v[2:3]
	v_exp_f32_e32 v158, v139
	v_pk_fma_f32 v[146:147], v[30:31], v[148:149], v[146:147]
	v_add_f32_e32 v68, 1.0, v68
	v_pk_fma_f32 v[146:147], v[18:19], v[166:167], v[146:147]
	v_cvt_pk_f32_fp8_sdwa v[130:131], v131 src0_sel:WORD_1
	v_pk_fma_f32 v[142:143], v[48:49], v[142:143], v[4:5]
	v_pk_mul_f32 v[146:147], v[146:147], v[150:151]
	v_rcp_f32_e32 v150, v68
	v_add_f32_e32 v68, 1.0, v158
	v_rcp_f32_e32 v151, v68
	v_pk_fma_f32 v[142:143], v[32:33], v[144:145], v[142:143]
	v_med3_f32 v68, v162, s41, v1
	v_pk_fma_f32 v[142:143], v[20:21], v[130:131], v[142:143]
	v_pk_mul_f32 v[138:139], v[138:139], v[150:151]
	v_med3_f32 v146, v146, s41, v1
	v_pk_mul_f32 v[138:139], v[142:143], v[138:139]
	v_med3_f32 v143, v163, s41, v1
	v_cvt_pk_fp8_f32 v142, v68, v143
	v_med3_f32 v147, v147, s41, v1
	s_waitcnt vmcnt(37)
; #define CV_LOAD(G_, V_, r0_) do { _Pragma("unroll") for (int i_ = 0; i_ < 8; ++i_) { G_[i_] = *(const GAS v2u*)(ap + (size_t)((r0_) + i_) * F2); V_[i_] = *(const GAS v2u*)(ap + (size_t)((r0_) + i_) * F2 + 128); } } while (0)
; __device__ __forceinline__ void conv_phase(Frame& F) {
;     ...
;         CV_LOAD(GA, VA, 0); CV_LOAD(GB, VB, 8); CV_COMP(GA, VA, 0); CV_LOAD(GA, VA, 16); CV_COMP(GB, VB, 8); CV_LOAD(GB, VB, 24); CV_COMP(GA, VA, 16); CV_COMP(GB, VB, 24);
	v_cvt_pk_f32_fp8_e32 v[168:169], v126
	v_med3_f32 v68, v154, s41, v1
	v_med3_f32 v150, v155, s41, v1
	v_cvt_pk_fp8_f32 v143, v146, v147
	v_cvt_pk_fp8_f32 v142, v68, v150 op_sel:[0,0,1]
	v_pk_fma_f32 v[150:151], v[62:63], v[170:171], v[14:15]
	v_med3_f32 v68, v138, s41, v1
	v_pk_fma_f32 v[150:151], v[50:51], v[180:181], v[150:151]
	v_med3_f32 v138, v139, s41, v1
	v_pk_fma_f32 v[150:151], v[34:35], v[168:169], v[150:151]
	v_cvt_pk_fp8_f32 v143, v68, v138 op_sel:[0,0,1]
	s_waitcnt vmcnt(36)
	v_cvt_pk_f32_fp8_e32 v[158:159], v122
	v_cvt_pk_f32_fp8_sdwa v[146:147], v122 src0_sel:WORD_1
	v_exp_f32_e32 v68, v150
	v_exp_f32_e32 v163, v151
	v_cvt_pk_f32_fp8_sdwa v[154:155], v126 src0_sel:WORD_1
	v_add_f32_e32 v68, 1.0, v68
	v_rcp_f32_e32 v162, v68
	v_add_f32_e32 v68, 1.0, v163
	v_rcp_f32_e32 v163, v68
	v_pk_fma_f32 v[160:161], v[64:65], v[160:161], v[16:17]
	v_pk_fma_f32 v[164:165], v[58:59], v[164:165], v[10:11]
	v_pk_fma_f32 v[160:161], v[52:53], v[176:177], v[160:161]
	v_pk_fma_f32 v[164:165], v[42:43], v[178:179], v[164:165]
	v_pk_fma_f32 v[160:161], v[36:37], v[154:155], v[160:161]
	v_pk_fma_f32 v[164:165], v[26:27], v[158:159], v[164:165]
	v_pk_mul_f32 v[150:151], v[150:151], v[162:163]
	v_pk_mul_f32 v[150:151], v[164:165], v[150:151]
	v_exp_f32_e32 v68, v160
	v_exp_f32_e32 v164, v161
	v_add_co_u32_e32 v138, vcc, s28, v70
	v_add_f32_e32 v68, 1.0, v68
	s_nop 0
	v_addc_co_u32_e32 v139, vcc, 0, v71, vcc
	global_store_dwordx2 v[138:139], v[142:143], off offset:2048
	v_cvt_pk_f32_fp8_e32 v[142:143], v127
	v_rcp_f32_e32 v162, v68
	v_add_f32_e32 v68, 1.0, v164
	v_rcp_f32_e32 v163, v68
	v_pk_fma_f32 v[152:153], v[54:55], v[152:153], v[6:7]
	v_pk_fma_f32 v[156:157], v[60:61], v[156:157], v[12:13]
	v_pk_fma_f32 v[152:153], v[38:39], v[172:173], v[152:153]
	v_pk_mul_f32 v[160:161], v[160:161], v[162:163]
	v_pk_fma_f32 v[152:153], v[22:23], v[142:143], v[152:153]
	v_pk_fma_f32 v[156:157], v[44:45], v[174:175], v[156:157]
	v_exp_f32_e32 v68, v152
	v_exp_f32_e32 v162, v153
	v_pk_fma_f32 v[156:157], v[28:29], v[146:147], v[156:157]
	v_cvt_pk_f32_fp8_sdwa v[126:127], v127 src0_sel:WORD_1
	v_add_f32_e32 v68, 1.0, v68
	v_pk_mul_f32 v[156:157], v[156:157], v[160:161]
	v_rcp_f32_e32 v160, v68
	v_add_f32_e32 v68, 1.0, v162
	v_rcp_f32_e32 v161, v68
	v_pk_fma_f32 v[140:141], v[56:57], v[140:141], v[8:9]
	v_cvt_pk_f32_fp8_e32 v[138:139], v123
	v_pk_fma_f32 v[140:141], v[40:41], v[134:135], v[140:141]
	v_pk_mul_f32 v[152:153], v[152:153], v[160:161]
	v_pk_fma_f32 v[140:141], v[24:25], v[126:127], v[140:141]
	v_pk_fma_f32 v[148:149], v[46:47], v[148:149], v[2:3]
	v_exp_f32_e32 v68, v140
	v_exp_f32_e32 v160, v141
	v_pk_fma_f32 v[148:149], v[30:31], v[166:167], v[148:149]
	v_add_f32_e32 v68, 1.0, v68
	v_pk_fma_f32 v[148:149], v[18:19], v[138:139], v[148:149]
	v_cvt_pk_f32_fp8_sdwa v[122:123], v123 src0_sel:WORD_1
	v_pk_fma_f32 v[144:145], v[48:49], v[144:145], v[4:5]
	v_pk_mul_f32 v[148:149], v[148:149], v[152:153]
	v_rcp_f32_e32 v152, v68
	v_add_f32_e32 v68, 1.0, v160
	v_rcp_f32_e32 v153, v68
	v_pk_fma_f32 v[144:145], v[32:33], v[130:131], v[144:145]
	v_med3_f32 v68, v150, s41, v1
	v_pk_fma_f32 v[144:145], v[20:21], v[122:123], v[144:145]
	v_pk_mul_f32 v[140:141], v[140:141], v[152:153]
	v_med3_f32 v148, v148, s41, v1
	v_pk_mul_f32 v[140:141], v[144:145], v[140:141]
	v_med3_f32 v145, v151, s41, v1
	v_cvt_pk_fp8_f32 v144, v68, v145
	v_med3_f32 v149, v149, s41, v1
	s_waitcnt vmcnt(36)
	v_cvt_pk_f32_fp8_e32 v[164:165], v118
	v_med3_f32 v68, v156, s41, v1
	v_med3_f32 v150, v157, s41, v1
	v_cvt_pk_fp8_f32 v145, v148, v149
	v_cvt_pk_fp8_f32 v144, v68, v150 op_sel:[0,0,1]
	v_pk_fma_f32 v[150:151], v[62:63], v[180:181], v[14:15]
	v_med3_f32 v68, v140, s41, v1
	v_pk_fma_f32 v[150:151], v[50:51], v[168:169], v[150:151]
	v_med3_f32 v140, v141, s41, v1
	v_pk_fma_f32 v[150:151], v[34:35], v[164:165], v[150:151]
	v_cvt_pk_fp8_f32 v145, v68, v140 op_sel:[0,0,1]
	s_waitcnt vmcnt(35)
	v_cvt_pk_f32_fp8_e32 v[160:161], v114
	v_cvt_pk_f32_fp8_sdwa v[148:149], v114 src0_sel:WORD_1
	v_exp_f32_e32 v68, v150
	v_exp_f32_e32 v157, v151
	v_pk_fma_f32 v[162:163], v[58:59], v[178:179], v[10:11]
	v_add_f32_e32 v68, 1.0, v68
	v_rcp_f32_e32 v156, v68
	v_add_f32_e32 v68, 1.0, v157
	v_rcp_f32_e32 v157, v68
	v_cvt_pk_f32_fp8_sdwa v[152:153], v118 src0_sel:WORD_1
	v_pk_fma_f32 v[162:163], v[42:43], v[158:159], v[162:163]
	v_add_co_u32_e32 v140, vcc, s56, v70
	v_pk_fma_f32 v[162:163], v[26:27], v[160:161], v[162:163]
	v_pk_mul_f32 v[150:151], v[150:151], v[156:157]
	v_pk_mul_f32 v[150:151], v[162:163], v[150:151]
	v_pk_fma_f32 v[162:163], v[64:65], v[176:177], v[16:17]
	v_pk_fma_f32 v[162:163], v[52:53], v[154:155], v[162:163]
	v_addc_co_u32_e32 v141, vcc, 0, v71, vcc
	v_pk_fma_f32 v[162:163], v[36:37], v[152:153], v[162:163]
	global_store_dwordx2 v[140:141], v[144:145], off offset:768
	v_exp_f32_e32 v68, v162
	v_exp_f32_e32 v170, v163
	v_cvt_pk_f32_fp8_e32 v[144:145], v119
	v_add_f32_e32 v68, 1.0, v68
	v_rcp_f32_e32 v156, v68
	v_add_f32_e32 v68, 1.0, v170
	v_rcp_f32_e32 v157, v68
	v_pk_fma_f32 v[170:171], v[60:61], v[174:175], v[12:13]
	v_cvt_pk_f32_fp8_sdwa v[118:119], v119 src0_sel:WORD_1
	v_pk_fma_f32 v[170:171], v[44:45], v[146:147], v[170:171]
	v_pk_mul_f32 v[156:157], v[162:163], v[156:157]
	v_pk_fma_f32 v[170:171], v[28:29], v[148:149], v[170:171]
	v_pk_fma_f32 v[134:135], v[56:57], v[134:135], v[8:9]
	v_pk_mul_f32 v[156:157], v[170:171], v[156:157]
	v_pk_fma_f32 v[170:171], v[54:55], v[172:173], v[6:7]
	v_pk_fma_f32 v[170:171], v[38:39], v[142:143], v[170:171]
	v_pk_fma_f32 v[134:135], v[40:41], v[126:127], v[134:135]
	v_pk_fma_f32 v[170:171], v[22:23], v[144:145], v[170:171]
	v_pk_fma_f32 v[134:135], v[24:25], v[118:119], v[134:135]
	v_exp_f32_e32 v68, v170
	v_exp_f32_e32 v172, v171
	v_cvt_pk_f32_fp8_e32 v[140:141], v115
	v_add_f32_e32 v68, 1.0, v68
	v_rcp_f32_e32 v162, v68
	v_add_f32_e32 v68, 1.0, v172
	v_rcp_f32_e32 v163, v68
	v_exp_f32_e32 v68, v134
	v_pk_fma_f32 v[166:167], v[46:47], v[166:167], v[2:3]
	v_pk_mul_f32 v[162:163], v[170:171], v[162:163]
	v_exp_f32_e32 v170, v135
	v_pk_fma_f32 v[166:167], v[30:31], v[138:139], v[166:167]
	v_add_f32_e32 v68, 1.0, v68
	v_pk_fma_f32 v[166:167], v[18:19], v[140:141], v[166:167]
	v_cvt_pk_f32_fp8_sdwa v[114:115], v115 src0_sel:WORD_1
	v_pk_fma_f32 v[130:131], v[48:49], v[130:131], v[4:5]
	v_pk_mul_f32 v[162:163], v[166:167], v[162:163]
	v_rcp_f32_e32 v166, v68
	v_add_f32_e32 v68, 1.0, v170
	v_rcp_f32_e32 v167, v68
	v_pk_fma_f32 v[130:131], v[32:33], v[122:123], v[130:131]
	v_med3_f32 v68, v150, s41, v1
	v_pk_fma_f32 v[130:131], v[20:21], v[114:115], v[130:131]
	v_pk_mul_f32 v[134:135], v[134:135], v[166:167]
	s_waitcnt vmcnt(35)
; #define CV_LOAD(G_, V_, r0_) do { _Pragma("unroll") for (int i_ = 0; i_ < 8; ++i_) { G_[i_] = *(const GAS v2u*)(ap + (size_t)((r0_) + i_) * F2); V_[i_] = *(const GAS v2u*)(ap + (size_t)((r0_) + i_) * F2 + 128); } } while (0)
; __device__ __forceinline__ void conv_phase(Frame& F) {
;     ...
;         CV_LOAD(GA, VA, 0); CV_LOAD(GB, VB, 8); CV_COMP(GA, VA, 0); CV_LOAD(GA, VA, 16); CV_COMP(GB, VB, 8); CV_LOAD(GB, VB, 24); CV_COMP(GA, VA, 16); CV_COMP(GB, VB, 24);
	v_cvt_pk_f32_fp8_e32 v[166:167], v110
	v_pk_mul_f32 v[130:131], v[130:131], v[134:135]
	v_med3_f32 v135, v151, s41, v1
	v_cvt_pk_fp8_f32 v134, v68, v135
	v_med3_f32 v68, v156, s41, v1
	v_med3_f32 v151, v162, s41, v1
	v_med3_f32 v156, v163, s41, v1
	v_cvt_pk_fp8_f32 v135, v151, v156
	v_pk_fma_f32 v[168:169], v[62:63], v[168:169], v[14:15]
	v_med3_f32 v150, v157, s41, v1
	v_pk_fma_f32 v[168:169], v[50:51], v[164:165], v[168:169]
	v_cvt_pk_fp8_f32 v134, v68, v150 op_sel:[0,0,1]
	v_med3_f32 v68, v130, s41, v1
	v_med3_f32 v130, v131, s41, v1
	v_pk_fma_f32 v[168:169], v[34:35], v[166:167], v[168:169]
	v_cvt_pk_fp8_f32 v135, v68, v130 op_sel:[0,0,1]
	s_waitcnt vmcnt(34)
	v_cvt_pk_f32_fp8_e32 v[162:163], v106
	v_cvt_pk_f32_fp8_sdwa v[150:151], v106 src0_sel:WORD_1
	v_exp_f32_e32 v68, v168
	v_exp_f32_e32 v171, v169
	v_cvt_pk_f32_fp8_sdwa v[156:157], v110 src0_sel:WORD_1
	v_add_f32_e32 v68, 1.0, v68
	v_rcp_f32_e32 v170, v68
	v_add_f32_e32 v68, 1.0, v171
	v_rcp_f32_e32 v171, v68
	v_pk_fma_f32 v[154:155], v[64:65], v[154:155], v[16:17]
	v_pk_fma_f32 v[158:159], v[58:59], v[158:159], v[10:11]
	v_pk_fma_f32 v[154:155], v[52:53], v[152:153], v[154:155]
	v_pk_mul_f32 v[168:169], v[168:169], v[170:171]
	v_pk_fma_f32 v[154:155], v[36:37], v[156:157], v[154:155]
	v_add_co_u32_e32 v130, vcc, s29, v70
	v_exp_f32_e32 v68, v154
	v_exp_f32_e32 v170, v155
	v_pk_fma_f32 v[158:159], v[42:43], v[160:161], v[158:159]
	v_addc_co_u32_e32 v131, vcc, 0, v71, vcc
	v_pk_fma_f32 v[158:159], v[26:27], v[162:163], v[158:159]
	global_store_dwordx2 v[130:131], v[134:135], off offset:3584
	v_cvt_pk_f32_fp8_e32 v[134:135], v111
	v_add_f32_e32 v68, 1.0, v68
	v_pk_mul_f32 v[158:159], v[158:159], v[168:169]
	v_rcp_f32_e32 v168, v68
	v_add_f32_e32 v68, 1.0, v170
	v_rcp_f32_e32 v169, v68
	v_pk_fma_f32 v[142:143], v[54:55], v[142:143], v[6:7]
	v_pk_fma_f32 v[146:147], v[60:61], v[146:147], v[12:13]
	v_pk_fma_f32 v[142:143], v[38:39], v[144:145], v[142:143]
	v_pk_mul_f32 v[154:155], v[154:155], v[168:169]
	v_pk_fma_f32 v[142:143], v[22:23], v[134:135], v[142:143]
	v_pk_fma_f32 v[146:147], v[44:45], v[148:149], v[146:147]
	v_exp_f32_e32 v68, v142
	v_exp_f32_e32 v168, v143
	v_pk_fma_f32 v[146:147], v[28:29], v[150:151], v[146:147]
	v_cvt_pk_f32_fp8_sdwa v[110:111], v111 src0_sel:WORD_1
	v_add_f32_e32 v68, 1.0, v68
	v_pk_mul_f32 v[146:147], v[146:147], v[154:155]
	v_rcp_f32_e32 v154, v68
	v_add_f32_e32 v68, 1.0, v168
	v_rcp_f32_e32 v155, v68
	v_pk_fma_f32 v[126:127], v[56:57], v[126:127], v[8:9]
	v_cvt_pk_f32_fp8_e32 v[130:131], v107
	v_pk_fma_f32 v[126:127], v[40:41], v[118:119], v[126:127]
	v_pk_mul_f32 v[142:143], v[142:143], v[154:155]
	v_pk_fma_f32 v[126:127], v[24:25], v[110:111], v[126:127]
	v_pk_fma_f32 v[138:139], v[46:47], v[138:139], v[2:3]
	v_exp_f32_e32 v68, v126
	v_exp_f32_e32 v154, v127
	v_pk_fma_f32 v[138:139], v[30:31], v[140:141], v[138:139]
	v_add_f32_e32 v68, 1.0, v68
	v_pk_fma_f32 v[138:139], v[18:19], v[130:131], v[138:139]
	v_cvt_pk_f32_fp8_sdwa v[106:107], v107 src0_sel:WORD_1
	v_pk_fma_f32 v[122:123], v[48:49], v[122:123], v[4:5]
	v_pk_mul_f32 v[138:139], v[138:139], v[142:143]
	v_rcp_f32_e32 v142, v68
	v_add_f32_e32 v68, 1.0, v154
	v_rcp_f32_e32 v143, v68
	v_pk_fma_f32 v[122:123], v[32:33], v[114:115], v[122:123]
	v_med3_f32 v68, v158, s41, v1
	v_pk_fma_f32 v[122:123], v[20:21], v[106:107], v[122:123]
	v_pk_mul_f32 v[126:127], v[126:127], v[142:143]
	v_med3_f32 v138, v138, s41, v1
	v_pk_mul_f32 v[122:123], v[122:123], v[126:127]
	v_med3_f32 v127, v159, s41, v1
	v_cvt_pk_fp8_f32 v126, v68, v127
	v_med3_f32 v139, v139, s41, v1
	s_waitcnt vmcnt(34)
	v_cvt_pk_f32_fp8_e32 v[154:155], v102
	v_cvt_pk_fp8_f32 v127, v138, v139
	v_pk_fma_f32 v[158:159], v[62:63], v[164:165], v[14:15]
	v_med3_f32 v68, v146, s41, v1
	v_med3_f32 v142, v147, s41, v1
	v_pk_fma_f32 v[158:159], v[50:51], v[166:167], v[158:159]
	v_cvt_pk_fp8_f32 v126, v68, v142 op_sel:[0,0,1]
	v_med3_f32 v68, v122, s41, v1
	v_med3_f32 v122, v123, s41, v1
	v_pk_fma_f32 v[158:159], v[34:35], v[154:155], v[158:159]
	v_cvt_pk_fp8_f32 v127, v68, v122 op_sel:[0,0,1]
	s_waitcnt vmcnt(33)
	v_cvt_pk_f32_fp8_e32 v[146:147], v98
	v_cvt_pk_f32_fp8_sdwa v[138:139], v98 src0_sel:WORD_1
	v_exp_f32_e32 v68, v158
	v_exp_f32_e32 v165, v159
	v_cvt_pk_f32_fp8_sdwa v[142:143], v102 src0_sel:WORD_1
	v_add_f32_e32 v68, 1.0, v68
	v_rcp_f32_e32 v164, v68
	v_add_f32_e32 v68, 1.0, v165
	v_rcp_f32_e32 v165, v68
	v_pk_fma_f32 v[152:153], v[64:65], v[152:153], v[16:17]
	v_pk_fma_f32 v[160:161], v[58:59], v[160:161], v[10:11]
	v_pk_fma_f32 v[152:153], v[52:53], v[156:157], v[152:153]
	v_pk_mul_f32 v[158:159], v[158:159], v[164:165]
	v_pk_fma_f32 v[152:153], v[36:37], v[142:143], v[152:153]
	v_add_co_u32_e32 v122, vcc, s57, v70
	v_exp_f32_e32 v68, v152
	v_exp_f32_e32 v164, v153
	v_pk_fma_f32 v[160:161], v[42:43], v[162:163], v[160:161]
	v_addc_co_u32_e32 v123, vcc, 0, v71, vcc
	v_pk_fma_f32 v[160:161], v[26:27], v[146:147], v[160:161]
	global_store_dwordx2 v[122:123], v[126:127], off offset:2304
	v_cvt_pk_f32_fp8_e32 v[126:127], v103
	v_add_f32_e32 v68, 1.0, v68
	v_pk_mul_f32 v[158:159], v[160:161], v[158:159]
	v_rcp_f32_e32 v160, v68
	v_add_f32_e32 v68, 1.0, v164
	v_rcp_f32_e32 v161, v68
	v_pk_fma_f32 v[144:145], v[54:55], v[144:145], v[6:7]
	v_pk_fma_f32 v[148:149], v[60:61], v[148:149], v[12:13]
	v_pk_fma_f32 v[144:145], v[38:39], v[134:135], v[144:145]
	v_pk_mul_f32 v[152:153], v[152:153], v[160:161]
	v_pk_fma_f32 v[144:145], v[22:23], v[126:127], v[144:145]
	v_pk_fma_f32 v[148:149], v[44:45], v[150:151], v[148:149]
	v_exp_f32_e32 v68, v144
	v_exp_f32_e32 v160, v145
	v_pk_fma_f32 v[148:149], v[28:29], v[138:139], v[148:149]
	v_cvt_pk_f32_fp8_sdwa v[102:103], v103 src0_sel:WORD_1
	v_add_f32_e32 v68, 1.0, v68
	v_pk_mul_f32 v[148:149], v[148:149], v[152:153]
	v_rcp_f32_e32 v152, v68
	v_add_f32_e32 v68, 1.0, v160
	v_rcp_f32_e32 v153, v68
	v_pk_fma_f32 v[118:119], v[56:57], v[118:119], v[8:9]
	v_cvt_pk_f32_fp8_e32 v[122:123], v99
	v_pk_fma_f32 v[118:119], v[40:41], v[110:111], v[118:119]
	v_pk_mul_f32 v[144:145], v[144:145], v[152:153]
	v_pk_fma_f32 v[118:119], v[24:25], v[102:103], v[118:119]
	v_pk_fma_f32 v[140:141], v[46:47], v[140:141], v[2:3]
	v_exp_f32_e32 v68, v118
	v_exp_f32_e32 v152, v119
	v_pk_fma_f32 v[140:141], v[30:31], v[130:131], v[140:141]
	v_add_f32_e32 v68, 1.0, v68
	v_pk_fma_f32 v[140:141], v[18:19], v[122:123], v[140:141]
	v_cvt_pk_f32_fp8_sdwa v[98:99], v99 src0_sel:WORD_1
	v_pk_fma_f32 v[114:115], v[48:49], v[114:115], v[4:5]
	v_pk_mul_f32 v[140:141], v[140:141], v[144:145]
	v_rcp_f32_e32 v144, v68
	v_add_f32_e32 v68, 1.0, v152
	v_rcp_f32_e32 v145, v68
	v_pk_fma_f32 v[114:115], v[32:33], v[106:107], v[114:115]
	v_med3_f32 v68, v158, s41, v1
	v_pk_fma_f32 v[114:115], v[20:21], v[98:99], v[114:115]
	v_pk_mul_f32 v[118:119], v[118:119], v[144:145]
	v_med3_f32 v140, v140, s41, v1
	v_pk_mul_f32 v[114:115], v[114:115], v[118:119]
	v_med3_f32 v119, v159, s41, v1
	v_cvt_pk_fp8_f32 v118, v68, v119
	v_med3_f32 v141, v141, s41, v1
	s_waitcnt vmcnt(33)
; #define CV_LOAD(G_, V_, r0_) do { _Pragma("unroll") for (int i_ = 0; i_ < 8; ++i_) { G_[i_] = *(const GAS v2u*)(ap + (size_t)((r0_) + i_) * F2); V_[i_] = *(const GAS v2u*)(ap + (size_t)((r0_) + i_) * F2 + 128); } } while (0)
; __device__ __forceinline__ void conv_phase(Frame& F) {
;     ...
;         CV_LOAD(GA, VA, 0); CV_LOAD(GB, VB, 8); CV_COMP(GA, VA, 0); CV_LOAD(GA, VA, 16); CV_COMP(GB, VB, 8); CV_LOAD(GB, VB, 24); CV_COMP(GA, VA, 16); CV_COMP(GB, VB, 24);
	v_cvt_pk_f32_fp8_e32 v[174:175], v94
	v_cvt_pk_fp8_f32 v119, v140, v141
	v_pk_fma_f32 v[140:141], v[62:63], v[166:167], v[14:15]
	v_med3_f32 v68, v148, s41, v1
	v_med3_f32 v144, v149, s41, v1
	v_pk_fma_f32 v[140:141], v[50:51], v[154:155], v[140:141]
	v_cvt_pk_fp8_f32 v118, v68, v144 op_sel:[0,0,1]
	v_med3_f32 v68, v114, s41, v1
	v_med3_f32 v114, v115, s41, v1
	v_pk_fma_f32 v[140:141], v[34:35], v[174:175], v[140:141]
	v_cvt_pk_fp8_f32 v119, v68, v114 op_sel:[0,0,1]
	s_waitcnt vmcnt(32)
	v_cvt_pk_f32_fp8_e32 v[172:173], v90
	v_cvt_pk_f32_fp8_sdwa v[164:165], v90 src0_sel:WORD_1
	v_exp_f32_e32 v68, v140
	v_exp_f32_e32 v145, v141
	v_pk_fma_f32 v[148:149], v[58:59], v[162:163], v[10:11]
	v_add_f32_e32 v68, 1.0, v68
	v_rcp_f32_e32 v144, v68
	v_add_f32_e32 v68, 1.0, v145
	v_rcp_f32_e32 v145, v68
	v_cvt_pk_f32_fp8_sdwa v[170:171], v94 src0_sel:WORD_1
	v_pk_fma_f32 v[148:149], v[42:43], v[146:147], v[148:149]
	v_add_co_u32_e32 v114, vcc, s30, v70
	v_pk_fma_f32 v[148:149], v[26:27], v[172:173], v[148:149]
	v_pk_mul_f32 v[140:141], v[140:141], v[144:145]
	v_pk_mul_f32 v[140:141], v[148:149], v[140:141]
	v_pk_fma_f32 v[148:149], v[64:65], v[156:157], v[16:17]
	v_addc_co_u32_e32 v115, vcc, 0, v71, vcc
	v_pk_fma_f32 v[148:149], v[52:53], v[142:143], v[148:149]
	global_store_dwordx2 v[114:115], v[118:119], off offset:1024
	v_pk_fma_f32 v[148:149], v[36:37], v[170:171], v[148:149]
	v_cvt_pk_f32_fp8_e32 v[118:119], v95
	v_exp_f32_e32 v68, v148
	v_exp_f32_e32 v152, v149
	v_add_f32_e32 v68, 1.0, v68
	v_rcp_f32_e32 v144, v68
	v_add_f32_e32 v68, 1.0, v152
	v_rcp_f32_e32 v145, v68
	v_pk_fma_f32 v[134:135], v[54:55], v[134:135], v[6:7]
	v_pk_fma_f32 v[150:151], v[60:61], v[150:151], v[12:13]
	v_pk_fma_f32 v[134:135], v[38:39], v[126:127], v[134:135]
	v_pk_fma_f32 v[150:151], v[44:45], v[138:139], v[150:151]
	v_pk_fma_f32 v[134:135], v[22:23], v[118:119], v[134:135]
	v_pk_fma_f32 v[150:151], v[28:29], v[164:165], v[150:151]
	v_pk_mul_f32 v[144:145], v[148:149], v[144:145]
	v_pk_mul_f32 v[144:145], v[150:151], v[144:145]
	v_exp_f32_e32 v68, v134
	v_exp_f32_e32 v150, v135
	v_cvt_pk_f32_fp8_sdwa v[94:95], v95 src0_sel:WORD_1
	v_add_f32_e32 v68, 1.0, v68
	v_rcp_f32_e32 v148, v68
	v_add_f32_e32 v68, 1.0, v150
	v_rcp_f32_e32 v149, v68
	v_pk_fma_f32 v[110:111], v[56:57], v[110:111], v[8:9]
	v_cvt_pk_f32_fp8_e32 v[114:115], v91
	v_pk_fma_f32 v[110:111], v[40:41], v[102:103], v[110:111]
	v_pk_mul_f32 v[134:135], v[134:135], v[148:149]
	v_pk_fma_f32 v[110:111], v[24:25], v[94:95], v[110:111]
	v_pk_fma_f32 v[130:131], v[46:47], v[130:131], v[2:3]
	v_exp_f32_e32 v68, v110
	v_exp_f32_e32 v148, v111
	v_pk_fma_f32 v[130:131], v[30:31], v[122:123], v[130:131]
	v_add_f32_e32 v68, 1.0, v68
	v_pk_fma_f32 v[130:131], v[18:19], v[114:115], v[130:131]
	v_cvt_pk_f32_fp8_sdwa v[90:91], v91 src0_sel:WORD_1
	v_pk_fma_f32 v[106:107], v[48:49], v[106:107], v[4:5]
	v_pk_mul_f32 v[130:131], v[130:131], v[134:135]
	v_rcp_f32_e32 v134, v68
	v_add_f32_e32 v68, 1.0, v148
	v_rcp_f32_e32 v135, v68
	v_pk_fma_f32 v[106:107], v[32:33], v[98:99], v[106:107]
	v_med3_f32 v68, v140, s41, v1
	v_pk_fma_f32 v[106:107], v[20:21], v[90:91], v[106:107]
	v_pk_mul_f32 v[110:111], v[110:111], v[134:135]
	v_med3_f32 v130, v130, s41, v1
	v_pk_mul_f32 v[106:107], v[106:107], v[110:111]
	v_med3_f32 v111, v141, s41, v1
	v_cvt_pk_fp8_f32 v110, v68, v111
	v_med3_f32 v131, v131, s41, v1
	v_cvt_pk_fp8_f32 v111, v130, v131
	s_waitcnt vmcnt(32)
	v_cvt_pk_f32_fp8_e32 v[166:167], v86
	v_med3_f32 v68, v144, s41, v1
	v_med3_f32 v134, v145, s41, v1
	v_cvt_pk_fp8_f32 v110, v68, v134 op_sel:[0,0,1]
	v_med3_f32 v68, v106, s41, v1
	v_med3_f32 v106, v107, s41, v1
	v_cvt_pk_f32_fp8_sdwa v[156:157], v86 src0_sel:WORD_1
	v_cvt_pk_f32_fp8_e32 v[148:149], v87
	v_cvt_pk_f32_fp8_sdwa v[134:135], v87 src0_sel:WORD_1
	v_pk_fma_f32 v[86:87], v[62:63], v[154:155], v[14:15]
	v_cvt_pk_fp8_f32 v111, v68, v106 op_sel:[0,0,1]
	v_pk_fma_f32 v[86:87], v[50:51], v[174:175], v[86:87]
	v_add_co_u32_e32 v106, vcc, s58, v70
	v_pk_fma_f32 v[86:87], v[34:35], v[166:167], v[86:87]
	s_nop 0
	v_addc_co_u32_e32 v107, vcc, 0, v71, vcc
	s_waitcnt vmcnt(31)
	v_cvt_pk_f32_fp8_e32 v[160:161], v82
	v_cvt_pk_f32_fp8_sdwa v[152:153], v82 src0_sel:WORD_1
	v_exp_f32_e32 v68, v86
	global_store_dwordx2 v[106:107], v[110:111], off offset:3840
	v_exp_f32_e32 v106, v87
	v_add_f32_e32 v68, 1.0, v68
	v_rcp_f32_e32 v82, v68
	v_cvt_pk_f32_fp8_e32 v[144:145], v83
	v_add_f32_e32 v68, 1.0, v106
	v_cvt_pk_f32_fp8_sdwa v[140:141], v83 src0_sel:WORD_1
	v_rcp_f32_e32 v83, v68
	v_pk_fma_f32 v[106:107], v[58:59], v[146:147], v[10:11]
	v_pk_fma_f32 v[102:103], v[56:57], v[102:103], v[8:9]
	v_pk_fma_f32 v[106:107], v[42:43], v[172:173], v[106:107]
	v_pk_mul_f32 v[82:83], v[86:87], v[82:83]
	v_pk_fma_f32 v[106:107], v[26:27], v[160:161], v[106:107]
	v_pk_fma_f32 v[122:123], v[46:47], v[122:123], v[2:3]
	v_pk_mul_f32 v[82:83], v[106:107], v[82:83]
	v_pk_fma_f32 v[106:107], v[64:65], v[142:143], v[16:17]
	v_pk_fma_f32 v[106:107], v[52:53], v[170:171], v[106:107]
	v_pk_fma_f32 v[102:103], v[40:41], v[94:95], v[102:103]
	v_pk_fma_f32 v[106:107], v[36:37], v[156:157], v[106:107]
	v_pk_fma_f32 v[122:123], v[30:31], v[114:115], v[122:123]
	v_exp_f32_e32 v68, v106
	v_exp_f32_e32 v110, v107
	v_pk_fma_f32 v[102:103], v[24:25], v[134:135], v[102:103]
	v_add_f32_e32 v68, 1.0, v68
	v_rcp_f32_e32 v86, v68
	v_add_f32_e32 v68, 1.0, v110
	v_rcp_f32_e32 v87, v68
	v_pk_fma_f32 v[110:111], v[60:61], v[138:139], v[12:13]
	v_pk_fma_f32 v[122:123], v[18:19], v[144:145], v[122:123]
	v_pk_fma_f32 v[110:111], v[44:45], v[164:165], v[110:111]
	v_pk_mul_f32 v[86:87], v[106:107], v[86:87]
	v_pk_fma_f32 v[110:111], v[28:29], v[152:153], v[110:111]
	v_pk_fma_f32 v[98:99], v[48:49], v[98:99], v[4:5]
	v_pk_mul_f32 v[86:87], v[110:111], v[86:87]
	v_pk_fma_f32 v[110:111], v[54:55], v[126:127], v[6:7]
	v_pk_fma_f32 v[110:111], v[38:39], v[118:119], v[110:111]
	v_pk_fma_f32 v[98:99], v[32:33], v[90:91], v[98:99]
	v_pk_fma_f32 v[110:111], v[22:23], v[148:149], v[110:111]
	v_pk_fma_f32 v[98:99], v[20:21], v[140:141], v[98:99]
	v_exp_f32_e32 v68, v110
	v_exp_f32_e32 v126, v111
	v_add_f32_e32 v68, 1.0, v68
	v_rcp_f32_e32 v106, v68
	v_add_f32_e32 v68, 1.0, v126
	v_rcp_f32_e32 v107, v68
	v_exp_f32_e32 v68, v102
	v_med3_f32 v83, v83, s41, v1
	v_pk_mul_f32 v[106:107], v[110:111], v[106:107]
	v_pk_mul_f32 v[106:107], v[122:123], v[106:107]
	v_exp_f32_e32 v122, v103
	v_add_f32_e32 v68, 1.0, v68
	v_rcp_f32_e32 v110, v68
	v_add_f32_e32 v68, 1.0, v122
	v_rcp_f32_e32 v111, v68
	v_med3_f32 v68, v82, s41, v1
	v_cvt_pk_fp8_f32 v82, v68, v83
	v_pk_mul_f32 v[102:103], v[102:103], v[110:111]
	v_med3_f32 v68, v86, s41, v1
	v_pk_mul_f32 v[98:99], v[98:99], v[102:103]
	v_med3_f32 v86, v87, s41, v1
	v_med3_f32 v87, v106, s41, v1
	v_med3_f32 v102, v107, s41, v1
	v_cvt_pk_fp8_f32 v83, v87, v102
	s_waitcnt vmcnt(31)
; #define CV_LOAD(G_, V_, r0_) do { _Pragma("unroll") for (int i_ = 0; i_ < 8; ++i_) { G_[i_] = *(const GAS v2u*)(ap + (size_t)((r0_) + i_) * F2); V_[i_] = *(const GAS v2u*)(ap + (size_t)((r0_) + i_) * F2 + 128); } } while (0)
; __device__ __forceinline__ void conv_phase(Frame& F) {
;     ...
;         CV_LOAD(GA, VA, 0); CV_LOAD(GB, VB, 8); CV_COMP(GA, VA, 0); CV_LOAD(GA, VA, 16); CV_COMP(GB, VB, 8); CV_LOAD(GB, VB, 24); CV_COMP(GA, VA, 16); CV_COMP(GB, VB, 24);
	v_cvt_pk_f32_fp8_e32 v[168:169], v78
	v_cvt_pk_fp8_f32 v82, v68, v86 op_sel:[0,0,1]
	v_med3_f32 v68, v98, s41, v1
	v_med3_f32 v86, v99, s41, v1
	v_cvt_pk_f32_fp8_sdwa v[158:159], v78 src0_sel:WORD_1
	v_cvt_pk_f32_fp8_e32 v[150:151], v79
	v_cvt_pk_f32_fp8_sdwa v[138:139], v79 src0_sel:WORD_1
	v_pk_fma_f32 v[78:79], v[62:63], v[174:175], v[14:15]
	v_cvt_pk_fp8_f32 v83, v68, v86 op_sel:[0,0,1]
	v_pk_fma_f32 v[78:79], v[50:51], v[166:167], v[78:79]
	v_add_co_u32_e32 v86, vcc, s31, v70
	v_pk_fma_f32 v[78:79], v[34:35], v[168:169], v[78:79]
	s_nop 0
	v_addc_co_u32_e32 v87, vcc, 0, v71, vcc
	s_waitcnt vmcnt(30)
	v_cvt_pk_f32_fp8_e32 v[162:163], v74
	v_cvt_pk_f32_fp8_sdwa v[154:155], v74 src0_sel:WORD_1
	v_exp_f32_e32 v68, v78
	global_store_dwordx2 v[86:87], v[82:83], off offset:2560
	v_exp_f32_e32 v82, v79
	v_add_f32_e32 v68, 1.0, v68
	v_rcp_f32_e32 v74, v68
	v_cvt_pk_f32_fp8_e32 v[146:147], v75
	v_add_f32_e32 v68, 1.0, v82
	v_cvt_pk_f32_fp8_sdwa v[142:143], v75 src0_sel:WORD_1
	v_rcp_f32_e32 v75, v68
	v_pk_fma_f32 v[82:83], v[58:59], v[172:173], v[10:11]
	v_pk_fma_f32 v[94:95], v[56:57], v[94:95], v[8:9]
	v_pk_fma_f32 v[82:83], v[42:43], v[160:161], v[82:83]
	v_pk_mul_f32 v[74:75], v[78:79], v[74:75]
	v_pk_fma_f32 v[82:83], v[26:27], v[162:163], v[82:83]
	v_pk_fma_f32 v[94:95], v[40:41], v[134:135], v[94:95]
	v_pk_mul_f32 v[74:75], v[82:83], v[74:75]
	v_pk_fma_f32 v[82:83], v[64:65], v[170:171], v[16:17]
	v_pk_fma_f32 v[82:83], v[52:53], v[156:157], v[82:83]
	v_pk_fma_f32 v[94:95], v[24:25], v[138:139], v[94:95]
	v_pk_fma_f32 v[82:83], v[36:37], v[158:159], v[82:83]
	v_pk_fma_f32 v[90:91], v[48:49], v[90:91], v[4:5]
	v_exp_f32_e32 v68, v82
	v_exp_f32_e32 v86, v83
	v_med3_f32 v75, v75, s41, v1
	v_add_f32_e32 v68, 1.0, v68
	v_rcp_f32_e32 v78, v68
	v_add_f32_e32 v68, 1.0, v86
	v_rcp_f32_e32 v79, v68
	v_pk_fma_f32 v[86:87], v[60:61], v[164:165], v[12:13]
	v_pk_fma_f32 v[90:91], v[32:33], v[140:141], v[90:91]
	v_pk_fma_f32 v[86:87], v[44:45], v[152:153], v[86:87]
	v_pk_mul_f32 v[78:79], v[82:83], v[78:79]
	v_pk_fma_f32 v[86:87], v[28:29], v[154:155], v[86:87]
	s_waitcnt vmcnt(22)
	v_cvt_pk_f32_fp8_e32 v[178:179], v136
	v_pk_mul_f32 v[78:79], v[86:87], v[78:79]
	v_pk_fma_f32 v[86:87], v[54:55], v[118:119], v[6:7]
	v_pk_fma_f32 v[86:87], v[38:39], v[148:149], v[86:87]
	v_pk_fma_f32 v[90:91], v[20:21], v[142:143], v[90:91]
	v_pk_fma_f32 v[86:87], v[22:23], v[150:151], v[86:87]
	v_exp_f32_e32 v68, v86
	v_exp_f32_e32 v98, v87
	v_pk_fma_f32 v[166:167], v[62:63], v[166:167], v[14:15]
	v_add_f32_e32 v68, 1.0, v68
	v_rcp_f32_e32 v82, v68
	v_add_f32_e32 v68, 1.0, v98
	v_rcp_f32_e32 v83, v68
	v_pk_fma_f32 v[98:99], v[46:47], v[114:115], v[2:3]
	v_pk_fma_f32 v[98:99], v[30:31], v[144:145], v[98:99]
	v_pk_mul_f32 v[82:83], v[86:87], v[82:83]
	v_pk_fma_f32 v[98:99], v[18:19], v[146:147], v[98:99]
	v_exp_f32_e32 v68, v94
	v_pk_mul_f32 v[82:83], v[98:99], v[82:83]
	v_exp_f32_e32 v98, v95
	v_add_f32_e32 v68, 1.0, v68
	v_rcp_f32_e32 v86, v68
	v_add_f32_e32 v68, 1.0, v98
	v_rcp_f32_e32 v87, v68
	v_med3_f32 v68, v74, s41, v1
	v_cvt_pk_fp8_f32 v74, v68, v75
	v_med3_f32 v68, v78, s41, v1
	v_med3_f32 v78, v79, s41, v1
	v_med3_f32 v79, v82, s41, v1
	v_med3_f32 v82, v83, s41, v1
	v_cvt_pk_fp8_f32 v75, v79, v82
	v_pk_mul_f32 v[86:87], v[94:95], v[86:87]
	v_pk_fma_f32 v[166:167], v[50:51], v[168:169], v[166:167]
	v_pk_mul_f32 v[86:87], v[90:91], v[86:87]
	v_cvt_pk_fp8_f32 v74, v68, v78 op_sel:[0,0,1]
	v_med3_f32 v68, v86, s41, v1
	v_med3_f32 v78, v87, s41, v1
	v_pk_fma_f32 v[166:167], v[34:35], v[178:179], v[166:167]
	v_cvt_pk_fp8_f32 v75, v68, v78 op_sel:[0,0,1]
	s_waitcnt vmcnt(21)
	v_cvt_pk_f32_fp8_e32 v[176:177], v132
	v_cvt_pk_f32_fp8_sdwa v[172:173], v132 src0_sel:WORD_1
	v_exp_f32_e32 v68, v166
	v_exp_f32_e32 v181, v167
	v_cvt_pk_f32_fp8_sdwa v[174:175], v136 src0_sel:WORD_1
	v_add_f32_e32 v68, 1.0, v68
	v_rcp_f32_e32 v180, v68
	v_add_f32_e32 v68, 1.0, v181
	v_rcp_f32_e32 v181, v68
	v_pk_fma_f32 v[156:157], v[64:65], v[156:157], v[16:17]
	v_pk_fma_f32 v[160:161], v[58:59], v[160:161], v[10:11]
	v_pk_fma_f32 v[156:157], v[52:53], v[158:159], v[156:157]
	v_pk_mul_f32 v[166:167], v[166:167], v[180:181]
	v_pk_fma_f32 v[156:157], v[36:37], v[174:175], v[156:157]
	v_pk_fma_f32 v[160:161], v[42:43], v[162:163], v[160:161]
	v_exp_f32_e32 v68, v156
	v_exp_f32_e32 v180, v157
	v_pk_fma_f32 v[160:161], v[26:27], v[176:177], v[160:161]
	v_cvt_pk_f32_fp8_e32 v[170:171], v137
	v_add_f32_e32 v68, 1.0, v68
	v_pk_mul_f32 v[160:161], v[160:161], v[166:167]
	v_rcp_f32_e32 v166, v68
	v_add_f32_e32 v68, 1.0, v180
	v_rcp_f32_e32 v167, v68
	v_pk_fma_f32 v[148:149], v[54:55], v[148:149], v[6:7]
	v_pk_fma_f32 v[152:153], v[60:61], v[152:153], v[12:13]
	v_pk_fma_f32 v[148:149], v[38:39], v[150:151], v[148:149]
	v_pk_mul_f32 v[156:157], v[156:157], v[166:167]
	v_pk_fma_f32 v[148:149], v[22:23], v[170:171], v[148:149]
	v_pk_fma_f32 v[152:153], v[44:45], v[154:155], v[152:153]
	v_exp_f32_e32 v68, v148
	v_exp_f32_e32 v166, v149
	v_pk_fma_f32 v[152:153], v[28:29], v[172:173], v[152:153]
	v_cvt_pk_f32_fp8_sdwa v[136:137], v137 src0_sel:WORD_1
	v_add_f32_e32 v68, 1.0, v68
	v_pk_mul_f32 v[152:153], v[152:153], v[156:157]
	v_rcp_f32_e32 v156, v68
	v_add_f32_e32 v68, 1.0, v166
	v_rcp_f32_e32 v157, v68
	v_pk_fma_f32 v[134:135], v[56:57], v[134:135], v[8:9]
	v_cvt_pk_f32_fp8_e32 v[164:165], v133
	v_pk_fma_f32 v[134:135], v[40:41], v[138:139], v[134:135]
	v_pk_mul_f32 v[148:149], v[148:149], v[156:157]
	v_pk_fma_f32 v[134:135], v[24:25], v[136:137], v[134:135]
	v_pk_fma_f32 v[144:145], v[46:47], v[144:145], v[2:3]
	v_exp_f32_e32 v68, v134
	v_exp_f32_e32 v156, v135
	v_pk_fma_f32 v[144:145], v[30:31], v[146:147], v[144:145]
	v_add_f32_e32 v68, 1.0, v68
	v_pk_fma_f32 v[144:145], v[18:19], v[164:165], v[144:145]
	v_cvt_pk_f32_fp8_sdwa v[132:133], v133 src0_sel:WORD_1
	v_pk_fma_f32 v[140:141], v[48:49], v[140:141], v[4:5]
	v_pk_mul_f32 v[144:145], v[144:145], v[148:149]
	v_rcp_f32_e32 v148, v68
	v_add_f32_e32 v68, 1.0, v156
	v_rcp_f32_e32 v149, v68
	v_pk_fma_f32 v[140:141], v[32:33], v[142:143], v[140:141]
	v_med3_f32 v68, v160, s41, v1
	v_pk_fma_f32 v[140:141], v[20:21], v[132:133], v[140:141]
	v_pk_mul_f32 v[134:135], v[134:135], v[148:149]
	v_add_co_u32_e32 v78, vcc, s59, v70
	v_pk_mul_f32 v[134:135], v[140:141], v[134:135]
	v_med3_f32 v141, v161, s41, v1
	v_cvt_pk_fp8_f32 v140, v68, v141
	v_med3_f32 v144, v144, s41, v1
	v_med3_f32 v145, v145, s41, v1
	s_waitcnt vmcnt(20)
; #define CV_LOAD(G_, V_, r0_) do { _Pragma("unroll") for (int i_ = 0; i_ < 8; ++i_) { G_[i_] = *(const GAS v2u*)(ap + (size_t)((r0_) + i_) * F2); V_[i_] = *(const GAS v2u*)(ap + (size_t)((r0_) + i_) * F2 + 128); } } while (0)
; __device__ __forceinline__ void conv_phase(Frame& F) {
;     ...
;         CV_LOAD(GA, VA, 0); CV_LOAD(GB, VB, 8); CV_COMP(GA, VA, 0); CV_LOAD(GA, VA, 16); CV_COMP(GB, VB, 8); CV_LOAD(GB, VB, 24); CV_COMP(GA, VA, 16); CV_COMP(GB, VB, 24);
	v_cvt_pk_f32_fp8_e32 v[166:167], v128
	v_addc_co_u32_e32 v79, vcc, 0, v71, vcc
	v_med3_f32 v68, v152, s41, v1
	v_med3_f32 v148, v153, s41, v1
	v_cvt_pk_fp8_f32 v141, v144, v145
	global_store_dwordx2 v[78:79], v[74:75], off offset:1280
	v_add_co_u32_e32 v74, vcc, s60, v72
	v_cvt_pk_fp8_f32 v140, v68, v148 op_sel:[0,0,1]
	v_pk_fma_f32 v[148:149], v[62:63], v[168:169], v[14:15]
	v_addc_co_u32_e32 v75, vcc, 0, v73, vcc
	v_pk_fma_f32 v[148:149], v[50:51], v[178:179], v[148:149]
	v_add_co_u32_e32 v78, vcc, s61, v72
	v_med3_f32 v68, v134, s41, v1
	v_med3_f32 v134, v135, s41, v1
	v_pk_fma_f32 v[148:149], v[34:35], v[166:167], v[148:149]
	v_addc_co_u32_e32 v79, vcc, 0, v73, vcc
	v_cvt_pk_fp8_f32 v141, v68, v134 op_sel:[0,0,1]
	global_load_dwordx2 v[130:131], v[74:75], off nt
	global_load_dwordx2 v[126:127], v[74:75], off offset:128 nt
	global_load_dwordx2 v[122:123], v[78:79], off offset:1536 nt
	global_load_dwordx2 v[118:119], v[78:79], off offset:1664 nt
	v_add_co_u32_e32 v74, vcc, s62, v72
	s_waitcnt vmcnt(24)
	v_cvt_pk_f32_fp8_e32 v[156:157], v124
	v_cvt_pk_f32_fp8_sdwa v[144:145], v124 src0_sel:WORD_1
	v_exp_f32_e32 v68, v148
	v_addc_co_u32_e32 v75, vcc, 0, v73, vcc
	v_exp_f32_e32 v161, v149
	v_add_co_u32_e32 v78, vcc, s63, v72
	v_cvt_pk_f32_fp8_sdwa v[152:153], v128 src0_sel:WORD_1
	s_nop 0
	v_addc_co_u32_e32 v79, vcc, 0, v73, vcc
	global_load_dwordx2 v[114:115], v[74:75], off offset:3072 nt
	global_load_dwordx2 v[110:111], v[74:75], off offset:3200 nt
	global_load_dwordx2 v[106:107], v[78:79], off offset:512 nt
	global_load_dwordx2 v[102:103], v[78:79], off offset:640 nt
	v_add_co_u32_e32 v74, vcc, s64, v72
	v_add_f32_e32 v68, 1.0, v68
	s_nop 0
	v_addc_co_u32_e32 v75, vcc, 0, v73, vcc
	v_rcp_f32_e32 v160, v68
	v_add_f32_e32 v68, 1.0, v161
	v_add_co_u32_e32 v78, vcc, s65, v72
	v_rcp_f32_e32 v161, v68
	v_pk_fma_f32 v[158:159], v[64:65], v[158:159], v[16:17]
	v_addc_co_u32_e32 v79, vcc, 0, v73, vcc
	v_pk_fma_f32 v[162:163], v[58:59], v[162:163], v[10:11]
	v_pk_fma_f32 v[158:159], v[52:53], v[174:175], v[158:159]
	global_load_dwordx2 v[98:99], v[74:75], off offset:2048 nt
	global_load_dwordx2 v[94:95], v[74:75], off offset:2176 nt
	global_load_dwordx2 v[90:91], v[78:79], off offset:3584 nt
	global_load_dwordx2 v[86:87], v[78:79], off offset:3712 nt
	v_add_co_u32_e32 v74, vcc, s66, v72
	v_pk_fma_f32 v[162:163], v[42:43], v[176:177], v[162:163]
	v_pk_fma_f32 v[158:159], v[36:37], v[152:153], v[158:159]
	v_addc_co_u32_e32 v75, vcc, 0, v73, vcc
	v_pk_fma_f32 v[162:163], v[26:27], v[156:157], v[162:163]
	v_add_co_u32_e32 v72, vcc, s67, v72
	v_pk_mul_f32 v[148:149], v[148:149], v[160:161]
	v_pk_mul_f32 v[148:149], v[162:163], v[148:149]
	v_exp_f32_e32 v68, v158
	v_addc_co_u32_e32 v73, vcc, 0, v73, vcc
	v_exp_f32_e32 v162, v159
	v_add_co_u32_e32 v134, vcc, s33, v70
	global_load_dwordx2 v[82:83], v[74:75], off offset:1024 nt
	global_load_dwordx2 v[78:79], v[74:75], off offset:1152 nt
	s_nop 0
	global_load_dwordx2 v[74:75], v[72:73], off offset:2560 nt
	s_nop 0
	global_load_dwordx2 v[72:73], v[72:73], off offset:2688 nt
	v_addc_co_u32_e32 v135, vcc, 0, v71, vcc
	global_store_dwordx2 v[134:135], v[140:141], off
	v_cvt_pk_f32_fp8_e32 v[140:141], v129
	v_add_f32_e32 v68, 1.0, v68
	v_rcp_f32_e32 v160, v68
	v_add_f32_e32 v68, 1.0, v162
	v_rcp_f32_e32 v161, v68
	v_pk_fma_f32 v[150:151], v[54:55], v[150:151], v[6:7]
	v_pk_fma_f32 v[154:155], v[60:61], v[154:155], v[12:13]
	v_pk_fma_f32 v[150:151], v[38:39], v[170:171], v[150:151]
	v_pk_mul_f32 v[158:159], v[158:159], v[160:161]
	v_pk_fma_f32 v[150:151], v[22:23], v[140:141], v[150:151]
	v_pk_fma_f32 v[154:155], v[44:45], v[172:173], v[154:155]
	v_exp_f32_e32 v68, v150
	v_exp_f32_e32 v160, v151
	v_pk_fma_f32 v[154:155], v[28:29], v[144:145], v[154:155]
	v_cvt_pk_f32_fp8_sdwa v[128:129], v129 src0_sel:WORD_1
	v_add_f32_e32 v68, 1.0, v68
	v_pk_mul_f32 v[154:155], v[154:155], v[158:159]
	v_rcp_f32_e32 v158, v68
	v_add_f32_e32 v68, 1.0, v160
	v_rcp_f32_e32 v159, v68
	v_pk_fma_f32 v[138:139], v[56:57], v[138:139], v[8:9]
	v_cvt_pk_f32_fp8_e32 v[134:135], v125
	v_pk_fma_f32 v[138:139], v[40:41], v[136:137], v[138:139]
	v_pk_mul_f32 v[150:151], v[150:151], v[158:159]
	v_pk_fma_f32 v[138:139], v[24:25], v[128:129], v[138:139]
	v_pk_fma_f32 v[146:147], v[46:47], v[146:147], v[2:3]
	v_exp_f32_e32 v68, v138
	v_exp_f32_e32 v158, v139
	v_pk_fma_f32 v[146:147], v[30:31], v[164:165], v[146:147]
	v_add_f32_e32 v68, 1.0, v68
	v_pk_fma_f32 v[146:147], v[18:19], v[134:135], v[146:147]
	v_cvt_pk_f32_fp8_sdwa v[124:125], v125 src0_sel:WORD_1
	v_pk_fma_f32 v[142:143], v[48:49], v[142:143], v[4:5]
	v_pk_mul_f32 v[146:147], v[146:147], v[150:151]
	v_rcp_f32_e32 v150, v68
	v_add_f32_e32 v68, 1.0, v158
	v_rcp_f32_e32 v151, v68
	v_pk_fma_f32 v[142:143], v[32:33], v[132:133], v[142:143]
	v_med3_f32 v68, v148, s41, v1
	v_pk_fma_f32 v[142:143], v[20:21], v[124:125], v[142:143]
	v_pk_mul_f32 v[138:139], v[138:139], v[150:151]
	v_med3_f32 v146, v146, s41, v1
	v_pk_mul_f32 v[138:139], v[142:143], v[138:139]
	v_med3_f32 v143, v149, s41, v1
	v_cvt_pk_fp8_f32 v142, v68, v143
	v_med3_f32 v147, v147, s41, v1
	s_waitcnt vmcnt(36)
	v_cvt_pk_f32_fp8_e32 v[162:163], v120
	v_med3_f32 v68, v154, s41, v1
	v_med3_f32 v148, v155, s41, v1
	v_cvt_pk_fp8_f32 v143, v146, v147
	v_cvt_pk_fp8_f32 v142, v68, v148 op_sel:[0,0,1]
	v_pk_fma_f32 v[148:149], v[62:63], v[178:179], v[14:15]
	v_med3_f32 v68, v138, s41, v1
	v_pk_fma_f32 v[148:149], v[50:51], v[166:167], v[148:149]
	v_med3_f32 v138, v139, s41, v1
	v_pk_fma_f32 v[148:149], v[34:35], v[162:163], v[148:149]
	v_cvt_pk_fp8_f32 v143, v68, v138 op_sel:[0,0,1]
	s_waitcnt vmcnt(35)
; #define CV_LOAD(G_, V_, r0_) do { _Pragma("unroll") for (int i_ = 0; i_ < 8; ++i_) { G_[i_] = *(const GAS v2u*)(ap + (size_t)((r0_) + i_) * F2); V_[i_] = *(const GAS v2u*)(ap + (size_t)((r0_) + i_) * F2 + 128); } } while (0)
; __device__ __forceinline__ void conv_phase(Frame& F) {
;     ...
;         CV_LOAD(GA, VA, 0); CV_LOAD(GB, VB, 8); CV_COMP(GA, VA, 0); CV_LOAD(GA, VA, 16); CV_COMP(GB, VB, 8); CV_LOAD(GB, VB, 24); CV_COMP(GA, VA, 16); CV_COMP(GB, VB, 24);
	v_cvt_pk_f32_fp8_e32 v[158:159], v116
	v_cvt_pk_f32_fp8_sdwa v[146:147], v116 src0_sel:WORD_1
	v_exp_f32_e32 v68, v148
	v_exp_f32_e32 v155, v149
	v_pk_fma_f32 v[160:161], v[58:59], v[176:177], v[10:11]
	v_add_f32_e32 v68, 1.0, v68
	v_rcp_f32_e32 v154, v68
	v_add_f32_e32 v68, 1.0, v155
	v_rcp_f32_e32 v155, v68
	v_cvt_pk_f32_fp8_sdwa v[150:151], v120 src0_sel:WORD_1
	v_pk_fma_f32 v[160:161], v[42:43], v[156:157], v[160:161]
	v_add_co_u32_e32 v138, vcc, s68, v70
	v_pk_fma_f32 v[160:161], v[26:27], v[158:159], v[160:161]
	v_pk_mul_f32 v[148:149], v[148:149], v[154:155]
	v_pk_mul_f32 v[148:149], v[160:161], v[148:149]
	v_pk_fma_f32 v[160:161], v[64:65], v[174:175], v[16:17]
	v_pk_fma_f32 v[160:161], v[52:53], v[152:153], v[160:161]
	v_addc_co_u32_e32 v139, vcc, 0, v71, vcc
	v_pk_fma_f32 v[160:161], v[36:37], v[150:151], v[160:161]
	global_store_dwordx2 v[138:139], v[142:143], off offset:2816
	v_exp_f32_e32 v68, v160
	v_exp_f32_e32 v168, v161
	v_cvt_pk_f32_fp8_e32 v[142:143], v121
	v_add_f32_e32 v68, 1.0, v68
	v_rcp_f32_e32 v154, v68
	v_add_f32_e32 v68, 1.0, v168
	v_rcp_f32_e32 v155, v68
	v_pk_fma_f32 v[168:169], v[60:61], v[172:173], v[12:13]
	v_cvt_pk_f32_fp8_sdwa v[120:121], v121 src0_sel:WORD_1
	v_pk_fma_f32 v[168:169], v[44:45], v[144:145], v[168:169]
	v_pk_mul_f32 v[154:155], v[160:161], v[154:155]
	v_pk_fma_f32 v[168:169], v[28:29], v[146:147], v[168:169]
	v_pk_fma_f32 v[136:137], v[56:57], v[136:137], v[8:9]
	v_pk_mul_f32 v[154:155], v[168:169], v[154:155]
	v_pk_fma_f32 v[168:169], v[54:55], v[170:171], v[6:7]
	v_pk_fma_f32 v[168:169], v[38:39], v[140:141], v[168:169]
	v_pk_fma_f32 v[136:137], v[40:41], v[128:129], v[136:137]
	v_pk_fma_f32 v[168:169], v[22:23], v[142:143], v[168:169]
	v_pk_fma_f32 v[136:137], v[24:25], v[120:121], v[136:137]
	v_exp_f32_e32 v68, v168
	v_exp_f32_e32 v170, v169
	v_cvt_pk_f32_fp8_e32 v[138:139], v117
	v_add_f32_e32 v68, 1.0, v68
	v_rcp_f32_e32 v160, v68
	v_add_f32_e32 v68, 1.0, v170
	v_rcp_f32_e32 v161, v68
	v_exp_f32_e32 v68, v136
	v_pk_fma_f32 v[164:165], v[46:47], v[164:165], v[2:3]
	v_pk_mul_f32 v[160:161], v[168:169], v[160:161]
	v_exp_f32_e32 v168, v137
	v_pk_fma_f32 v[164:165], v[30:31], v[134:135], v[164:165]
	v_add_f32_e32 v68, 1.0, v68
	v_pk_fma_f32 v[164:165], v[18:19], v[138:139], v[164:165]
	v_cvt_pk_f32_fp8_sdwa v[116:117], v117 src0_sel:WORD_1
	v_pk_fma_f32 v[132:133], v[48:49], v[132:133], v[4:5]
	v_pk_mul_f32 v[160:161], v[164:165], v[160:161]
	v_rcp_f32_e32 v164, v68
	v_add_f32_e32 v68, 1.0, v168
	v_rcp_f32_e32 v165, v68
	v_pk_fma_f32 v[132:133], v[32:33], v[124:125], v[132:133]
	v_med3_f32 v68, v148, s41, v1
	v_pk_fma_f32 v[132:133], v[20:21], v[116:117], v[132:133]
	v_pk_mul_f32 v[136:137], v[136:137], v[164:165]
	s_waitcnt vmcnt(35)
	v_cvt_pk_f32_fp8_e32 v[164:165], v112
	v_pk_mul_f32 v[132:133], v[132:133], v[136:137]
	v_med3_f32 v137, v149, s41, v1
	v_cvt_pk_fp8_f32 v136, v68, v137
	v_med3_f32 v68, v154, s41, v1
	v_med3_f32 v149, v160, s41, v1
	v_med3_f32 v154, v161, s41, v1
	v_cvt_pk_fp8_f32 v137, v149, v154
	v_pk_fma_f32 v[166:167], v[62:63], v[166:167], v[14:15]
	v_med3_f32 v148, v155, s41, v1
	v_pk_fma_f32 v[166:167], v[50:51], v[162:163], v[166:167]
	v_cvt_pk_fp8_f32 v136, v68, v148 op_sel:[0,0,1]
	v_med3_f32 v68, v132, s41, v1
	v_med3_f32 v132, v133, s41, v1
	v_pk_fma_f32 v[166:167], v[34:35], v[164:165], v[166:167]
	v_cvt_pk_fp8_f32 v137, v68, v132 op_sel:[0,0,1]
	s_waitcnt vmcnt(34)
	v_cvt_pk_f32_fp8_e32 v[160:161], v108
	v_cvt_pk_f32_fp8_sdwa v[148:149], v108 src0_sel:WORD_1
	v_exp_f32_e32 v68, v166
	v_exp_f32_e32 v169, v167
	v_cvt_pk_f32_fp8_sdwa v[154:155], v112 src0_sel:WORD_1
	v_add_f32_e32 v68, 1.0, v68
	v_rcp_f32_e32 v168, v68
	v_add_f32_e32 v68, 1.0, v169
	v_rcp_f32_e32 v169, v68
	v_pk_fma_f32 v[152:153], v[64:65], v[152:153], v[16:17]
	v_pk_fma_f32 v[156:157], v[58:59], v[156:157], v[10:11]
	v_pk_fma_f32 v[152:153], v[52:53], v[150:151], v[152:153]
	v_pk_mul_f32 v[166:167], v[166:167], v[168:169]
	v_pk_fma_f32 v[152:153], v[36:37], v[154:155], v[152:153]
	v_add_co_u32_e32 v132, vcc, s34, v70
	v_exp_f32_e32 v68, v152
	v_exp_f32_e32 v168, v153
	v_pk_fma_f32 v[156:157], v[42:43], v[158:159], v[156:157]
	v_addc_co_u32_e32 v133, vcc, 0, v71, vcc
	v_pk_fma_f32 v[156:157], v[26:27], v[160:161], v[156:157]
	global_store_dwordx2 v[132:133], v[136:137], off offset:1536
	v_cvt_pk_f32_fp8_e32 v[136:137], v113
	v_add_f32_e32 v68, 1.0, v68
	v_pk_mul_f32 v[156:157], v[156:157], v[166:167]
	v_rcp_f32_e32 v166, v68
	v_add_f32_e32 v68, 1.0, v168
	v_rcp_f32_e32 v167, v68
	v_pk_fma_f32 v[140:141], v[54:55], v[140:141], v[6:7]
	v_pk_fma_f32 v[144:145], v[60:61], v[144:145], v[12:13]
	v_pk_fma_f32 v[140:141], v[38:39], v[142:143], v[140:141]
	v_pk_mul_f32 v[152:153], v[152:153], v[166:167]
	v_pk_fma_f32 v[140:141], v[22:23], v[136:137], v[140:141]
	v_pk_fma_f32 v[144:145], v[44:45], v[146:147], v[144:145]
	v_exp_f32_e32 v68, v140
	v_exp_f32_e32 v166, v141
	v_pk_fma_f32 v[144:145], v[28:29], v[148:149], v[144:145]
	v_cvt_pk_f32_fp8_sdwa v[112:113], v113 src0_sel:WORD_1
	v_add_f32_e32 v68, 1.0, v68
	v_pk_mul_f32 v[144:145], v[144:145], v[152:153]
	v_rcp_f32_e32 v152, v68
	v_add_f32_e32 v68, 1.0, v166
	v_rcp_f32_e32 v153, v68
	v_pk_fma_f32 v[128:129], v[56:57], v[128:129], v[8:9]
	v_cvt_pk_f32_fp8_e32 v[132:133], v109
	v_pk_fma_f32 v[128:129], v[40:41], v[120:121], v[128:129]
	v_pk_mul_f32 v[140:141], v[140:141], v[152:153]
	v_pk_fma_f32 v[128:129], v[24:25], v[112:113], v[128:129]
	v_pk_fma_f32 v[134:135], v[46:47], v[134:135], v[2:3]
	v_exp_f32_e32 v68, v128
	v_exp_f32_e32 v152, v129
	v_pk_fma_f32 v[134:135], v[30:31], v[138:139], v[134:135]
	v_add_f32_e32 v68, 1.0, v68
	v_pk_fma_f32 v[134:135], v[18:19], v[132:133], v[134:135]
	v_cvt_pk_f32_fp8_sdwa v[108:109], v109 src0_sel:WORD_1
	v_pk_fma_f32 v[124:125], v[48:49], v[124:125], v[4:5]
	v_pk_mul_f32 v[134:135], v[134:135], v[140:141]
	v_rcp_f32_e32 v140, v68
	v_add_f32_e32 v68, 1.0, v152
	v_rcp_f32_e32 v141, v68
	v_pk_fma_f32 v[124:125], v[32:33], v[116:117], v[124:125]
	v_med3_f32 v68, v156, s41, v1
	v_pk_fma_f32 v[124:125], v[20:21], v[108:109], v[124:125]
	v_pk_mul_f32 v[128:129], v[128:129], v[140:141]
	v_med3_f32 v134, v134, s41, v1
	v_pk_mul_f32 v[124:125], v[124:125], v[128:129]
	v_med3_f32 v129, v157, s41, v1
	v_cvt_pk_fp8_f32 v128, v68, v129
	v_med3_f32 v135, v135, s41, v1
	s_waitcnt vmcnt(34)
; #define CV_LOAD(G_, V_, r0_) do { _Pragma("unroll") for (int i_ = 0; i_ < 8; ++i_) { G_[i_] = *(const GAS v2u*)(ap + (size_t)((r0_) + i_) * F2); V_[i_] = *(const GAS v2u*)(ap + (size_t)((r0_) + i_) * F2 + 128); } } while (0)
; __device__ __forceinline__ void conv_phase(Frame& F) {
;     ...
;         CV_LOAD(GA, VA, 0); CV_LOAD(GB, VB, 8); CV_COMP(GA, VA, 0); CV_LOAD(GA, VA, 16); CV_COMP(GB, VB, 8); CV_LOAD(GB, VB, 24); CV_COMP(GA, VA, 16); CV_COMP(GB, VB, 24);
	v_cvt_pk_f32_fp8_e32 v[156:157], v104
	v_cvt_pk_fp8_f32 v129, v134, v135
	v_pk_fma_f32 v[134:135], v[62:63], v[162:163], v[14:15]
	v_med3_f32 v68, v144, s41, v1
	v_med3_f32 v140, v145, s41, v1
	v_pk_fma_f32 v[134:135], v[50:51], v[164:165], v[134:135]
	v_cvt_pk_fp8_f32 v128, v68, v140 op_sel:[0,0,1]
	v_med3_f32 v68, v124, s41, v1
	v_med3_f32 v124, v125, s41, v1
	v_pk_fma_f32 v[134:135], v[34:35], v[156:157], v[134:135]
	v_cvt_pk_fp8_f32 v129, v68, v124 op_sel:[0,0,1]
	s_waitcnt vmcnt(33)
	v_cvt_pk_f32_fp8_e32 v[152:153], v100
	v_cvt_pk_f32_fp8_sdwa v[140:141], v100 src0_sel:WORD_1
	v_exp_f32_e32 v68, v134
	v_exp_f32_e32 v163, v135
	v_cvt_pk_f32_fp8_sdwa v[144:145], v104 src0_sel:WORD_1
	v_add_f32_e32 v68, 1.0, v68
	v_rcp_f32_e32 v162, v68
	v_add_f32_e32 v68, 1.0, v163
	v_rcp_f32_e32 v163, v68
	v_pk_fma_f32 v[150:151], v[64:65], v[150:151], v[16:17]
	v_pk_fma_f32 v[158:159], v[58:59], v[158:159], v[10:11]
	v_pk_fma_f32 v[150:151], v[52:53], v[154:155], v[150:151]
	v_pk_mul_f32 v[134:135], v[134:135], v[162:163]
	v_pk_fma_f32 v[150:151], v[36:37], v[144:145], v[150:151]
	v_add_co_u32_e32 v124, vcc, s69, v70
	v_exp_f32_e32 v68, v150
	v_exp_f32_e32 v162, v151
	v_pk_fma_f32 v[158:159], v[42:43], v[160:161], v[158:159]
	v_addc_co_u32_e32 v125, vcc, 0, v71, vcc
	v_pk_fma_f32 v[158:159], v[26:27], v[152:153], v[158:159]
	global_store_dwordx2 v[124:125], v[128:129], off offset:256
	v_cvt_pk_f32_fp8_e32 v[128:129], v105
	v_add_f32_e32 v68, 1.0, v68
	v_pk_mul_f32 v[134:135], v[158:159], v[134:135]
	v_rcp_f32_e32 v158, v68
	v_add_f32_e32 v68, 1.0, v162
	v_rcp_f32_e32 v159, v68
	v_pk_fma_f32 v[142:143], v[54:55], v[142:143], v[6:7]
	v_pk_fma_f32 v[146:147], v[60:61], v[146:147], v[12:13]
	v_pk_fma_f32 v[142:143], v[38:39], v[136:137], v[142:143]
	v_pk_mul_f32 v[150:151], v[150:151], v[158:159]
	v_pk_fma_f32 v[142:143], v[22:23], v[128:129], v[142:143]
	v_pk_fma_f32 v[146:147], v[44:45], v[148:149], v[146:147]
	v_exp_f32_e32 v68, v142
	v_exp_f32_e32 v158, v143
	v_pk_fma_f32 v[146:147], v[28:29], v[140:141], v[146:147]
	v_cvt_pk_f32_fp8_sdwa v[104:105], v105 src0_sel:WORD_1
	v_add_f32_e32 v68, 1.0, v68
	v_pk_mul_f32 v[146:147], v[146:147], v[150:151]
	v_rcp_f32_e32 v150, v68
	v_add_f32_e32 v68, 1.0, v158
	v_rcp_f32_e32 v151, v68
	v_pk_fma_f32 v[120:121], v[56:57], v[120:121], v[8:9]
	v_cvt_pk_f32_fp8_e32 v[124:125], v101
	v_pk_fma_f32 v[120:121], v[40:41], v[112:113], v[120:121]
	v_pk_mul_f32 v[142:143], v[142:143], v[150:151]
	v_pk_fma_f32 v[120:121], v[24:25], v[104:105], v[120:121]
	v_pk_fma_f32 v[138:139], v[46:47], v[138:139], v[2:3]
	v_exp_f32_e32 v68, v120
	v_exp_f32_e32 v150, v121
	v_pk_fma_f32 v[138:139], v[30:31], v[132:133], v[138:139]
	v_add_f32_e32 v68, 1.0, v68
	v_pk_fma_f32 v[138:139], v[18:19], v[124:125], v[138:139]
	v_cvt_pk_f32_fp8_sdwa v[100:101], v101 src0_sel:WORD_1
	v_pk_fma_f32 v[116:117], v[48:49], v[116:117], v[4:5]
	v_pk_mul_f32 v[138:139], v[138:139], v[142:143]
	v_rcp_f32_e32 v142, v68
	v_add_f32_e32 v68, 1.0, v150
	v_rcp_f32_e32 v143, v68
	v_pk_fma_f32 v[116:117], v[32:33], v[108:109], v[116:117]
	v_med3_f32 v68, v134, s41, v1
	v_pk_fma_f32 v[116:117], v[20:21], v[100:101], v[116:117]
	v_pk_mul_f32 v[120:121], v[120:121], v[142:143]
	v_med3_f32 v134, v147, s41, v1
	v_pk_mul_f32 v[116:117], v[116:117], v[120:121]
	v_med3_f32 v121, v135, s41, v1
	v_cvt_pk_fp8_f32 v120, v68, v121
	v_med3_f32 v135, v138, s41, v1
	v_med3_f32 v138, v139, s41, v1
	v_cvt_pk_fp8_f32 v121, v135, v138
	v_med3_f32 v68, v146, s41, v1
	v_cvt_pk_fp8_f32 v120, v68, v134 op_sel:[0,0,1]
	v_med3_f32 v68, v116, s41, v1
	v_med3_f32 v116, v117, s41, v1
	v_cvt_pk_fp8_f32 v121, v68, v116 op_sel:[0,0,1]
	v_add_co_u32_e32 v116, vcc, s35, v70
	s_waitcnt vmcnt(33)
	v_cvt_pk_f32_fp8_e32 v[158:159], v96
	v_addc_co_u32_e32 v117, vcc, 0, v71, vcc
	global_store_dwordx2 v[116:117], v[120:121], off offset:3072
	v_pk_fma_f32 v[116:117], v[62:63], v[164:165], v[14:15]
	s_waitcnt vmcnt(33)
	v_cvt_pk_f32_fp8_e32 v[150:151], v92
	v_pk_fma_f32 v[116:117], v[50:51], v[156:157], v[116:117]
	v_cvt_pk_f32_fp8_sdwa v[138:139], v92 src0_sel:WORD_1
	v_pk_fma_f32 v[146:147], v[34:35], v[158:159], v[116:117]
	v_cvt_pk_f32_fp8_sdwa v[142:143], v96 src0_sel:WORD_1
	v_exp_f32_e32 v68, v146
	v_exp_f32_e32 v162, v147
	v_cvt_pk_f32_fp8_e32 v[120:121], v93
	v_add_f32_e32 v68, 1.0, v68
	v_rcp_f32_e32 v92, v68
	v_add_f32_e32 v68, 1.0, v162
	v_cvt_pk_f32_fp8_sdwa v[116:117], v93 src0_sel:WORD_1
	v_rcp_f32_e32 v93, v68
	v_pk_fma_f32 v[154:155], v[64:65], v[154:155], v[16:17]
	v_pk_fma_f32 v[160:161], v[58:59], v[160:161], v[10:11]
	v_pk_fma_f32 v[154:155], v[52:53], v[144:145], v[154:155]
	v_pk_fma_f32 v[160:161], v[42:43], v[152:153], v[160:161]
	v_pk_fma_f32 v[154:155], v[36:37], v[142:143], v[154:155]
	v_pk_fma_f32 v[160:161], v[26:27], v[150:151], v[160:161]
	v_pk_mul_f32 v[92:93], v[146:147], v[92:93]
	v_pk_mul_f32 v[92:93], v[160:161], v[92:93]
	v_exp_f32_e32 v68, v154
	v_exp_f32_e32 v160, v155
	v_cvt_pk_f32_fp8_e32 v[134:135], v97
	v_add_f32_e32 v68, 1.0, v68
	v_rcp_f32_e32 v146, v68
	v_add_f32_e32 v68, 1.0, v160
	v_rcp_f32_e32 v147, v68
	v_pk_fma_f32 v[136:137], v[54:55], v[136:137], v[6:7]
	v_pk_fma_f32 v[148:149], v[60:61], v[148:149], v[12:13]
	v_pk_fma_f32 v[136:137], v[38:39], v[128:129], v[136:137]
	v_pk_mul_f32 v[146:147], v[154:155], v[146:147]
	v_pk_fma_f32 v[136:137], v[22:23], v[134:135], v[136:137]
	v_pk_fma_f32 v[148:149], v[44:45], v[140:141], v[148:149]
	v_exp_f32_e32 v68, v136
	v_exp_f32_e32 v154, v137
	v_pk_fma_f32 v[148:149], v[28:29], v[138:139], v[148:149]
	v_cvt_pk_f32_fp8_sdwa v[96:97], v97 src0_sel:WORD_1
	v_add_f32_e32 v68, 1.0, v68
	v_pk_mul_f32 v[146:147], v[148:149], v[146:147]
; #define CV_LOAD(G_, V_, r0_) do { _Pragma("unroll") for (int i_ = 0; i_ < 8; ++i_) { G_[i_] = *(const GAS v2u*)(ap + (size_t)((r0_) + i_) * F2); V_[i_] = *(const GAS v2u*)(ap + (size_t)((r0_) + i_) * F2 + 128); } } while (0)
; __device__ __forceinline__ void conv_phase(Frame& F) {
;     ...
;         CV_LOAD(GA, VA, 0); CV_LOAD(GB, VB, 8); CV_COMP(GA, VA, 0); CV_LOAD(GA, VA, 16); CV_COMP(GB, VB, 8); CV_LOAD(GB, VB, 24); CV_COMP(GA, VA, 16); CV_COMP(GB, VB, 24);
	v_rcp_f32_e32 v148, v68
	v_add_f32_e32 v68, 1.0, v154
	v_rcp_f32_e32 v149, v68
	v_pk_fma_f32 v[112:113], v[56:57], v[112:113], v[8:9]
	v_pk_fma_f32 v[132:133], v[46:47], v[132:133], v[2:3]
	v_pk_fma_f32 v[112:113], v[40:41], v[104:105], v[112:113]
	v_pk_mul_f32 v[136:137], v[136:137], v[148:149]
	v_pk_fma_f32 v[112:113], v[24:25], v[96:97], v[112:113]
	v_pk_fma_f32 v[132:133], v[30:31], v[124:125], v[132:133]
	v_exp_f32_e32 v68, v112
	v_exp_f32_e32 v148, v113
	v_pk_fma_f32 v[132:133], v[18:19], v[120:121], v[132:133]
	v_add_f32_e32 v68, 1.0, v68
	v_pk_fma_f32 v[108:109], v[48:49], v[108:109], v[4:5]
	v_pk_mul_f32 v[132:133], v[132:133], v[136:137]
	v_rcp_f32_e32 v136, v68
	v_add_f32_e32 v68, 1.0, v148
	v_rcp_f32_e32 v137, v68
	v_pk_fma_f32 v[108:109], v[32:33], v[100:101], v[108:109]
	v_med3_f32 v68, v92, s41, v1
	v_pk_fma_f32 v[108:109], v[20:21], v[116:117], v[108:109]
	v_pk_mul_f32 v[112:113], v[112:113], v[136:137]
	v_med3_f32 v93, v93, s41, v1
	v_pk_mul_f32 v[108:109], v[108:109], v[112:113]
	v_cvt_pk_fp8_f32 v92, v68, v93
	v_med3_f32 v113, v132, s41, v1
	v_med3_f32 v132, v133, s41, v1
	v_cvt_pk_fp8_f32 v93, v113, v132
	v_med3_f32 v68, v146, s41, v1
	v_med3_f32 v112, v147, s41, v1
	v_cvt_pk_fp8_f32 v92, v68, v112 op_sel:[0,0,1]
	v_med3_f32 v68, v108, s41, v1
	v_med3_f32 v108, v109, s41, v1
	v_cvt_pk_fp8_f32 v93, v68, v108 op_sel:[0,0,1]
	v_add_co_u32_e32 v108, vcc, s70, v70
	s_waitcnt vmcnt(32)
	v_cvt_pk_f32_fp8_e32 v[148:149], v88
	v_addc_co_u32_e32 v109, vcc, 0, v71, vcc
	global_store_dwordx2 v[108:109], v[92:93], off offset:1792
	v_pk_fma_f32 v[92:93], v[62:63], v[156:157], v[14:15]
	s_waitcnt vmcnt(32)
	v_cvt_pk_f32_fp8_e32 v[146:147], v84
	v_pk_fma_f32 v[92:93], v[50:51], v[158:159], v[92:93]
	v_cvt_pk_f32_fp8_sdwa v[132:133], v84 src0_sel:WORD_1
	v_pk_fma_f32 v[92:93], v[34:35], v[148:149], v[92:93]
	v_cvt_pk_f32_fp8_sdwa v[136:137], v88 src0_sel:WORD_1
	v_exp_f32_e32 v68, v92
	v_exp_f32_e32 v155, v93
	v_pk_fma_f32 v[144:145], v[64:65], v[144:145], v[16:17]
	v_add_f32_e32 v68, 1.0, v68
	v_rcp_f32_e32 v154, v68
	v_add_f32_e32 v68, 1.0, v155
	v_rcp_f32_e32 v155, v68
	v_pk_fma_f32 v[144:145], v[52:53], v[142:143], v[144:145]
	v_pk_fma_f32 v[152:153], v[58:59], v[152:153], v[10:11]
	v_pk_fma_f32 v[144:145], v[36:37], v[136:137], v[144:145]
	v_pk_mul_f32 v[92:93], v[92:93], v[154:155]
	v_exp_f32_e32 v68, v144
	v_exp_f32_e32 v154, v145
	v_pk_fma_f32 v[152:153], v[42:43], v[150:151], v[152:153]
	v_cvt_pk_f32_fp8_e32 v[112:113], v89
	v_pk_fma_f32 v[152:153], v[26:27], v[146:147], v[152:153]
	v_add_f32_e32 v68, 1.0, v68
	v_pk_fma_f32 v[128:129], v[54:55], v[128:129], v[6:7]
	v_pk_mul_f32 v[92:93], v[152:153], v[92:93]
	v_rcp_f32_e32 v152, v68
	v_add_f32_e32 v68, 1.0, v154
	v_rcp_f32_e32 v153, v68
	v_pk_fma_f32 v[128:129], v[38:39], v[134:135], v[128:129]
	v_pk_fma_f32 v[140:141], v[60:61], v[140:141], v[12:13]
	v_pk_fma_f32 v[128:129], v[22:23], v[112:113], v[128:129]
	v_pk_mul_f32 v[144:145], v[144:145], v[152:153]
	v_exp_f32_e32 v68, v128
	v_exp_f32_e32 v152, v129
	v_pk_fma_f32 v[140:141], v[44:45], v[138:139], v[140:141]
	v_cvt_pk_f32_fp8_sdwa v[88:89], v89 src0_sel:WORD_1
	v_pk_fma_f32 v[140:141], v[28:29], v[132:133], v[140:141]
	v_add_f32_e32 v68, 1.0, v68
	v_pk_fma_f32 v[104:105], v[56:57], v[104:105], v[8:9]
	v_pk_mul_f32 v[140:141], v[140:141], v[144:145]
	v_rcp_f32_e32 v144, v68
	v_add_f32_e32 v68, 1.0, v152
	v_rcp_f32_e32 v145, v68
	v_pk_fma_f32 v[104:105], v[40:41], v[96:97], v[104:105]
	v_cvt_pk_f32_fp8_e32 v[108:109], v85
	v_pk_fma_f32 v[104:105], v[24:25], v[88:89], v[104:105]
	v_pk_mul_f32 v[128:129], v[128:129], v[144:145]
	v_exp_f32_e32 v68, v104
	v_pk_fma_f32 v[124:125], v[46:47], v[124:125], v[2:3]
	v_exp_f32_e32 v144, v105
	v_pk_fma_f32 v[124:125], v[30:31], v[120:121], v[124:125]
	v_add_f32_e32 v68, 1.0, v68
	v_pk_fma_f32 v[124:125], v[18:19], v[108:109], v[124:125]
	v_cvt_pk_f32_fp8_sdwa v[84:85], v85 src0_sel:WORD_1
	v_pk_fma_f32 v[100:101], v[48:49], v[100:101], v[4:5]
	v_pk_mul_f32 v[124:125], v[124:125], v[128:129]
	v_rcp_f32_e32 v128, v68
	v_add_f32_e32 v68, 1.0, v144
	v_rcp_f32_e32 v129, v68
	v_pk_fma_f32 v[100:101], v[32:33], v[116:117], v[100:101]
	v_med3_f32 v68, v92, s41, v1
	v_pk_fma_f32 v[100:101], v[20:21], v[84:85], v[100:101]
	v_pk_mul_f32 v[104:105], v[104:105], v[128:129]
	v_med3_f32 v93, v93, s41, v1
	v_pk_mul_f32 v[100:101], v[100:101], v[104:105]
	v_cvt_pk_fp8_f32 v92, v68, v93
	v_med3_f32 v105, v124, s41, v1
	v_med3_f32 v124, v125, s41, v1
	v_cvt_pk_fp8_f32 v93, v105, v124
	v_med3_f32 v68, v140, s41, v1
	v_med3_f32 v104, v141, s41, v1
	v_cvt_pk_fp8_f32 v92, v68, v104 op_sel:[0,0,1]
	v_med3_f32 v68, v100, s41, v1
	v_med3_f32 v100, v101, s41, v1
	v_cvt_pk_fp8_f32 v93, v68, v100 op_sel:[0,0,1]
	v_add_co_u32_e32 v100, vcc, s36, v70
	s_waitcnt vmcnt(31)
	v_cvt_pk_f32_fp8_e32 v[152:153], v80
	v_addc_co_u32_e32 v101, vcc, 0, v71, vcc
	global_store_dwordx2 v[100:101], v[92:93], off offset:512
	v_pk_fma_f32 v[92:93], v[62:63], v[158:159], v[14:15]
	s_waitcnt vmcnt(31)
; #define CV_LOAD(G_, V_, r0_) do { _Pragma("unroll") for (int i_ = 0; i_ < 8; ++i_) { G_[i_] = *(const GAS v2u*)(ap + (size_t)((r0_) + i_) * F2); V_[i_] = *(const GAS v2u*)(ap + (size_t)((r0_) + i_) * F2 + 128); } } while (0)
; __device__ __forceinline__ void conv_phase(Frame& F) {
;     ...
;         CV_LOAD(GA, VA, 0); CV_LOAD(GB, VB, 8); CV_COMP(GA, VA, 0); CV_LOAD(GA, VA, 16); CV_COMP(GB, VB, 8); CV_LOAD(GB, VB, 24); CV_COMP(GA, VA, 16); CV_COMP(GB, VB, 24);
	v_cvt_pk_f32_fp8_e32 v[144:145], v76
	v_pk_fma_f32 v[92:93], v[50:51], v[148:149], v[92:93]
	v_cvt_pk_f32_fp8_sdwa v[128:129], v76 src0_sel:WORD_1
	v_pk_fma_f32 v[104:105], v[34:35], v[152:153], v[92:93]
	v_cvt_pk_f32_fp8_sdwa v[140:141], v80 src0_sel:WORD_1
	v_exp_f32_e32 v68, v104
	v_exp_f32_e32 v154, v105
	v_cvt_pk_f32_fp8_e32 v[100:101], v77
	v_add_f32_e32 v68, 1.0, v68
	v_rcp_f32_e32 v76, v68
	v_add_f32_e32 v68, 1.0, v154
	v_cvt_pk_f32_fp8_sdwa v[92:93], v77 src0_sel:WORD_1
	v_rcp_f32_e32 v77, v68
	v_pk_fma_f32 v[142:143], v[64:65], v[142:143], v[16:17]
	v_pk_fma_f32 v[150:151], v[58:59], v[150:151], v[10:11]
	v_pk_fma_f32 v[142:143], v[52:53], v[136:137], v[142:143]
	v_pk_fma_f32 v[150:151], v[42:43], v[146:147], v[150:151]
	v_pk_fma_f32 v[142:143], v[36:37], v[140:141], v[142:143]
	v_pk_fma_f32 v[150:151], v[26:27], v[144:145], v[150:151]
	v_pk_mul_f32 v[76:77], v[104:105], v[76:77]
	v_pk_mul_f32 v[76:77], v[150:151], v[76:77]
	v_exp_f32_e32 v68, v142
	v_exp_f32_e32 v150, v143
	v_cvt_pk_f32_fp8_e32 v[124:125], v81
	v_add_f32_e32 v68, 1.0, v68
	v_rcp_f32_e32 v104, v68
	v_add_f32_e32 v68, 1.0, v150
	v_rcp_f32_e32 v105, v68
	v_pk_fma_f32 v[134:135], v[54:55], v[134:135], v[6:7]
	v_pk_fma_f32 v[138:139], v[60:61], v[138:139], v[12:13]
	v_pk_fma_f32 v[134:135], v[38:39], v[112:113], v[134:135]
	v_pk_mul_f32 v[104:105], v[142:143], v[104:105]
	v_pk_fma_f32 v[134:135], v[22:23], v[124:125], v[134:135]
	v_pk_fma_f32 v[138:139], v[44:45], v[132:133], v[138:139]
	v_exp_f32_e32 v68, v134
	v_exp_f32_e32 v142, v135
	v_pk_fma_f32 v[138:139], v[28:29], v[128:129], v[138:139]
	v_cvt_pk_f32_fp8_sdwa v[80:81], v81 src0_sel:WORD_1
	v_add_f32_e32 v68, 1.0, v68
	v_pk_mul_f32 v[104:105], v[138:139], v[104:105]
	v_rcp_f32_e32 v138, v68
	v_add_f32_e32 v68, 1.0, v142
	v_rcp_f32_e32 v139, v68
	v_pk_fma_f32 v[96:97], v[56:57], v[96:97], v[8:9]
	v_pk_fma_f32 v[120:121], v[46:47], v[120:121], v[2:3]
	v_pk_fma_f32 v[96:97], v[40:41], v[88:89], v[96:97]
	v_pk_mul_f32 v[134:135], v[134:135], v[138:139]
	v_pk_fma_f32 v[96:97], v[24:25], v[80:81], v[96:97]
	v_pk_fma_f32 v[120:121], v[30:31], v[108:109], v[120:121]
	v_exp_f32_e32 v68, v96
	v_exp_f32_e32 v138, v97
	v_pk_fma_f32 v[120:121], v[18:19], v[100:101], v[120:121]
	v_add_f32_e32 v68, 1.0, v68
	v_pk_fma_f32 v[116:117], v[48:49], v[116:117], v[4:5]
	v_pk_mul_f32 v[120:121], v[120:121], v[134:135]
	v_rcp_f32_e32 v134, v68
	v_add_f32_e32 v68, 1.0, v138
	v_rcp_f32_e32 v135, v68
	v_pk_fma_f32 v[116:117], v[32:33], v[84:85], v[116:117]
	v_med3_f32 v68, v76, s41, v1
	v_pk_fma_f32 v[116:117], v[20:21], v[92:93], v[116:117]
	v_pk_mul_f32 v[96:97], v[96:97], v[134:135]
	v_med3_f32 v77, v77, s41, v1
	v_pk_mul_f32 v[96:97], v[116:117], v[96:97]
	v_cvt_pk_fp8_f32 v76, v68, v77
	v_med3_f32 v68, v104, s41, v1
	v_med3_f32 v104, v105, s41, v1
	v_med3_f32 v105, v120, s41, v1
	v_med3_f32 v116, v121, s41, v1
	v_cvt_pk_fp8_f32 v77, v105, v116
	v_cvt_pk_fp8_f32 v76, v68, v104 op_sel:[0,0,1]
	v_med3_f32 v68, v96, s41, v1
	v_med3_f32 v96, v97, s41, v1
	v_cvt_pk_fp8_f32 v77, v68, v96 op_sel:[0,0,1]
	v_add_co_u32_e32 v96, vcc, s71, v70
	s_waitcnt vmcnt(22)
	v_cvt_pk_f32_fp8_e32 v[138:139], v130
	v_addc_co_u32_e32 v97, vcc, 0, v71, vcc
	global_store_dwordx2 v[96:97], v[76:77], off offset:3328
	v_pk_fma_f32 v[96:97], v[62:63], v[148:149], v[14:15]
	v_cvt_pk_f32_fp8_sdwa v[134:135], v130 src0_sel:WORD_1
	v_pk_fma_f32 v[96:97], v[50:51], v[152:153], v[96:97]
	v_cvt_pk_f32_fp8_e32 v[116:117], v131
	v_pk_fma_f32 v[142:143], v[34:35], v[138:139], v[96:97]
	v_cvt_pk_f32_fp8_sdwa v[76:77], v131 src0_sel:WORD_1
	v_exp_f32_e32 v68, v142
	v_exp_f32_e32 v148, v143
	s_waitcnt vmcnt(22)
	v_cvt_pk_f32_fp8_e32 v[130:131], v126
	v_add_f32_e32 v68, 1.0, v68
	v_cvt_pk_f32_fp8_sdwa v[120:121], v126 src0_sel:WORD_1
	v_rcp_f32_e32 v126, v68
	v_add_f32_e32 v68, 1.0, v148
	v_cvt_pk_f32_fp8_e32 v[104:105], v127
	v_cvt_pk_f32_fp8_sdwa v[96:97], v127 src0_sel:WORD_1
	v_rcp_f32_e32 v127, v68
	v_pk_fma_f32 v[136:137], v[64:65], v[136:137], v[16:17]
	v_pk_fma_f32 v[146:147], v[58:59], v[146:147], v[10:11]
	v_pk_fma_f32 v[136:137], v[52:53], v[140:141], v[136:137]
	v_pk_fma_f32 v[146:147], v[42:43], v[144:145], v[146:147]
	v_pk_fma_f32 v[136:137], v[36:37], v[134:135], v[136:137]
	v_pk_fma_f32 v[146:147], v[26:27], v[130:131], v[146:147]
	v_pk_mul_f32 v[126:127], v[142:143], v[126:127]
	v_pk_mul_f32 v[126:127], v[146:147], v[126:127]
	v_exp_f32_e32 v68, v136
	v_exp_f32_e32 v146, v137
	v_add_f32_e32 v68, 1.0, v68
	v_rcp_f32_e32 v142, v68
	v_add_f32_e32 v68, 1.0, v146
	v_rcp_f32_e32 v143, v68
	v_pk_fma_f32 v[112:113], v[54:55], v[112:113], v[6:7]
	v_pk_fma_f32 v[132:133], v[60:61], v[132:133], v[12:13]
	v_pk_fma_f32 v[112:113], v[38:39], v[124:125], v[112:113]
	v_pk_mul_f32 v[136:137], v[136:137], v[142:143]
	v_pk_fma_f32 v[112:113], v[22:23], v[116:117], v[112:113]
	v_pk_fma_f32 v[132:133], v[44:45], v[128:129], v[132:133]
	v_exp_f32_e32 v68, v112
	v_exp_f32_e32 v142, v113
	v_pk_fma_f32 v[132:133], v[28:29], v[120:121], v[132:133]
	v_add_f32_e32 v68, 1.0, v68
	v_pk_fma_f32 v[88:89], v[56:57], v[88:89], v[8:9]
	v_pk_mul_f32 v[132:133], v[132:133], v[136:137]
	v_rcp_f32_e32 v136, v68
	v_add_f32_e32 v68, 1.0, v142
	v_rcp_f32_e32 v137, v68
	v_pk_fma_f32 v[88:89], v[40:41], v[80:81], v[88:89]
	v_pk_fma_f32 v[108:109], v[46:47], v[108:109], v[2:3]
	v_pk_fma_f32 v[88:89], v[24:25], v[76:77], v[88:89]
	v_pk_mul_f32 v[112:113], v[112:113], v[136:137]
	v_exp_f32_e32 v68, v88
	v_exp_f32_e32 v136, v89
	v_pk_fma_f32 v[108:109], v[30:31], v[100:101], v[108:109]
	v_add_f32_e32 v68, 1.0, v68
	v_pk_fma_f32 v[108:109], v[18:19], v[104:105], v[108:109]
	v_pk_fma_f32 v[84:85], v[48:49], v[84:85], v[4:5]
	v_pk_fma_f32 v[84:85], v[32:33], v[92:93], v[84:85]
	v_pk_mul_f32 v[108:109], v[108:109], v[112:113]
	v_rcp_f32_e32 v112, v68
	v_add_f32_e32 v68, 1.0, v136
	v_rcp_f32_e32 v113, v68
	v_pk_fma_f32 v[84:85], v[20:21], v[96:97], v[84:85]
	v_med3_f32 v68, v126, s41, v1
	v_pk_mul_f32 v[88:89], v[88:89], v[112:113]
	v_med3_f32 v108, v108, s41, v1
	v_pk_mul_f32 v[84:85], v[84:85], v[88:89]
	v_med3_f32 v89, v127, s41, v1
	v_cvt_pk_fp8_f32 v88, v68, v89
	v_med3_f32 v109, v109, s41, v1
	v_cvt_pk_fp8_f32 v89, v108, v109
	v_med3_f32 v68, v132, s41, v1
	v_med3_f32 v112, v133, s41, v1
	v_cvt_pk_fp8_f32 v88, v68, v112 op_sel:[0,0,1]
	v_med3_f32 v68, v84, s41, v1
	v_med3_f32 v84, v85, s41, v1
	v_cvt_pk_fp8_f32 v89, v68, v84 op_sel:[0,0,1]
	v_add_co_u32_e32 v84, vcc, s37, v70
	s_waitcnt vmcnt(21)
; #define CV_LOAD(G_, V_, r0_) do { _Pragma("unroll") for (int i_ = 0; i_ < 8; ++i_) { G_[i_] = *(const GAS v2u*)(ap + (size_t)((r0_) + i_) * F2); V_[i_] = *(const GAS v2u*)(ap + (size_t)((r0_) + i_) * F2 + 128); } } while (0)
; __device__ __forceinline__ void conv_phase(Frame& F) {
;     ...
;         CV_LOAD(GA, VA, 0); CV_LOAD(GB, VB, 8); CV_COMP(GA, VA, 0); CV_LOAD(GA, VA, 16); CV_COMP(GB, VB, 8); CV_LOAD(GB, VB, 24); CV_COMP(GA, VA, 16); CV_COMP(GB, VB, 24);
	v_cvt_pk_f32_fp8_e32 v[136:137], v122
	v_addc_co_u32_e32 v85, vcc, 0, v71, vcc
	global_store_dwordx2 v[84:85], v[88:89], off offset:2048
	v_pk_fma_f32 v[88:89], v[62:63], v[152:153], v[14:15]
	v_cvt_pk_f32_fp8_sdwa v[126:127], v122 src0_sel:WORD_1
	v_pk_fma_f32 v[88:89], v[50:51], v[138:139], v[88:89]
	v_cvt_pk_f32_fp8_e32 v[112:113], v123
	v_pk_fma_f32 v[142:143], v[34:35], v[136:137], v[88:89]
	v_cvt_pk_f32_fp8_sdwa v[84:85], v123 src0_sel:WORD_1
	v_exp_f32_e32 v68, v142
	v_exp_f32_e32 v146, v143
	s_waitcnt vmcnt(21)
	v_cvt_pk_f32_fp8_e32 v[132:133], v118
	v_add_f32_e32 v68, 1.0, v68
	v_cvt_pk_f32_fp8_sdwa v[122:123], v118 src0_sel:WORD_1
	v_rcp_f32_e32 v118, v68
	v_add_f32_e32 v68, 1.0, v146
	v_cvt_pk_f32_fp8_e32 v[108:109], v119
	v_cvt_pk_f32_fp8_sdwa v[88:89], v119 src0_sel:WORD_1
	v_rcp_f32_e32 v119, v68
	v_pk_fma_f32 v[140:141], v[64:65], v[140:141], v[16:17]
	v_pk_fma_f32 v[144:145], v[58:59], v[144:145], v[10:11]
	v_pk_fma_f32 v[140:141], v[52:53], v[134:135], v[140:141]
	v_pk_fma_f32 v[144:145], v[42:43], v[130:131], v[144:145]
	v_pk_fma_f32 v[140:141], v[36:37], v[126:127], v[140:141]
	v_pk_fma_f32 v[144:145], v[26:27], v[132:133], v[144:145]
	v_pk_mul_f32 v[118:119], v[142:143], v[118:119]
	v_pk_mul_f32 v[118:119], v[144:145], v[118:119]
	v_exp_f32_e32 v68, v140
	v_exp_f32_e32 v144, v141
	v_add_f32_e32 v68, 1.0, v68
	v_rcp_f32_e32 v142, v68
	v_add_f32_e32 v68, 1.0, v144
	v_rcp_f32_e32 v143, v68
	v_pk_fma_f32 v[124:125], v[54:55], v[124:125], v[6:7]
	v_pk_fma_f32 v[128:129], v[60:61], v[128:129], v[12:13]
	v_pk_fma_f32 v[124:125], v[38:39], v[116:117], v[124:125]
	v_pk_mul_f32 v[140:141], v[140:141], v[142:143]
	v_pk_fma_f32 v[124:125], v[22:23], v[112:113], v[124:125]
	v_pk_fma_f32 v[128:129], v[44:45], v[120:121], v[128:129]
	v_exp_f32_e32 v68, v124
	v_exp_f32_e32 v142, v125
	v_pk_fma_f32 v[128:129], v[28:29], v[122:123], v[128:129]
	v_add_f32_e32 v68, 1.0, v68
	v_pk_fma_f32 v[80:81], v[56:57], v[80:81], v[8:9]
	v_pk_mul_f32 v[128:129], v[128:129], v[140:141]
	v_rcp_f32_e32 v140, v68
	v_add_f32_e32 v68, 1.0, v142
	v_rcp_f32_e32 v141, v68
	v_pk_fma_f32 v[80:81], v[40:41], v[76:77], v[80:81]
	v_pk_fma_f32 v[100:101], v[46:47], v[100:101], v[2:3]
	v_pk_fma_f32 v[80:81], v[24:25], v[84:85], v[80:81]
	v_pk_mul_f32 v[124:125], v[124:125], v[140:141]
	v_exp_f32_e32 v68, v80
	v_exp_f32_e32 v140, v81
	v_pk_fma_f32 v[100:101], v[30:31], v[104:105], v[100:101]
	v_add_f32_e32 v68, 1.0, v68
	v_pk_fma_f32 v[100:101], v[18:19], v[108:109], v[100:101]
	v_pk_fma_f32 v[92:93], v[48:49], v[92:93], v[4:5]
	v_pk_fma_f32 v[92:93], v[32:33], v[96:97], v[92:93]
	v_pk_mul_f32 v[100:101], v[100:101], v[124:125]
	v_rcp_f32_e32 v124, v68
	v_add_f32_e32 v68, 1.0, v140
	v_rcp_f32_e32 v125, v68
	v_pk_fma_f32 v[92:93], v[20:21], v[88:89], v[92:93]
	v_med3_f32 v68, v118, s41, v1
	v_pk_mul_f32 v[80:81], v[80:81], v[124:125]
	v_med3_f32 v100, v100, s41, v1
	v_pk_mul_f32 v[80:81], v[92:93], v[80:81]
	v_med3_f32 v93, v119, s41, v1
	v_cvt_pk_fp8_f32 v92, v68, v93
	v_med3_f32 v101, v101, s41, v1
	v_cvt_pk_fp8_f32 v93, v100, v101
	v_med3_f32 v68, v128, s41, v1
	v_med3_f32 v118, v129, s41, v1
	v_cvt_pk_fp8_f32 v92, v68, v118 op_sel:[0,0,1]
	v_med3_f32 v68, v80, s41, v1
	v_med3_f32 v80, v81, s41, v1
	v_cvt_pk_fp8_f32 v93, v68, v80 op_sel:[0,0,1]
	v_add_co_u32_e32 v80, vcc, s72, v70
	s_waitcnt vmcnt(20)
	v_cvt_pk_f32_fp8_e32 v[140:141], v114
	v_addc_co_u32_e32 v81, vcc, 0, v71, vcc
	global_store_dwordx2 v[80:81], v[92:93], off offset:768
	v_pk_fma_f32 v[92:93], v[62:63], v[138:139], v[14:15]
	v_cvt_pk_f32_fp8_sdwa v[124:125], v114 src0_sel:WORD_1
	v_pk_fma_f32 v[92:93], v[50:51], v[136:137], v[92:93]
	v_cvt_pk_f32_fp8_e32 v[118:119], v115
	v_pk_fma_f32 v[138:139], v[34:35], v[140:141], v[92:93]
	v_cvt_pk_f32_fp8_sdwa v[80:81], v115 src0_sel:WORD_1
	v_exp_f32_e32 v68, v138
	v_exp_f32_e32 v142, v139
	s_waitcnt vmcnt(20)
	v_cvt_pk_f32_fp8_e32 v[128:129], v110
	v_add_f32_e32 v68, 1.0, v68
	v_cvt_pk_f32_fp8_sdwa v[114:115], v110 src0_sel:WORD_1
	v_rcp_f32_e32 v110, v68
	v_add_f32_e32 v68, 1.0, v142
	v_cvt_pk_f32_fp8_e32 v[100:101], v111
	v_cvt_pk_f32_fp8_sdwa v[92:93], v111 src0_sel:WORD_1
	v_rcp_f32_e32 v111, v68
	v_pk_fma_f32 v[134:135], v[64:65], v[134:135], v[16:17]
	v_pk_fma_f32 v[130:131], v[58:59], v[130:131], v[10:11]
	v_pk_fma_f32 v[134:135], v[52:53], v[126:127], v[134:135]
	v_pk_mul_f32 v[110:111], v[138:139], v[110:111]
	v_pk_fma_f32 v[134:135], v[36:37], v[124:125], v[134:135]
	v_pk_fma_f32 v[130:131], v[42:43], v[132:133], v[130:131]
	v_exp_f32_e32 v68, v134
	v_exp_f32_e32 v138, v135
	v_pk_fma_f32 v[130:131], v[26:27], v[128:129], v[130:131]
	v_add_f32_e32 v68, 1.0, v68
	v_pk_fma_f32 v[116:117], v[54:55], v[116:117], v[6:7]
	v_pk_mul_f32 v[110:111], v[130:131], v[110:111]
	v_rcp_f32_e32 v130, v68
	v_add_f32_e32 v68, 1.0, v138
	v_rcp_f32_e32 v131, v68
	v_pk_fma_f32 v[116:117], v[38:39], v[112:113], v[116:117]
	v_pk_fma_f32 v[120:121], v[60:61], v[120:121], v[12:13]
	v_pk_fma_f32 v[116:117], v[22:23], v[118:119], v[116:117]
	v_pk_mul_f32 v[130:131], v[134:135], v[130:131]
	v_exp_f32_e32 v68, v116
	v_exp_f32_e32 v134, v117
	v_pk_fma_f32 v[120:121], v[44:45], v[122:123], v[120:121]
	v_add_f32_e32 v68, 1.0, v68
	v_pk_fma_f32 v[120:121], v[28:29], v[114:115], v[120:121]
	v_pk_fma_f32 v[76:77], v[56:57], v[76:77], v[8:9]
	v_pk_fma_f32 v[76:77], v[40:41], v[84:85], v[76:77]
	v_pk_mul_f32 v[120:121], v[120:121], v[130:131]
	v_rcp_f32_e32 v130, v68
	v_add_f32_e32 v68, 1.0, v134
	v_rcp_f32_e32 v131, v68
	v_pk_fma_f32 v[76:77], v[24:25], v[80:81], v[76:77]
	v_pk_fma_f32 v[104:105], v[46:47], v[104:105], v[2:3]
	v_pk_mul_f32 v[116:117], v[116:117], v[130:131]
	v_exp_f32_e32 v68, v76
	v_exp_f32_e32 v130, v77
	v_pk_fma_f32 v[104:105], v[30:31], v[108:109], v[104:105]
	v_add_f32_e32 v68, 1.0, v68
	v_pk_fma_f32 v[104:105], v[18:19], v[100:101], v[104:105]
	v_pk_fma_f32 v[96:97], v[48:49], v[96:97], v[4:5]
	v_pk_fma_f32 v[96:97], v[32:33], v[88:89], v[96:97]
	v_pk_mul_f32 v[104:105], v[104:105], v[116:117]
	v_rcp_f32_e32 v116, v68
	v_add_f32_e32 v68, 1.0, v130
	v_rcp_f32_e32 v117, v68
	v_pk_fma_f32 v[96:97], v[20:21], v[92:93], v[96:97]
	v_med3_f32 v68, v110, s41, v1
	v_pk_mul_f32 v[76:77], v[76:77], v[116:117]
	v_med3_f32 v104, v104, s41, v1
	v_pk_mul_f32 v[76:77], v[96:97], v[76:77]
	v_med3_f32 v97, v111, s41, v1
	v_cvt_pk_fp8_f32 v96, v68, v97
	v_med3_f32 v105, v105, s41, v1
	v_cvt_pk_fp8_f32 v97, v104, v105
	v_med3_f32 v68, v120, s41, v1
	v_med3_f32 v110, v121, s41, v1
	v_cvt_pk_fp8_f32 v96, v68, v110 op_sel:[0,0,1]
	v_med3_f32 v68, v76, s41, v1
	v_med3_f32 v76, v77, s41, v1
	v_cvt_pk_fp8_f32 v97, v68, v76 op_sel:[0,0,1]
	v_add_co_u32_e32 v76, vcc, s38, v70
	s_waitcnt vmcnt(19)
; #define CV_LOAD(G_, V_, r0_) do { _Pragma("unroll") for (int i_ = 0; i_ < 8; ++i_) { G_[i_] = *(const GAS v2u*)(ap + (size_t)((r0_) + i_) * F2); V_[i_] = *(const GAS v2u*)(ap + (size_t)((r0_) + i_) * F2 + 128); } } while (0)
; __device__ __forceinline__ void conv_phase(Frame& F) {
;     ...
;         CV_LOAD(GA, VA, 0); CV_LOAD(GB, VB, 8); CV_COMP(GA, VA, 0); CV_LOAD(GA, VA, 16); CV_COMP(GB, VB, 8); CV_LOAD(GB, VB, 24); CV_COMP(GA, VA, 16); CV_COMP(GB, VB, 24);
	v_cvt_pk_f32_fp8_e32 v[130:131], v106
	v_addc_co_u32_e32 v77, vcc, 0, v71, vcc
	global_store_dwordx2 v[76:77], v[96:97], off offset:3584
	v_pk_fma_f32 v[96:97], v[62:63], v[136:137], v[14:15]
	v_cvt_pk_f32_fp8_sdwa v[116:117], v106 src0_sel:WORD_1
	v_pk_fma_f32 v[96:97], v[50:51], v[140:141], v[96:97]
	v_cvt_pk_f32_fp8_e32 v[110:111], v107
	v_pk_fma_f32 v[134:135], v[34:35], v[130:131], v[96:97]
	v_cvt_pk_f32_fp8_sdwa v[76:77], v107 src0_sel:WORD_1
	v_exp_f32_e32 v68, v134
	v_exp_f32_e32 v136, v135
	s_waitcnt vmcnt(19)
	v_cvt_pk_f32_fp8_e32 v[120:121], v102
	v_add_f32_e32 v68, 1.0, v68
	v_cvt_pk_f32_fp8_sdwa v[106:107], v102 src0_sel:WORD_1
	v_rcp_f32_e32 v102, v68
	v_add_f32_e32 v68, 1.0, v136
	v_cvt_pk_f32_fp8_e32 v[104:105], v103
	v_cvt_pk_f32_fp8_sdwa v[96:97], v103 src0_sel:WORD_1
	v_rcp_f32_e32 v103, v68
	v_pk_fma_f32 v[126:127], v[64:65], v[126:127], v[16:17]
	v_pk_fma_f32 v[132:133], v[58:59], v[132:133], v[10:11]
	v_pk_fma_f32 v[126:127], v[52:53], v[124:125], v[126:127]
	v_pk_mul_f32 v[102:103], v[134:135], v[102:103]
	v_pk_fma_f32 v[126:127], v[36:37], v[116:117], v[126:127]
	v_pk_fma_f32 v[132:133], v[42:43], v[128:129], v[132:133]
	v_exp_f32_e32 v68, v126
	v_exp_f32_e32 v134, v127
	v_pk_fma_f32 v[132:133], v[26:27], v[120:121], v[132:133]
	v_add_f32_e32 v68, 1.0, v68
	v_pk_fma_f32 v[112:113], v[54:55], v[112:113], v[6:7]
	v_pk_mul_f32 v[102:103], v[132:133], v[102:103]
	v_rcp_f32_e32 v132, v68
	v_add_f32_e32 v68, 1.0, v134
	v_rcp_f32_e32 v133, v68
	v_pk_fma_f32 v[112:113], v[38:39], v[118:119], v[112:113]
	v_pk_fma_f32 v[122:123], v[60:61], v[122:123], v[12:13]
	v_pk_fma_f32 v[112:113], v[22:23], v[110:111], v[112:113]
	v_pk_mul_f32 v[126:127], v[126:127], v[132:133]
	v_exp_f32_e32 v68, v112
	v_exp_f32_e32 v132, v113
	v_pk_fma_f32 v[122:123], v[44:45], v[114:115], v[122:123]
	v_add_f32_e32 v68, 1.0, v68
	v_pk_fma_f32 v[122:123], v[28:29], v[106:107], v[122:123]
	v_pk_fma_f32 v[84:85], v[56:57], v[84:85], v[8:9]
	v_pk_fma_f32 v[84:85], v[40:41], v[80:81], v[84:85]
	v_pk_mul_f32 v[122:123], v[122:123], v[126:127]
	v_rcp_f32_e32 v126, v68
	v_add_f32_e32 v68, 1.0, v132
	v_rcp_f32_e32 v127, v68
	v_pk_fma_f32 v[84:85], v[24:25], v[76:77], v[84:85]
	v_pk_fma_f32 v[108:109], v[46:47], v[108:109], v[2:3]
	v_pk_mul_f32 v[112:113], v[112:113], v[126:127]
	v_exp_f32_e32 v68, v84
	v_exp_f32_e32 v126, v85
	v_pk_fma_f32 v[108:109], v[30:31], v[100:101], v[108:109]
	v_add_f32_e32 v68, 1.0, v68
	v_pk_fma_f32 v[108:109], v[18:19], v[104:105], v[108:109]
	v_pk_fma_f32 v[88:89], v[48:49], v[88:89], v[4:5]
	v_pk_fma_f32 v[88:89], v[32:33], v[92:93], v[88:89]
	v_pk_mul_f32 v[108:109], v[108:109], v[112:113]
	v_rcp_f32_e32 v112, v68
	v_add_f32_e32 v68, 1.0, v126
	v_rcp_f32_e32 v113, v68
	v_pk_fma_f32 v[88:89], v[20:21], v[96:97], v[88:89]
	v_med3_f32 v68, v102, s41, v1
	v_pk_mul_f32 v[84:85], v[84:85], v[112:113]
	v_med3_f32 v102, v123, s41, v1
	v_pk_mul_f32 v[84:85], v[88:89], v[84:85]
	v_med3_f32 v89, v103, s41, v1
	v_cvt_pk_fp8_f32 v88, v68, v89
	v_med3_f32 v103, v108, s41, v1
	v_med3_f32 v108, v109, s41, v1
	v_cvt_pk_fp8_f32 v89, v103, v108
	v_med3_f32 v68, v122, s41, v1
	v_cvt_pk_fp8_f32 v88, v68, v102 op_sel:[0,0,1]
	v_med3_f32 v68, v84, s41, v1
	v_med3_f32 v84, v85, s41, v1
	v_cvt_pk_fp8_f32 v89, v68, v84 op_sel:[0,0,1]
	v_add_co_u32_e32 v84, vcc, s73, v70
	s_waitcnt vmcnt(18)
	v_cvt_pk_f32_fp8_e32 v[126:127], v98
	v_addc_co_u32_e32 v85, vcc, 0, v71, vcc
	global_store_dwordx2 v[84:85], v[88:89], off offset:2304
	v_pk_fma_f32 v[88:89], v[62:63], v[140:141], v[14:15]
	v_cvt_pk_f32_fp8_sdwa v[112:113], v98 src0_sel:WORD_1
	v_pk_fma_f32 v[88:89], v[50:51], v[130:131], v[88:89]
	s_waitcnt vmcnt(18)
	v_cvt_pk_f32_fp8_e32 v[122:123], v94
	v_pk_fma_f32 v[132:133], v[34:35], v[126:127], v[88:89]
	v_cvt_pk_f32_fp8_sdwa v[108:109], v94 src0_sel:WORD_1
	v_exp_f32_e32 v68, v132
	v_exp_f32_e32 v134, v133
	v_cvt_pk_f32_fp8_e32 v[102:103], v99
	v_add_f32_e32 v68, 1.0, v68
	v_rcp_f32_e32 v94, v68
	v_add_f32_e32 v68, 1.0, v134
	v_cvt_pk_f32_fp8_sdwa v[84:85], v99 src0_sel:WORD_1
	v_cvt_pk_f32_fp8_e32 v[98:99], v95
	v_cvt_pk_f32_fp8_sdwa v[88:89], v95 src0_sel:WORD_1
	v_rcp_f32_e32 v95, v68
	v_pk_fma_f32 v[124:125], v[64:65], v[124:125], v[16:17]
	v_pk_fma_f32 v[128:129], v[58:59], v[128:129], v[10:11]
	v_pk_fma_f32 v[124:125], v[52:53], v[116:117], v[124:125]
	v_pk_mul_f32 v[94:95], v[132:133], v[94:95]
	v_pk_fma_f32 v[124:125], v[36:37], v[112:113], v[124:125]
	v_pk_fma_f32 v[128:129], v[42:43], v[120:121], v[128:129]
	v_exp_f32_e32 v68, v124
	v_exp_f32_e32 v132, v125
	v_pk_fma_f32 v[128:129], v[26:27], v[122:123], v[128:129]
	v_add_f32_e32 v68, 1.0, v68
	v_pk_fma_f32 v[118:119], v[54:55], v[118:119], v[6:7]
	v_pk_mul_f32 v[94:95], v[128:129], v[94:95]
	v_rcp_f32_e32 v128, v68
	v_add_f32_e32 v68, 1.0, v132
	v_rcp_f32_e32 v129, v68
	v_pk_fma_f32 v[118:119], v[38:39], v[110:111], v[118:119]
	v_pk_fma_f32 v[114:115], v[60:61], v[114:115], v[12:13]
	v_pk_fma_f32 v[118:119], v[22:23], v[102:103], v[118:119]
	v_pk_mul_f32 v[124:125], v[124:125], v[128:129]
	v_exp_f32_e32 v68, v118
	v_exp_f32_e32 v128, v119
	v_pk_fma_f32 v[114:115], v[44:45], v[106:107], v[114:115]
	v_add_f32_e32 v68, 1.0, v68
	v_pk_fma_f32 v[114:115], v[28:29], v[108:109], v[114:115]
	v_pk_fma_f32 v[80:81], v[56:57], v[80:81], v[8:9]
	v_pk_fma_f32 v[80:81], v[40:41], v[76:77], v[80:81]
	v_pk_mul_f32 v[114:115], v[114:115], v[124:125]
	v_rcp_f32_e32 v124, v68
	v_add_f32_e32 v68, 1.0, v128
	v_rcp_f32_e32 v125, v68
	v_pk_fma_f32 v[80:81], v[24:25], v[84:85], v[80:81]
	v_pk_fma_f32 v[100:101], v[46:47], v[100:101], v[2:3]
	v_pk_mul_f32 v[118:119], v[118:119], v[124:125]
	v_exp_f32_e32 v68, v80
	v_exp_f32_e32 v124, v81
	v_pk_fma_f32 v[100:101], v[30:31], v[104:105], v[100:101]
	v_add_f32_e32 v68, 1.0, v68
	v_pk_fma_f32 v[100:101], v[18:19], v[98:99], v[100:101]
	v_pk_fma_f32 v[92:93], v[48:49], v[92:93], v[4:5]
	v_pk_fma_f32 v[92:93], v[32:33], v[96:97], v[92:93]
	v_pk_mul_f32 v[100:101], v[100:101], v[118:119]
	v_rcp_f32_e32 v118, v68
	v_add_f32_e32 v68, 1.0, v124
	v_rcp_f32_e32 v119, v68
	v_pk_fma_f32 v[92:93], v[20:21], v[88:89], v[92:93]
	v_med3_f32 v68, v94, s41, v1
	v_pk_mul_f32 v[80:81], v[80:81], v[118:119]
	s_waitcnt vmcnt(17)
; #define CV_LOAD(G_, V_, r0_) do { _Pragma("unroll") for (int i_ = 0; i_ < 8; ++i_) { G_[i_] = *(const GAS v2u*)(ap + (size_t)((r0_) + i_) * F2); V_[i_] = *(const GAS v2u*)(ap + (size_t)((r0_) + i_) * F2 + 128); } } while (0)
; __device__ __forceinline__ void conv_phase(Frame& F) {
;     ...
;         CV_LOAD(GA, VA, 0); CV_LOAD(GB, VB, 8); CV_COMP(GA, VA, 0); CV_LOAD(GA, VA, 16); CV_COMP(GB, VB, 8); CV_LOAD(GB, VB, 24); CV_COMP(GA, VA, 16); CV_COMP(GB, VB, 24);
	v_cvt_pk_f32_fp8_e32 v[118:119], v90
	v_pk_mul_f32 v[80:81], v[92:93], v[80:81]
	v_med3_f32 v93, v95, s41, v1
	v_cvt_pk_fp8_f32 v92, v68, v93
	v_med3_f32 v95, v100, s41, v1
	v_med3_f32 v100, v101, s41, v1
	v_cvt_pk_fp8_f32 v93, v95, v100
	v_pk_fma_f32 v[124:125], v[62:63], v[130:131], v[14:15]
	v_med3_f32 v68, v114, s41, v1
	v_med3_f32 v94, v115, s41, v1
	v_pk_fma_f32 v[124:125], v[50:51], v[126:127], v[124:125]
	v_cvt_pk_fp8_f32 v92, v68, v94 op_sel:[0,0,1]
	v_med3_f32 v68, v80, s41, v1
	v_med3_f32 v80, v81, s41, v1
	v_pk_fma_f32 v[124:125], v[34:35], v[118:119], v[124:125]
	v_cvt_pk_fp8_f32 v93, v68, v80 op_sel:[0,0,1]
	s_waitcnt vmcnt(16)
	v_cvt_pk_f32_fp8_e32 v[114:115], v86
	v_cvt_pk_f32_fp8_sdwa v[94:95], v86 src0_sel:WORD_1
	v_exp_f32_e32 v68, v124
	v_exp_f32_e32 v129, v125
	v_cvt_pk_f32_fp8_sdwa v[100:101], v90 src0_sel:WORD_1
	v_add_f32_e32 v68, 1.0, v68
	v_rcp_f32_e32 v128, v68
	v_add_f32_e32 v68, 1.0, v129
	v_rcp_f32_e32 v129, v68
	v_pk_fma_f32 v[116:117], v[64:65], v[116:117], v[16:17]
	v_pk_fma_f32 v[120:121], v[58:59], v[120:121], v[10:11]
	v_pk_fma_f32 v[116:117], v[52:53], v[112:113], v[116:117]
	v_pk_mul_f32 v[124:125], v[124:125], v[128:129]
	v_pk_fma_f32 v[116:117], v[36:37], v[100:101], v[116:117]
	v_add_co_u32_e32 v80, vcc, s39, v70
	v_exp_f32_e32 v68, v116
	v_exp_f32_e32 v128, v117
	v_pk_fma_f32 v[120:121], v[42:43], v[122:123], v[120:121]
	v_addc_co_u32_e32 v81, vcc, 0, v71, vcc
	v_pk_fma_f32 v[120:121], v[26:27], v[114:115], v[120:121]
	global_store_dwordx2 v[80:81], v[92:93], off offset:1024
	v_cvt_pk_f32_fp8_e32 v[92:93], v91
	v_add_f32_e32 v68, 1.0, v68
	v_pk_mul_f32 v[120:121], v[120:121], v[124:125]
	v_rcp_f32_e32 v124, v68
	v_add_f32_e32 v68, 1.0, v128
	v_rcp_f32_e32 v125, v68
	v_pk_fma_f32 v[110:111], v[54:55], v[110:111], v[6:7]
	v_pk_fma_f32 v[106:107], v[60:61], v[106:107], v[12:13]
	v_pk_fma_f32 v[110:111], v[38:39], v[102:103], v[110:111]
	v_pk_mul_f32 v[116:117], v[116:117], v[124:125]
	v_pk_fma_f32 v[110:111], v[22:23], v[92:93], v[110:111]
	v_pk_fma_f32 v[106:107], v[44:45], v[108:109], v[106:107]
	v_exp_f32_e32 v68, v110
	v_exp_f32_e32 v124, v111
	v_pk_fma_f32 v[106:107], v[28:29], v[94:95], v[106:107]
	v_cvt_pk_f32_fp8_sdwa v[80:81], v91 src0_sel:WORD_1
	v_add_f32_e32 v68, 1.0, v68
	v_pk_mul_f32 v[106:107], v[106:107], v[116:117]
	v_rcp_f32_e32 v116, v68
	v_add_f32_e32 v68, 1.0, v124
	v_rcp_f32_e32 v117, v68
	v_pk_fma_f32 v[76:77], v[56:57], v[76:77], v[8:9]
	v_cvt_pk_f32_fp8_e32 v[90:91], v87
	v_pk_fma_f32 v[76:77], v[40:41], v[84:85], v[76:77]
	v_pk_mul_f32 v[110:111], v[110:111], v[116:117]
	v_pk_fma_f32 v[76:77], v[24:25], v[80:81], v[76:77]
	v_pk_fma_f32 v[104:105], v[46:47], v[104:105], v[2:3]
	v_exp_f32_e32 v68, v76
	v_exp_f32_e32 v116, v77
	v_pk_fma_f32 v[104:105], v[30:31], v[98:99], v[104:105]
	v_add_f32_e32 v68, 1.0, v68
	v_pk_fma_f32 v[104:105], v[18:19], v[90:91], v[104:105]
	v_cvt_pk_f32_fp8_sdwa v[86:87], v87 src0_sel:WORD_1
	v_pk_fma_f32 v[96:97], v[48:49], v[96:97], v[4:5]
	v_pk_mul_f32 v[104:105], v[104:105], v[110:111]
	v_rcp_f32_e32 v110, v68
	v_add_f32_e32 v68, 1.0, v116
	v_rcp_f32_e32 v111, v68
	v_pk_fma_f32 v[96:97], v[32:33], v[88:89], v[96:97]
	v_med3_f32 v68, v120, s41, v1
	v_pk_fma_f32 v[96:97], v[20:21], v[86:87], v[96:97]
	v_pk_mul_f32 v[76:77], v[76:77], v[110:111]
	v_med3_f32 v104, v104, s41, v1
	v_pk_mul_f32 v[76:77], v[96:97], v[76:77]
	v_med3_f32 v97, v121, s41, v1
	v_cvt_pk_fp8_f32 v96, v68, v97
	v_med3_f32 v105, v105, s41, v1
	v_cvt_pk_fp8_f32 v97, v104, v105
	v_med3_f32 v68, v106, s41, v1
	v_med3_f32 v106, v107, s41, v1
	v_cvt_pk_fp8_f32 v96, v68, v106 op_sel:[0,0,1]
	v_med3_f32 v68, v76, s41, v1
	v_med3_f32 v76, v77, s41, v1
	v_cvt_pk_fp8_f32 v97, v68, v76 op_sel:[0,0,1]
	v_add_co_u32_e32 v76, vcc, s74, v70
	v_pk_fma_f32 v[120:121], v[62:63], v[126:127], v[14:15]
	s_nop 0
	v_addc_co_u32_e32 v77, vcc, 0, v71, vcc
	global_store_dwordx2 v[76:77], v[96:97], off offset:3840
	s_waitcnt vmcnt(17)
	v_cvt_pk_f32_fp8_e32 v[76:77], v82
	v_pk_fma_f32 v[120:121], v[50:51], v[118:119], v[120:121]
	s_waitcnt vmcnt(16)
; #define CV_LOAD(G_, V_, r0_) do { _Pragma("unroll") for (int i_ = 0; i_ < 8; ++i_) { G_[i_] = *(const GAS v2u*)(ap + (size_t)((r0_) + i_) * F2); V_[i_] = *(const GAS v2u*)(ap + (size_t)((r0_) + i_) * F2 + 128); } } while (0)
; __device__ __forceinline__ void conv_phase(Frame& F) {
;     ...
;     for (size_t idx = (size_t)F.gw * 64 + F.lane; idx < total; idx += (size_t)F.NGW * 64) {
;     ...
;         CV_LOAD(GA, VA, 0); CV_LOAD(GB, VB, 8); CV_COMP(GA, VA, 0); CV_LOAD(GA, VA, 16); CV_COMP(GB, VB, 8); CV_LOAD(GB, VB, 24); CV_COMP(GA, VA, 16); CV_COMP(GB, VB, 24);
	v_cvt_pk_f32_fp8_e32 v[106:107], v78
	v_cvt_pk_f32_fp8_sdwa v[110:111], v78 src0_sel:WORD_1
	v_pk_fma_f32 v[120:121], v[34:35], v[76:77], v[120:121]
	v_cvt_pk_f32_fp8_sdwa v[96:97], v82 src0_sel:WORD_1
	v_exp_f32_e32 v68, v120
	v_exp_f32_e32 v125, v121
	v_pk_fma_f32 v[112:113], v[64:65], v[112:113], v[16:17]
	v_add_f32_e32 v68, 1.0, v68
	v_rcp_f32_e32 v124, v68
	v_add_f32_e32 v68, 1.0, v125
	v_rcp_f32_e32 v125, v68
	v_pk_fma_f32 v[112:113], v[52:53], v[100:101], v[112:113]
	v_pk_fma_f32 v[122:123], v[58:59], v[122:123], v[10:11]
	v_pk_fma_f32 v[112:113], v[36:37], v[96:97], v[112:113]
	v_pk_mul_f32 v[120:121], v[120:121], v[124:125]
	v_exp_f32_e32 v68, v112
	v_exp_f32_e32 v124, v113
	v_pk_fma_f32 v[122:123], v[42:43], v[114:115], v[122:123]
	v_cvt_pk_f32_fp8_e32 v[104:105], v83
	v_pk_fma_f32 v[122:123], v[26:27], v[106:107], v[122:123]
	v_add_f32_e32 v68, 1.0, v68
	v_pk_fma_f32 v[102:103], v[54:55], v[102:103], v[6:7]
	v_pk_mul_f32 v[120:121], v[122:123], v[120:121]
	v_rcp_f32_e32 v122, v68
	v_add_f32_e32 v68, 1.0, v124
	v_rcp_f32_e32 v123, v68
	v_pk_fma_f32 v[102:103], v[38:39], v[92:93], v[102:103]
	v_pk_fma_f32 v[108:109], v[60:61], v[108:109], v[12:13]
	v_pk_fma_f32 v[102:103], v[22:23], v[104:105], v[102:103]
	v_pk_mul_f32 v[112:113], v[112:113], v[122:123]
	v_exp_f32_e32 v68, v102
	v_exp_f32_e32 v122, v103
	v_pk_fma_f32 v[108:109], v[44:45], v[94:95], v[108:109]
	v_cvt_pk_f32_fp8_sdwa v[82:83], v83 src0_sel:WORD_1
	v_pk_fma_f32 v[108:109], v[28:29], v[110:111], v[108:109]
	v_add_f32_e32 v68, 1.0, v68
	v_pk_fma_f32 v[84:85], v[56:57], v[84:85], v[8:9]
	v_pk_mul_f32 v[108:109], v[108:109], v[112:113]
	v_rcp_f32_e32 v112, v68
	v_add_f32_e32 v68, 1.0, v122
	v_rcp_f32_e32 v113, v68
	v_pk_fma_f32 v[84:85], v[40:41], v[80:81], v[84:85]
	v_cvt_pk_f32_fp8_e32 v[116:117], v79
	v_pk_fma_f32 v[84:85], v[24:25], v[82:83], v[84:85]
	v_pk_mul_f32 v[102:103], v[102:103], v[112:113]
	v_exp_f32_e32 v68, v84
	v_pk_fma_f32 v[98:99], v[46:47], v[98:99], v[2:3]
	v_exp_f32_e32 v112, v85
	v_pk_fma_f32 v[98:99], v[30:31], v[90:91], v[98:99]
	v_add_f32_e32 v68, 1.0, v68
	v_pk_fma_f32 v[98:99], v[18:19], v[116:117], v[98:99]
	v_cvt_pk_f32_fp8_sdwa v[78:79], v79 src0_sel:WORD_1
	v_pk_fma_f32 v[88:89], v[48:49], v[88:89], v[4:5]
	v_pk_mul_f32 v[98:99], v[98:99], v[102:103]
	v_rcp_f32_e32 v102, v68
	v_add_f32_e32 v68, 1.0, v112
	v_rcp_f32_e32 v103, v68
	v_pk_fma_f32 v[88:89], v[32:33], v[86:87], v[88:89]
	v_med3_f32 v68, v120, s41, v1
	v_pk_fma_f32 v[88:89], v[20:21], v[78:79], v[88:89]
	v_pk_mul_f32 v[84:85], v[84:85], v[102:103]
	v_med3_f32 v98, v98, s41, v1
	v_pk_mul_f32 v[84:85], v[88:89], v[84:85]
	v_med3_f32 v89, v121, s41, v1
	v_cvt_pk_fp8_f32 v88, v68, v89
	v_med3_f32 v99, v99, s41, v1
	v_cvt_pk_fp8_f32 v89, v98, v99
	v_med3_f32 v68, v108, s41, v1
	v_med3_f32 v102, v109, s41, v1
	v_cvt_pk_fp8_f32 v88, v68, v102 op_sel:[0,0,1]
	v_med3_f32 v68, v84, s41, v1
	v_med3_f32 v84, v85, s41, v1
	v_cvt_pk_fp8_f32 v89, v68, v84 op_sel:[0,0,1]
	v_add_co_u32_e32 v84, vcc, s40, v70
	v_pk_fma_f32 v[14:15], v[62:63], v[118:119], v[14:15]
	s_nop 0
	v_addc_co_u32_e32 v85, vcc, 0, v71, vcc
	global_store_dwordx2 v[84:85], v[88:89], off offset:2560
	s_waitcnt vmcnt(16)
	v_cvt_pk_f32_fp8_e32 v[84:85], v74
	v_pk_fma_f32 v[14:15], v[50:51], v[76:77], v[14:15]
	v_cvt_pk_f32_fp8_sdwa v[88:89], v74 src0_sel:WORD_1
	s_waitcnt vmcnt(15)
	v_cvt_pk_f32_fp8_e32 v[102:103], v72
	v_pk_fma_f32 v[14:15], v[34:35], v[84:85], v[14:15]
	v_pk_fma_f32 v[16:17], v[64:65], v[100:101], v[16:17]
	v_exp_f32_e32 v50, v14
	v_exp_f32_e32 v51, v15
	v_pk_fma_f32 v[10:11], v[58:59], v[114:115], v[10:11]
	v_pk_fma_f32 v[16:17], v[52:53], v[96:97], v[16:17]
	v_add_f32_e32 v50, 1.0, v50
	v_add_f32_e32 v51, 1.0, v51
	v_pk_fma_f32 v[10:11], v[42:43], v[106:107], v[10:11]
	v_pk_fma_f32 v[16:17], v[36:37], v[88:89], v[16:17]
	v_rcp_f32_e32 v50, v50
	v_rcp_f32_e32 v51, v51
	v_pk_fma_f32 v[10:11], v[26:27], v[102:103], v[10:11]
	v_exp_f32_e32 v26, v16
	v_exp_f32_e32 v27, v17
	v_pk_mul_f32 v[14:15], v[14:15], v[50:51]
	v_cvt_pk_f32_fp8_e32 v[98:99], v75
	v_pk_mul_f32 v[10:11], v[10:11], v[14:15]
	v_add_f32_e32 v14, 1.0, v26
	v_add_f32_e32 v15, 1.0, v27
	v_rcp_f32_e32 v14, v14
	v_rcp_f32_e32 v15, v15
	v_pk_fma_f32 v[6:7], v[54:55], v[92:93], v[6:7]
	v_cvt_pk_f32_fp8_sdwa v[108:109], v72 src0_sel:WORD_1
	v_pk_fma_f32 v[6:7], v[38:39], v[104:105], v[6:7]
	v_pk_mul_f32 v[14:15], v[16:17], v[14:15]
	v_pk_fma_f32 v[6:7], v[22:23], v[98:99], v[6:7]
	v_pk_fma_f32 v[12:13], v[60:61], v[94:95], v[12:13]
	v_exp_f32_e32 v16, v6
	v_exp_f32_e32 v17, v7
	v_pk_fma_f32 v[12:13], v[44:45], v[110:111], v[12:13]
	v_cvt_pk_f32_fp8_sdwa v[74:75], v75 src0_sel:WORD_1
	v_pk_fma_f32 v[12:13], v[28:29], v[108:109], v[12:13]
	v_pk_fma_f32 v[8:9], v[56:57], v[80:81], v[8:9]
	v_pk_fma_f32 v[8:9], v[40:41], v[82:83], v[8:9]
	v_pk_mul_f32 v[12:13], v[12:13], v[14:15]
	v_add_f32_e32 v14, 1.0, v16
	v_add_f32_e32 v15, 1.0, v17
	v_rcp_f32_e32 v14, v14
	v_rcp_f32_e32 v15, v15
	v_cvt_pk_f32_fp8_e32 v[112:113], v73
	v_pk_fma_f32 v[8:9], v[24:25], v[74:75], v[8:9]
	v_pk_fma_f32 v[2:3], v[46:47], v[90:91], v[2:3]
	v_pk_mul_f32 v[6:7], v[6:7], v[14:15]
	v_exp_f32_e32 v14, v8
	v_exp_f32_e32 v15, v9
	v_pk_fma_f32 v[2:3], v[30:31], v[116:117], v[2:3]
	v_cvt_pk_f32_fp8_sdwa v[34:35], v73 src0_sel:WORD_1
	v_pk_fma_f32 v[2:3], v[18:19], v[112:113], v[2:3]
	v_pk_fma_f32 v[4:5], v[48:49], v[86:87], v[4:5]
	v_pk_fma_f32 v[4:5], v[32:33], v[78:79], v[4:5]
	v_pk_mul_f32 v[2:3], v[2:3], v[6:7]
	v_add_f32_e32 v6, 1.0, v14
	v_add_f32_e32 v7, 1.0, v15
	v_rcp_f32_e32 v6, v6
	v_rcp_f32_e32 v7, v7
	v_pk_fma_f32 v[4:5], v[20:21], v[34:35], v[4:5]
	v_med3_f32 v2, v2, s41, v1
	v_pk_mul_f32 v[6:7], v[8:9], v[6:7]
	v_med3_f32 v8, v11, s41, v1
	v_pk_mul_f32 v[4:5], v[4:5], v[6:7]
	v_med3_f32 v7, v10, s41, v1
	v_cvt_pk_fp8_f32 v6, v7, v8
	v_med3_f32 v3, v3, s41, v1
	v_cvt_pk_fp8_f32 v7, v2, v3
	v_med3_f32 v8, v12, s41, v1
	v_med3_f32 v9, v13, s41, v1
	v_med3_f32 v2, v4, s41, v1
	v_med3_f32 v3, v5, s41, v1
	v_cvt_pk_fp8_f32 v6, v8, v9 op_sel:[0,0,1]
	v_cvt_pk_fp8_f32 v7, v2, v3 op_sel:[0,0,1]
	v_add_co_u32_e32 v2, vcc, 0x53000, v70
	v_lshl_add_u64 v[66:67], v[66:67], 0, s[18:19]
	s_nop 0
	v_addc_co_u32_e32 v3, vcc, 0, v71, vcc
	global_store_dwordx2 v[2:3], v[6:7], off offset:1280
	s_mov_b64 s[22:23], 0x55fff
	v_cmp_lt_u64_e32 vcc, s[22:23], v[66:67]
	s_or_b64 s[16:17], vcc, s[16:17]
	s_andn2_b64 exec, exec, s[16:17]
	s_cbranch_execz .LBB0_2571
